# adds nt hint on read-once dwordx4 loads (weight conversion, norm1 L0 x rows, prep, post)
# speedup vs baseline: 1.0282x; 1.0234x over previous
.LBB0_11:
	v_lshl_add_u64 v[26:27], v[4:5], 0, s[6:7]
	v_add_co_u32_e32 v72, vcc, s9, v26
	ds_read2_b32 v[24:25], v28 offset1:2
	ds_read2_b32 v[22:23], v28 offset0:4 offset1:6
	ds_read2_b32 v[20:21], v28 offset0:8 offset1:10
	v_addc_co_u32_e32 v73, vcc, 0, v27, vcc
	v_add_co_u32_e32 v74, vcc, s10, v26
	global_load_dwordx4 v[30:33], v[26:27], off nt
	s_nop 0
	v_addc_co_u32_e32 v75, vcc, 0, v27, vcc
	v_add_co_u32_e32 v76, vcc, s11, v26
	v_add_u32_e32 v29, 0x2000, v28
	s_nop 0
	v_addc_co_u32_e32 v77, vcc, 0, v27, vcc
	v_add_co_u32_e32 v78, vcc, s18, v26
	v_add_u32_e32 v36, 0x4000, v28
	s_nop 0
	v_addc_co_u32_e32 v79, vcc, 0, v27, vcc
	v_add_co_u32_e32 v80, vcc, s19, v26
	v_add_u32_e32 v37, 0x6000, v28
	s_nop 0
	v_addc_co_u32_e32 v81, vcc, 0, v27, vcc
	v_add_co_u32_e32 v82, vcc, s20, v26
	ds_read2_b32 v[64:65], v28 offset0:12 offset1:14
	s_nop 0
	v_addc_co_u32_e32 v83, vcc, 0, v27, vcc
	v_add_co_u32_e32 v26, vcc, s21, v26
	ds_read2_b32 v[66:67], v29 offset1:2
	ds_read2_b32 v[68:69], v36 offset1:2
	ds_read2_b32 v[70:71], v37 offset1:2
	v_addc_co_u32_e32 v27, vcc, 0, v27, vcc
	ds_read2_b32 v[84:85], v29 offset0:4 offset1:6
	ds_read2_b32 v[86:87], v36 offset0:4 offset1:6
	ds_read2_b32 v[88:89], v37 offset0:4 offset1:6
	ds_read2_b32 v[90:91], v29 offset0:8 offset1:10
	ds_read2_b32 v[92:93], v36 offset0:8 offset1:10
	ds_read2_b32 v[94:95], v37 offset0:8 offset1:10
	ds_read2_b32 v[96:97], v29 offset0:12 offset1:14
	ds_read2_b32 v[98:99], v36 offset0:12 offset1:14
	ds_read2_b32 v[100:101], v37 offset0:12 offset1:14
	global_load_dwordx4 v[36:39], v[72:73], off nt
	global_load_dwordx4 v[40:43], v[74:75], off nt
	global_load_dwordx4 v[44:47], v[76:77], off nt
	global_load_dwordx4 v[48:51], v[78:79], off nt
	global_load_dwordx4 v[52:55], v[80:81], off nt
	global_load_dwordx4 v[56:59], v[82:83], off nt
	global_load_dwordx4 v[60:63], v[26:27], off nt
	s_waitcnt lgkmcnt(14)
	v_mov_b32_e32 v26, v25
	s_waitcnt lgkmcnt(11)
	v_mov_b32_e32 v78, v67
	s_waitcnt lgkmcnt(10)
	v_mov_b32_e32 v80, v69
	s_waitcnt lgkmcnt(9)
	v_mov_b32_e32 v82, v71
	v_mov_b32_e32 v72, v23
	s_waitcnt lgkmcnt(8)
	v_mov_b32_e32 v102, v85
	s_waitcnt lgkmcnt(7)
	v_mov_b32_e32 v104, v87
	s_waitcnt lgkmcnt(6)
	v_mov_b32_e32 v106, v89
	v_mov_b32_e32 v74, v21
	s_waitcnt lgkmcnt(5)
	v_mov_b32_e32 v108, v91
	s_waitcnt lgkmcnt(4)
	v_mov_b32_e32 v110, v93
	s_waitcnt lgkmcnt(3)
	v_mov_b32_e32 v112, v95
	s_add_u32 s6, s6, 0xc0000
	s_addc_u32 s7, s7, 0
	v_mov_b32_e32 v76, v65
	s_waitcnt lgkmcnt(2)
	v_mov_b32_e32 v114, v97
	s_waitcnt lgkmcnt(1)
	v_mov_b32_e32 v116, v99
	s_waitcnt lgkmcnt(0)
	v_mov_b32_e32 v118, v101
	v_add_u32_e32 v28, 64, v28
	s_cmp_eq_u32 s6, 0xc00000
	s_waitcnt vmcnt(7)
	v_pk_fma_f32 v[2:3], v[30:31], v[24:25], v[2:3] op_sel_hi:[1,0,1]
	v_pk_fma_f32 v[6:7], v[32:33], v[24:25], v[6:7] op_sel_hi:[1,0,1]
	v_pk_fma_f32 v[8:9], v[30:31], v[66:67], v[8:9] op_sel_hi:[1,0,1]
	v_pk_fma_f32 v[10:11], v[32:33], v[66:67], v[10:11] op_sel_hi:[1,0,1]
	v_pk_fma_f32 v[12:13], v[30:31], v[68:69], v[12:13] op_sel_hi:[1,0,1]
	v_pk_fma_f32 v[14:15], v[32:33], v[68:69], v[14:15] op_sel_hi:[1,0,1]
	v_pk_fma_f32 v[16:17], v[30:31], v[70:71], v[16:17] op_sel_hi:[1,0,1]
	v_pk_fma_f32 v[18:19], v[32:33], v[70:71], v[18:19] op_sel_hi:[1,0,1]
	s_waitcnt vmcnt(6)
	v_pk_fma_f32 v[2:3], v[36:37], v[26:27], v[2:3] op_sel_hi:[1,0,1]
	v_pk_fma_f32 v[6:7], v[38:39], v[26:27], v[6:7] op_sel_hi:[1,0,1]
	v_pk_fma_f32 v[8:9], v[36:37], v[78:79], v[8:9] op_sel_hi:[1,0,1]
	v_pk_fma_f32 v[10:11], v[38:39], v[78:79], v[10:11] op_sel_hi:[1,0,1]
	v_pk_fma_f32 v[12:13], v[36:37], v[80:81], v[12:13] op_sel_hi:[1,0,1]
	v_pk_fma_f32 v[14:15], v[38:39], v[80:81], v[14:15] op_sel_hi:[1,0,1]
	v_pk_fma_f32 v[16:17], v[36:37], v[82:83], v[16:17] op_sel_hi:[1,0,1]
	v_pk_fma_f32 v[18:19], v[38:39], v[82:83], v[18:19] op_sel_hi:[1,0,1]
	s_waitcnt vmcnt(5)
	v_pk_fma_f32 v[6:7], v[42:43], v[22:23], v[6:7] op_sel_hi:[1,0,1]
	v_pk_fma_f32 v[2:3], v[40:41], v[22:23], v[2:3] op_sel_hi:[1,0,1]
	v_pk_fma_f32 v[10:11], v[42:43], v[84:85], v[10:11] op_sel_hi:[1,0,1]
	v_pk_fma_f32 v[8:9], v[40:41], v[84:85], v[8:9] op_sel_hi:[1,0,1]
	v_pk_fma_f32 v[14:15], v[42:43], v[86:87], v[14:15] op_sel_hi:[1,0,1]
	v_pk_fma_f32 v[12:13], v[40:41], v[86:87], v[12:13] op_sel_hi:[1,0,1]
	v_pk_fma_f32 v[18:19], v[42:43], v[88:89], v[18:19] op_sel_hi:[1,0,1]
	v_pk_fma_f32 v[16:17], v[40:41], v[88:89], v[16:17] op_sel_hi:[1,0,1]
	s_waitcnt vmcnt(4)
	v_pk_fma_f32 v[6:7], v[46:47], v[72:73], v[6:7] op_sel_hi:[1,0,1]
	v_pk_fma_f32 v[2:3], v[44:45], v[72:73], v[2:3] op_sel_hi:[1,0,1]
	v_pk_fma_f32 v[10:11], v[46:47], v[102:103], v[10:11] op_sel_hi:[1,0,1]
	v_pk_fma_f32 v[8:9], v[44:45], v[102:103], v[8:9] op_sel_hi:[1,0,1]
	v_pk_fma_f32 v[14:15], v[46:47], v[104:105], v[14:15] op_sel_hi:[1,0,1]
	v_pk_fma_f32 v[12:13], v[44:45], v[104:105], v[12:13] op_sel_hi:[1,0,1]
	v_pk_fma_f32 v[18:19], v[46:47], v[106:107], v[18:19] op_sel_hi:[1,0,1]
	v_pk_fma_f32 v[16:17], v[44:45], v[106:107], v[16:17] op_sel_hi:[1,0,1]
	s_waitcnt vmcnt(3)
	v_pk_fma_f32 v[6:7], v[50:51], v[20:21], v[6:7] op_sel_hi:[1,0,1]
	v_pk_fma_f32 v[2:3], v[48:49], v[20:21], v[2:3] op_sel_hi:[1,0,1]
	v_pk_fma_f32 v[10:11], v[50:51], v[90:91], v[10:11] op_sel_hi:[1,0,1]
	v_pk_fma_f32 v[8:9], v[48:49], v[90:91], v[8:9] op_sel_hi:[1,0,1]
	v_pk_fma_f32 v[14:15], v[50:51], v[92:93], v[14:15] op_sel_hi:[1,0,1]
	v_pk_fma_f32 v[12:13], v[48:49], v[92:93], v[12:13] op_sel_hi:[1,0,1]
	v_pk_fma_f32 v[18:19], v[50:51], v[94:95], v[18:19] op_sel_hi:[1,0,1]
	v_pk_fma_f32 v[16:17], v[48:49], v[94:95], v[16:17] op_sel_hi:[1,0,1]
	s_waitcnt vmcnt(2)
	v_pk_fma_f32 v[6:7], v[54:55], v[74:75], v[6:7] op_sel_hi:[1,0,1]
	v_pk_fma_f32 v[2:3], v[52:53], v[74:75], v[2:3] op_sel_hi:[1,0,1]
	v_pk_fma_f32 v[10:11], v[54:55], v[108:109], v[10:11] op_sel_hi:[1,0,1]
	v_pk_fma_f32 v[8:9], v[52:53], v[108:109], v[8:9] op_sel_hi:[1,0,1]
	v_pk_fma_f32 v[14:15], v[54:55], v[110:111], v[14:15] op_sel_hi:[1,0,1]
	v_pk_fma_f32 v[12:13], v[52:53], v[110:111], v[12:13] op_sel_hi:[1,0,1]
	v_pk_fma_f32 v[18:19], v[54:55], v[112:113], v[18:19] op_sel_hi:[1,0,1]
	v_pk_fma_f32 v[16:17], v[52:53], v[112:113], v[16:17] op_sel_hi:[1,0,1]
	s_waitcnt vmcnt(1)
	v_pk_fma_f32 v[6:7], v[58:59], v[64:65], v[6:7] op_sel_hi:[1,0,1]
	v_pk_fma_f32 v[2:3], v[56:57], v[64:65], v[2:3] op_sel_hi:[1,0,1]
	v_pk_fma_f32 v[10:11], v[58:59], v[96:97], v[10:11] op_sel_hi:[1,0,1]
	v_pk_fma_f32 v[8:9], v[56:57], v[96:97], v[8:9] op_sel_hi:[1,0,1]
	v_pk_fma_f32 v[14:15], v[58:59], v[98:99], v[14:15] op_sel_hi:[1,0,1]
	v_pk_fma_f32 v[12:13], v[56:57], v[98:99], v[12:13] op_sel_hi:[1,0,1]
	v_pk_fma_f32 v[18:19], v[58:59], v[100:101], v[18:19] op_sel_hi:[1,0,1]
	v_pk_fma_f32 v[16:17], v[56:57], v[100:101], v[16:17] op_sel_hi:[1,0,1]
	s_waitcnt vmcnt(0)
	v_pk_fma_f32 v[6:7], v[62:63], v[76:77], v[6:7] op_sel_hi:[1,0,1]
	v_pk_fma_f32 v[2:3], v[60:61], v[76:77], v[2:3] op_sel_hi:[1,0,1]
	v_pk_fma_f32 v[10:11], v[62:63], v[114:115], v[10:11] op_sel_hi:[1,0,1]
	v_pk_fma_f32 v[8:9], v[60:61], v[114:115], v[8:9] op_sel_hi:[1,0,1]
	v_pk_fma_f32 v[14:15], v[62:63], v[116:117], v[14:15] op_sel_hi:[1,0,1]
	v_pk_fma_f32 v[12:13], v[60:61], v[116:117], v[12:13] op_sel_hi:[1,0,1]
	v_pk_fma_f32 v[18:19], v[62:63], v[118:119], v[18:19] op_sel_hi:[1,0,1]
	v_pk_fma_f32 v[16:17], v[60:61], v[118:119], v[16:17] op_sel_hi:[1,0,1]
	s_cbranch_scc0 .LBB0_11
	v_mbcnt_lo_u32_b32 v4, -1, 0
	v_mbcnt_hi_u32_b32 v4, -1, v4
	v_and_b32_e32 v20, 64, v4
	v_xor_b32_e32 v5, 32, v4
	v_add_u32_e32 v20, 64, v20
	v_cmp_lt_i32_e32 vcc, v5, v20
	s_nop 1
	v_cndmask_b32_e32 v4, v4, v5, vcc
	v_lshlrev_b32_e32 v33, 2, v4
	ds_bpermute_b32 v4, v33, v2
	ds_bpermute_b32 v20, v33, v8
	ds_bpermute_b32 v24, v33, v12
	ds_bpermute_b32 v28, v33, v16
	ds_bpermute_b32 v5, v33, v3
	ds_bpermute_b32 v21, v33, v9
	ds_bpermute_b32 v25, v33, v13
	ds_bpermute_b32 v29, v33, v17
	ds_bpermute_b32 v22, v33, v6
	ds_bpermute_b32 v26, v33, v10
	ds_bpermute_b32 v30, v33, v14
	ds_bpermute_b32 v32, v33, v18
	ds_bpermute_b32 v23, v33, v7
	ds_bpermute_b32 v27, v33, v11
	ds_bpermute_b32 v31, v33, v15
	ds_bpermute_b32 v33, v33, v19
	v_cmp_gt_u32_e32 vcc, 32, v34
	s_and_saveexec_b64 s[6:7], vcc
	s_cbranch_execz .LBB0_14
	s_lshl_b32 s9, s36, 11
	s_add_i32 s9, s9, 0
	s_waitcnt lgkmcnt(3)
	v_pk_add_f32 v[6:7], v[6:7], v[22:23]
	v_pk_add_f32 v[4:5], v[2:3], v[4:5]
	v_lshl_add_u32 v1, v1, 2, s9
	s_waitcnt lgkmcnt(0)
	v_pk_add_f32 v[18:19], v[18:19], v[32:33]
	v_pk_add_f32 v[16:17], v[16:17], v[28:29]
	v_pk_add_f32 v[14:15], v[14:15], v[30:31]
	v_pk_add_f32 v[12:13], v[12:13], v[24:25]
	v_pk_add_f32 v[10:11], v[10:11], v[26:27]
	v_pk_add_f32 v[8:9], v[8:9], v[20:21]
	ds_write_b128 v1, v[4:7] offset:32768
	ds_write_b128 v1, v[8:11] offset:33280
	ds_write_b128 v1, v[12:15] offset:33792
	ds_write_b128 v1, v[16:19] offset:34304

.LBB0_30:
	s_mul_hi_i32 s4, s67, 0x7a44c6b
	s_lshr_b32 s6, s4, 31
	s_ashr_i32 s4, s4, 7
	s_add_i32 s6, s4, s6
	s_mul_i32 s4, s6, 0xffffef40
	s_add_i32 s10, s67, s4
	s_ashr_i32 s7, s6, 31
	s_cmpk_gt_i32 s10, 0xcbf
	s_mov_b64 s[8:9], -1
	s_cbranch_scc0 .LBB0_32
	s_load_dwordx2 s[8:9], s[14:15], 0x38
	s_lshl_b64 s[18:19], s[6:7], 22
	s_lshl_b64 s[68:69], s[6:7], 24
	s_mul_i32 s4, s6, 0xffffde80
	v_mov_b32_e32 v5, v1
	s_waitcnt lgkmcnt(0)
	s_add_u32 s8, s8, s68
	s_addc_u32 s9, s9, s69
	s_add_u32 s11, s20, s18
	s_addc_u32 s18, s21, s19
	s_add_i32 s4, s26, s4
	s_and_b32 s19, s4, 0x780
	v_or_b32_e32 v4, s19, v24
	s_and_b32 s7, s24, 0x7e0
	v_lshlrev_b32_e32 v4, 13, v4
	v_lshl_add_u64 v[4:5], s[8:9], 0, v[4:5]
	s_lshl_b32 s4, s7, 2
	v_lshl_add_u64 v[4:5], v[4:5], 0, s[4:5]
	v_lshl_add_u64 v[88:89], v[4:5], 0, v[0:1]
	v_add_co_u32_e32 v8, vcc, s28, v88
	s_add_u32 s8, s11, s19
	s_nop 0
	v_addc_co_u32_e32 v9, vcc, 0, v89, vcc
	v_add_co_u32_e32 v12, vcc, s29, v88
	global_load_dwordx4 v[4:7], v[88:89], off nt
	s_nop 0
	global_load_dwordx4 v[8:11], v[8:9], off nt
	v_addc_co_u32_e32 v13, vcc, 0, v89, vcc
	v_add_co_u32_e32 v16, vcc, s30, v88
	s_addc_u32 s9, s18, 0
	s_nop 0
	v_addc_co_u32_e32 v17, vcc, 0, v89, vcc
	v_add_co_u32_e32 v20, vcc, s31, v88
	global_load_dwordx4 v[12:15], v[12:13], off nt
	s_nop 0
	global_load_dwordx4 v[16:19], v[16:17], off nt
	v_addc_co_u32_e32 v21, vcc, 0, v89, vcc
	v_add_co_u32_e32 v52, vcc, s37, v88
	s_nop 1
	v_addc_co_u32_e32 v53, vcc, 0, v89, vcc
	v_add_co_u32_e32 v56, vcc, s38, v88
	global_load_dwordx4 v[20:23], v[20:21], off nt
	s_nop 0
	global_load_dwordx4 v[52:55], v[52:53], off nt
	v_addc_co_u32_e32 v57, vcc, 0, v89, vcc
	v_add_co_u32_e32 v60, vcc, s39, v88
	s_nop 1
	v_addc_co_u32_e32 v61, vcc, 0, v89, vcc
	v_add_co_u32_e32 v64, vcc, s40, v88
	global_load_dwordx4 v[56:59], v[56:57], off nt
	s_nop 0
	global_load_dwordx4 v[60:63], v[60:61], off nt
	v_addc_co_u32_e32 v65, vcc, 0, v89, vcc
	v_add_co_u32_e32 v68, vcc, s41, v88
	s_nop 1
	v_addc_co_u32_e32 v69, vcc, 0, v89, vcc
	v_add_co_u32_e32 v72, vcc, s42, v88
	global_load_dwordx4 v[64:67], v[64:65], off nt
	s_nop 0
	global_load_dwordx4 v[68:71], v[68:69], off nt
	v_addc_co_u32_e32 v73, vcc, 0, v89, vcc
	v_add_co_u32_e32 v76, vcc, s43, v88
	s_nop 1
	v_addc_co_u32_e32 v77, vcc, 0, v89, vcc
	v_add_co_u32_e32 v80, vcc, s44, v88
	global_load_dwordx4 v[72:75], v[72:73], off nt
	s_nop 0
	global_load_dwordx4 v[76:79], v[76:77], off nt
	v_addc_co_u32_e32 v81, vcc, 0, v89, vcc
	v_add_co_u32_e32 v84, vcc, s45, v88
	s_nop 1
	v_addc_co_u32_e32 v85, vcc, 0, v89, vcc
	v_add_co_u32_e32 v90, vcc, s46, v88
	global_load_dwordx4 v[80:83], v[80:81], off nt
	s_nop 0
	global_load_dwordx4 v[84:87], v[84:85], off nt
	v_addc_co_u32_e32 v91, vcc, 0, v89, vcc
	v_add_co_u32_e32 v92, vcc, s47, v88
	s_nop 1
	v_addc_co_u32_e32 v93, vcc, 0, v89, vcc
	global_load_dwordx4 v[88:91], v[90:91], off nt
	s_nop 0
	global_load_dwordx4 v[92:95], v[92:93], off nt
	s_waitcnt vmcnt(15)
	ds_write_b128 v45, v[4:7]
	s_waitcnt vmcnt(14)
	ds_write_b128 v45, v[8:11] offset:1024
	s_waitcnt vmcnt(13)
	ds_write_b128 v38, v[12:15] offset:2048
	s_waitcnt vmcnt(12)
	ds_write_b128 v38, v[16:19] offset:3072
	s_waitcnt vmcnt(11)
	ds_write_b128 v39, v[20:23] offset:4096
	s_waitcnt vmcnt(10)
	ds_write_b128 v39, v[52:55] offset:5120
	s_waitcnt vmcnt(9)
	ds_write_b128 v40, v[56:59] offset:6144
	s_waitcnt vmcnt(8)
	ds_write_b128 v40, v[60:63] offset:7168
	s_waitcnt vmcnt(7)
	ds_write_b128 v41, v[64:67] offset:8192
	s_waitcnt vmcnt(6)
	ds_write_b128 v41, v[68:71] offset:9216
	s_waitcnt vmcnt(5)
	ds_write_b128 v42, v[72:75] offset:10240
	s_waitcnt vmcnt(4)
	ds_write_b128 v42, v[76:79] offset:11264
	s_waitcnt vmcnt(3)
	ds_write_b128 v43, v[80:83] offset:12288
	s_waitcnt vmcnt(2)
	ds_write_b128 v43, v[84:87] offset:13312
	s_waitcnt vmcnt(1)
	ds_write_b128 v44, v[88:91] offset:14336
	s_waitcnt vmcnt(0)
	ds_write_b128 v44, v[92:95] offset:15360
	s_waitcnt lgkmcnt(0)
	ds_read2_b32 v[6:7], v28 offset1:32
	ds_read2_b32 v[8:9], v46 offset1:32
	ds_read2_b32 v[10:11], v28 offset0:64 offset1:96
	ds_read2_b32 v[12:13], v46 offset0:64 offset1:96
	v_lshl_add_u64 v[4:5], s[8:9], 0, v[2:3]
	s_waitcnt lgkmcnt(3)
	v_mul_f32_e32 v14, 0x42000000, v6
	s_waitcnt lgkmcnt(2)
	v_mul_f32_e32 v15, 0x42000000, v8
	v_mul_f32_e32 v16, 0x42000000, v7
	v_mul_f32_e32 v17, 0x42000000, v9
	s_waitcnt lgkmcnt(1)
	v_mul_f32_e32 v18, 0x42000000, v10
	ds_read2_b32 v[6:7], v28 offset0:128 offset1:160
	s_waitcnt lgkmcnt(1)
	v_mul_f32_e32 v19, 0x42000000, v12
	v_mul_f32_e32 v20, 0x42000000, v11
	ds_read2_b32 v[8:9], v46 offset0:128 offset1:160
	v_mul_f32_e32 v21, 0x42000000, v13
	ds_read2_b32 v[10:11], v28 offset0:192 offset1:224
	ds_read2_b32 v[12:13], v46 offset0:192 offset1:224
	s_waitcnt lgkmcnt(3)
	v_mul_f32_e32 v22, 0x42000000, v6
	v_mul_f32_e32 v7, 0x42000000, v7
	s_waitcnt lgkmcnt(2)
	v_mul_f32_e32 v23, 0x42000000, v8
	s_waitcnt lgkmcnt(1)
	v_mul_f32_e32 v8, 0x42000000, v10
	s_waitcnt lgkmcnt(0)
	v_mul_f32_e32 v10, 0x42000000, v12
	v_mul_f32_e32 v12, 0x42000000, v13
	v_med3_f32 v13, v14, s48, v47
	v_med3_f32 v14, v16, s48, v47
	v_mov_b32_e32 v6, v1
	v_cvt_pk_fp8_f32 v6, v13, v14
	v_med3_f32 v13, v18, s48, v47
	v_med3_f32 v16, v22, s48, v47
	v_med3_f32 v18, v7, s48, v47
	v_mov_b32_e32 v7, v1
	v_cvt_pk_fp8_f32 v7, v16, v18
	v_mul_f32_e32 v11, 0x42000000, v11
	v_med3_f32 v14, v20, s48, v47
	v_med3_f32 v8, v8, s48, v47
	v_med3_f32 v11, v11, s48, v47
	v_mul_f32_e32 v9, 0x42000000, v9
	v_cvt_pk_fp8_f32 v6, v13, v14 op_sel:[0,0,1]
	v_cvt_pk_fp8_f32 v7, v8, v11 op_sel:[0,0,1]
	v_med3_f32 v11, v15, s48, v47
	v_med3_f32 v13, v17, s48, v47
	v_mov_b32_e32 v8, v1
	v_cvt_pk_fp8_f32 v8, v11, v13
	v_med3_f32 v14, v23, s48, v47
	v_med3_f32 v15, v9, s48, v47
	v_mov_b32_e32 v9, v1
	v_cvt_pk_fp8_f32 v9, v14, v15
	v_med3_f32 v11, v19, s48, v47
	v_med3_f32 v13, v21, s48, v47
	v_cvt_pk_fp8_f32 v8, v11, v13 op_sel:[0,0,1]
	v_med3_f32 v10, v10, s48, v47
	v_med3_f32 v11, v12, s48, v47
	v_cvt_pk_fp8_f32 v9, v10, v11 op_sel:[0,0,1]
	v_or_b32_e32 v10, s7, v24
	v_lshlrev_b32_e32 v10, 11, v10
	v_mov_b32_e32 v11, v1
	v_lshl_add_u64 v[10:11], v[4:5], 0, v[10:11]
	global_store_dwordx4 v[10:11], v[6:9], off sc1
	ds_read2_b32 v[6:7], v30 offset0:64 offset1:96
	ds_read2_b32 v[12:13], v30 offset1:32
	ds_read2_b32 v[8:9], v48 offset0:64 offset1:96
	ds_read2_b32 v[10:11], v30 offset0:128 offset1:160
	ds_read2_b32 v[14:15], v48 offset1:32
	s_waitcnt lgkmcnt(4)
	v_mul_f32_e32 v18, 0x42000000, v6
	v_mul_f32_e32 v20, 0x42000000, v7
	ds_read2_b32 v[6:7], v48 offset0:128 offset1:160
	s_waitcnt lgkmcnt(4)
	v_mul_f32_e32 v16, 0x42000000, v12
	v_mul_f32_e32 v17, 0x42000000, v13
	s_waitcnt lgkmcnt(3)
	v_mul_f32_e32 v19, 0x42000000, v8
	v_mul_f32_e32 v21, 0x42000000, v9
	s_waitcnt lgkmcnt(2)
	v_mul_f32_e32 v10, 0x42000000, v10
	ds_read2_b32 v[8:9], v30 offset0:192 offset1:224
	ds_read2_b32 v[12:13], v48 offset0:192 offset1:224
	s_waitcnt lgkmcnt(2)
	v_mul_f32_e32 v22, 0x42000000, v6
	v_mul_f32_e32 v11, 0x42000000, v11
	v_mul_f32_e32 v23, 0x42000000, v7
	v_med3_f32 v7, v16, s48, v47
	v_med3_f32 v16, v17, s48, v47
	v_mov_b32_e32 v6, v1
	v_cvt_pk_fp8_f32 v6, v7, v16
	v_med3_f32 v10, v10, s48, v47
	v_med3_f32 v11, v11, s48, v47
	v_mov_b32_e32 v7, v1
	v_cvt_pk_fp8_f32 v7, v10, v11
	s_waitcnt lgkmcnt(1)
	v_mul_f32_e32 v8, 0x42000000, v8
	v_mul_f32_e32 v9, 0x42000000, v9
	v_mul_f32_e32 v14, 0x42000000, v14
	v_mul_f32_e32 v15, 0x42000000, v15
	v_med3_f32 v8, v8, s48, v47
	v_med3_f32 v9, v9, s48, v47
	v_cvt_pk_fp8_f32 v7, v8, v9 op_sel:[0,0,1]
	v_med3_f32 v9, v14, s48, v47
	v_med3_f32 v10, v15, s48, v47
	v_mov_b32_e32 v8, v1
	v_cvt_pk_fp8_f32 v8, v9, v10
	v_med3_f32 v14, v22, s48, v47
	v_med3_f32 v15, v23, s48, v47
	v_mov_b32_e32 v9, v1
	v_cvt_pk_fp8_f32 v9, v14, v15
	s_waitcnt lgkmcnt(0)
	v_mul_f32_e32 v12, 0x42000000, v12
	v_mul_f32_e32 v13, 0x42000000, v13
	v_med3_f32 v10, v19, s48, v47
	v_med3_f32 v11, v21, s48, v47
	v_med3_f32 v16, v18, s48, v47
	v_med3_f32 v17, v20, s48, v47
	v_cvt_pk_fp8_f32 v8, v10, v11 op_sel:[0,0,1]
	v_med3_f32 v10, v12, s48, v47
	v_med3_f32 v11, v13, s48, v47
	v_cvt_pk_fp8_f32 v6, v16, v17 op_sel:[0,0,1]
	v_cvt_pk_fp8_f32 v9, v10, v11 op_sel:[0,0,1]
	v_or_b32_e32 v10, s7, v29
	v_lshlrev_b32_e32 v10, 11, v10
	v_mov_b32_e32 v11, v1
	v_lshl_add_u64 v[10:11], v[4:5], 0, v[10:11]
	global_store_dwordx4 v[10:11], v[6:9], off sc1
	ds_read2_b32 v[6:7], v32 offset0:64 offset1:96
	ds_read2_b32 v[12:13], v32 offset1:32
	ds_read2_b32 v[8:9], v49 offset0:64 offset1:96
	ds_read2_b32 v[10:11], v32 offset0:128 offset1:160
	ds_read2_b32 v[14:15], v49 offset1:32
	s_waitcnt lgkmcnt(4)
	v_mul_f32_e32 v18, 0x42000000, v6
	v_mul_f32_e32 v20, 0x42000000, v7
	ds_read2_b32 v[6:7], v49 offset0:128 offset1:160
	s_waitcnt lgkmcnt(4)
	v_mul_f32_e32 v16, 0x42000000, v12
	v_mul_f32_e32 v17, 0x42000000, v13
	s_waitcnt lgkmcnt(3)
	v_mul_f32_e32 v19, 0x42000000, v8
	v_mul_f32_e32 v21, 0x42000000, v9
	s_waitcnt lgkmcnt(2)
	v_mul_f32_e32 v10, 0x42000000, v10
	ds_read2_b32 v[8:9], v32 offset0:192 offset1:224
	ds_read2_b32 v[12:13], v49 offset0:192 offset1:224
	s_waitcnt lgkmcnt(2)
	v_mul_f32_e32 v22, 0x42000000, v6
	v_mul_f32_e32 v11, 0x42000000, v11
	v_mul_f32_e32 v23, 0x42000000, v7
	v_med3_f32 v7, v16, s48, v47
	v_med3_f32 v16, v17, s48, v47
	v_mov_b32_e32 v6, v1
	v_cvt_pk_fp8_f32 v6, v7, v16
	v_med3_f32 v10, v10, s48, v47
	v_med3_f32 v11, v11, s48, v47
	v_mov_b32_e32 v7, v1
	v_cvt_pk_fp8_f32 v7, v10, v11
	s_waitcnt lgkmcnt(1)
	v_mul_f32_e32 v8, 0x42000000, v8
	v_mul_f32_e32 v9, 0x42000000, v9
	v_mul_f32_e32 v14, 0x42000000, v14
	v_mul_f32_e32 v15, 0x42000000, v15
	v_med3_f32 v8, v8, s48, v47
	v_med3_f32 v9, v9, s48, v47
	v_cvt_pk_fp8_f32 v7, v8, v9 op_sel:[0,0,1]
	v_med3_f32 v9, v14, s48, v47
	v_med3_f32 v10, v15, s48, v47
	v_mov_b32_e32 v8, v1
	v_cvt_pk_fp8_f32 v8, v9, v10
	v_med3_f32 v14, v22, s48, v47
	v_med3_f32 v15, v23, s48, v47
	v_mov_b32_e32 v9, v1
	v_cvt_pk_fp8_f32 v9, v14, v15
	s_waitcnt lgkmcnt(0)
	v_mul_f32_e32 v12, 0x42000000, v12
	v_mul_f32_e32 v13, 0x42000000, v13
	v_med3_f32 v10, v19, s48, v47
	v_med3_f32 v11, v21, s48, v47
	v_med3_f32 v16, v18, s48, v47
	v_med3_f32 v17, v20, s48, v47
	v_cvt_pk_fp8_f32 v8, v10, v11 op_sel:[0,0,1]
	v_med3_f32 v10, v12, s48, v47
	v_med3_f32 v11, v13, s48, v47
	v_cvt_pk_fp8_f32 v6, v16, v17 op_sel:[0,0,1]
	v_cvt_pk_fp8_f32 v9, v10, v11 op_sel:[0,0,1]
	v_or_b32_e32 v10, s7, v31
	v_lshlrev_b32_e32 v10, 11, v10
	v_mov_b32_e32 v11, v1
	v_lshl_add_u64 v[10:11], v[4:5], 0, v[10:11]
	global_store_dwordx4 v[10:11], v[6:9], off sc1
	ds_read2_b32 v[6:7], v35 offset0:64 offset1:96
	ds_read2_b32 v[12:13], v35 offset1:32
	ds_read2_b32 v[8:9], v50 offset0:64 offset1:96
	ds_read2_b32 v[10:11], v35 offset0:128 offset1:160
	ds_read2_b32 v[14:15], v50 offset1:32
	s_waitcnt lgkmcnt(4)
	v_mul_f32_e32 v18, 0x42000000, v6
	v_mul_f32_e32 v20, 0x42000000, v7
	ds_read2_b32 v[6:7], v50 offset0:128 offset1:160
	s_waitcnt lgkmcnt(4)
	v_mul_f32_e32 v16, 0x42000000, v12
	v_mul_f32_e32 v17, 0x42000000, v13
	s_waitcnt lgkmcnt(3)
	v_mul_f32_e32 v19, 0x42000000, v8
	v_mul_f32_e32 v21, 0x42000000, v9
	s_waitcnt lgkmcnt(2)
	v_mul_f32_e32 v10, 0x42000000, v10
	ds_read2_b32 v[8:9], v35 offset0:192 offset1:224
	ds_read2_b32 v[12:13], v50 offset0:192 offset1:224
	s_waitcnt lgkmcnt(2)
	v_mul_f32_e32 v22, 0x42000000, v6
	v_mul_f32_e32 v11, 0x42000000, v11
	v_mul_f32_e32 v23, 0x42000000, v7
	v_med3_f32 v7, v16, s48, v47
	v_med3_f32 v16, v17, s48, v47
	v_mov_b32_e32 v6, v1
	v_cvt_pk_fp8_f32 v6, v7, v16
	v_med3_f32 v10, v10, s48, v47
	v_med3_f32 v11, v11, s48, v47
	v_mov_b32_e32 v7, v1
	v_cvt_pk_fp8_f32 v7, v10, v11
	s_waitcnt lgkmcnt(1)
	v_mul_f32_e32 v8, 0x42000000, v8
	v_mul_f32_e32 v9, 0x42000000, v9
	v_mul_f32_e32 v14, 0x42000000, v14
	v_mul_f32_e32 v15, 0x42000000, v15
	v_med3_f32 v8, v8, s48, v47
	v_med3_f32 v9, v9, s48, v47
	v_cvt_pk_fp8_f32 v7, v8, v9 op_sel:[0,0,1]
	v_med3_f32 v9, v14, s48, v47
	v_med3_f32 v10, v15, s48, v47
	v_mov_b32_e32 v8, v1
	v_cvt_pk_fp8_f32 v8, v9, v10
	v_med3_f32 v14, v22, s48, v47
	v_med3_f32 v15, v23, s48, v47
	v_mov_b32_e32 v9, v1
	v_cvt_pk_fp8_f32 v9, v14, v15
	s_waitcnt lgkmcnt(0)
	v_mul_f32_e32 v12, 0x42000000, v12
	v_mul_f32_e32 v13, 0x42000000, v13
	v_med3_f32 v10, v19, s48, v47
	v_med3_f32 v11, v21, s48, v47
	v_med3_f32 v16, v18, s48, v47
	v_med3_f32 v17, v20, s48, v47
	v_cvt_pk_fp8_f32 v8, v10, v11 op_sel:[0,0,1]
	v_med3_f32 v10, v12, s48, v47
	v_med3_f32 v11, v13, s48, v47
	v_cvt_pk_fp8_f32 v6, v16, v17 op_sel:[0,0,1]
	v_cvt_pk_fp8_f32 v9, v10, v11 op_sel:[0,0,1]
	v_or_b32_e32 v10, s7, v33
	v_lshlrev_b32_e32 v10, 11, v10
	v_mov_b32_e32 v11, v1
	v_lshl_add_u64 v[4:5], v[4:5], 0, v[10:11]
	global_store_dwordx4 v[4:5], v[6:9], off sc1
	s_waitcnt lgkmcnt(0)
	s_mov_b64 s[8:9], 0
.LBB0_32:
	s_andn2_b64 vcc, exec, s[8:9]
	s_cbranch_vccnz .LBB0_29
	s_load_dwordx2 s[8:9], s[14:15], 0x30
	s_mul_i32 s7, s6, 0x3300000
	s_mul_hi_i32 s4, s6, 0x3300000
	s_mul_i32 s11, s10, 0xffffa0a1
	s_waitcnt lgkmcnt(0)
	s_add_u32 s18, s8, s7
	s_addc_u32 s19, s9, s4
	s_lshr_b32 s4, s11, 16
	s_add_i32 s4, s4, s10
	s_sext_i32_i16 s7, s4
	s_ashr_i32 s7, s7, 7
	s_bfe_u32 s4, s4, 0x1000f
	s_add_i32 s4, s7, s4
	s_sext_i32_i16 s7, s4
	s_mulk_i32 s4, 0xcc
	s_lshl_b32 s7, s7, 7
	s_sub_i32 s4, s10, s4
	v_or_b32_e32 v4, s7, v24
	s_sext_i32_i16 s8, s4
	v_mul_i32_i24_e32 v4, 0x6600, v4
	s_lshl_b32 s8, s8, 5
	v_ashrrev_i32_e32 v5, 31, v4
	v_lshl_add_u64 v[4:5], s[18:19], 0, v[4:5]
	s_ashr_i32 s9, s8, 31
	v_lshl_add_u64 v[4:5], s[8:9], 2, v[4:5]
	v_lshl_add_u64 v[12:13], v[4:5], 0, v[0:1]
	v_add_co_u32_e32 v8, vcc, s49, v12
	s_nop 1
	v_addc_co_u32_e32 v9, vcc, 0, v13, vcc
	v_add_co_u32_e32 v14, vcc, s50, v12
	global_load_dwordx4 v[4:7], v[12:13], off nt
	s_nop 0
	global_load_dwordx4 v[8:11], v[8:9], off nt
	v_addc_co_u32_e32 v15, vcc, 0, v13, vcc
	v_add_co_u32_e32 v16, vcc, s51, v12
	s_nop 1
	v_addc_co_u32_e32 v17, vcc, 0, v13, vcc
	v_add_co_u32_e32 v20, vcc, s52, v12
	s_nop 1
	v_addc_co_u32_e32 v21, vcc, 0, v13, vcc
	v_add_co_u32_e32 v52, vcc, s53, v12
	s_nop 1
	v_addc_co_u32_e32 v53, vcc, 0, v13, vcc
	v_add_co_u32_e32 v56, vcc, s54, v12
	s_nop 1
	v_addc_co_u32_e32 v57, vcc, 0, v13, vcc
	v_add_co_u32_e32 v60, vcc, s55, v12
	s_nop 1
	v_addc_co_u32_e32 v61, vcc, 0, v13, vcc
	v_add_co_u32_e32 v64, vcc, s56, v12
	s_nop 1
	v_addc_co_u32_e32 v65, vcc, 0, v13, vcc
	v_add_co_u32_e32 v68, vcc, s57, v12
	s_nop 1
	v_addc_co_u32_e32 v69, vcc, 0, v13, vcc
	v_add_co_u32_e32 v72, vcc, s58, v12
	s_nop 1
	v_addc_co_u32_e32 v73, vcc, 0, v13, vcc
	v_add_co_u32_e32 v76, vcc, s59, v12
	s_nop 1
	v_addc_co_u32_e32 v77, vcc, 0, v13, vcc
	v_add_co_u32_e32 v80, vcc, s60, v12
	s_nop 1
	v_addc_co_u32_e32 v81, vcc, 0, v13, vcc
	v_add_co_u32_e32 v84, vcc, s61, v12
	s_nop 1
	v_addc_co_u32_e32 v85, vcc, 0, v13, vcc
	v_add_co_u32_e32 v88, vcc, s62, v12
	s_nop 1
	v_addc_co_u32_e32 v89, vcc, 0, v13, vcc
	v_add_co_u32_e32 v92, vcc, s63, v12
	s_nop 1
	v_addc_co_u32_e32 v93, vcc, 0, v13, vcc
	global_load_dwordx4 v[12:15], v[14:15], off nt
	s_nop 0
	global_load_dwordx4 v[16:19], v[16:17], off nt
	s_nop 0
	global_load_dwordx4 v[20:23], v[20:21], off nt
	s_nop 0
	global_load_dwordx4 v[52:55], v[52:53], off nt
	s_nop 0
	global_load_dwordx4 v[56:59], v[56:57], off nt
	s_nop 0
	global_load_dwordx4 v[60:63], v[60:61], off nt
	s_nop 0
	global_load_dwordx4 v[64:67], v[64:65], off nt
	s_nop 0
	global_load_dwordx4 v[68:71], v[68:69], off nt
	s_nop 0
	global_load_dwordx4 v[72:75], v[72:73], off nt
	s_nop 0
	global_load_dwordx4 v[76:79], v[76:77], off nt
	s_nop 0
	global_load_dwordx4 v[80:83], v[80:81], off nt
	s_nop 0
	global_load_dwordx4 v[84:87], v[84:85], off nt
	s_nop 0
	global_load_dwordx4 v[88:91], v[88:89], off nt
	s_nop 0
	global_load_dwordx4 v[92:95], v[92:93], off nt
	s_waitcnt vmcnt(15)
	ds_write_b128 v45, v[4:7]
	s_waitcnt vmcnt(14)
	ds_write_b128 v45, v[8:11] offset:1024
	s_waitcnt vmcnt(13)
	ds_write_b128 v38, v[12:15] offset:2048
	s_waitcnt vmcnt(12)
	ds_write_b128 v38, v[16:19] offset:3072
	s_waitcnt vmcnt(11)
	ds_write_b128 v39, v[20:23] offset:4096
	s_waitcnt vmcnt(10)
	ds_write_b128 v39, v[52:55] offset:5120
	s_waitcnt vmcnt(9)
	ds_write_b128 v40, v[56:59] offset:6144
	s_waitcnt vmcnt(8)
	ds_write_b128 v40, v[60:63] offset:7168
	s_waitcnt vmcnt(7)
	ds_write_b128 v41, v[64:67] offset:8192
	s_waitcnt vmcnt(6)
	ds_write_b128 v41, v[68:71] offset:9216
	s_waitcnt vmcnt(5)
	ds_write_b128 v42, v[72:75] offset:10240
	s_waitcnt vmcnt(4)
	ds_write_b128 v42, v[76:79] offset:11264
	s_waitcnt vmcnt(3)
	ds_write_b128 v43, v[80:83] offset:12288
	s_waitcnt vmcnt(2)
	ds_write_b128 v43, v[84:87] offset:13312
	s_waitcnt vmcnt(1)
	ds_write_b128 v44, v[88:91] offset:14336
	s_waitcnt vmcnt(0)
	ds_write_b128 v44, v[92:95] offset:15360
	s_waitcnt lgkmcnt(0)
	ds_read2_b32 v[20:21], v28 offset1:32
	ds_read2_b32 v[22:23], v46 offset1:32
	ds_read2_b32 v[16:17], v28 offset0:64 offset1:96
	ds_read2_b32 v[18:19], v46 offset0:64 offset1:96
	ds_read2_b32 v[12:13], v28 offset0:128 offset1:160
	ds_read2_b32 v[14:15], v46 offset0:128 offset1:160
	ds_read2_b32 v[8:9], v28 offset0:192 offset1:224
	ds_read2_b32 v[10:11], v46 offset0:192 offset1:224
	v_or_b32_e32 v4, s8, v24
	v_cmp_lt_i32_e64 s[10:11], s64, v4
	v_cmp_gt_i32_e32 vcc, s65, v4
	s_and_saveexec_b64 s[18:19], vcc
	s_bitcmp1_b32 s4, 0
	s_cselect_b64 s[68:69], -1, 0
	s_andn2_b64 s[10:11], s[10:11], exec
	s_and_b64 s[68:69], s[68:69], exec
	v_and_or_b32 v6, v4, s66, v36
	s_or_b64 s[10:11], s[10:11], s[68:69]
	s_or_b64 exec, exec, s[18:19]
	s_and_saveexec_b64 s[18:19], s[10:11]
	v_mov_b32_e32 v6, v4
	s_or_b64 exec, exec, s[18:19]
	s_waitcnt lgkmcnt(7)
	v_mul_f32_e32 v7, 0x42000000, v20
	v_mul_f32_e32 v21, 0x42000000, v21
	s_waitcnt lgkmcnt(3)
	v_mul_f32_e32 v12, 0x42000000, v12
	v_mul_f32_e32 v13, 0x42000000, v13
	v_med3_f32 v7, v7, s48, v47
	v_med3_f32 v21, v21, s48, v47
	v_mov_b32_e32 v52, 0
	v_cvt_pk_fp8_f32 v52, v7, v21
	v_med3_f32 v12, v12, s48, v47
	v_med3_f32 v13, v13, s48, v47
	v_mov_b32_e32 v53, 0
	v_cvt_pk_fp8_f32 v53, v12, v13
	v_mul_f32_e32 v16, 0x42000000, v16
	v_mul_f32_e32 v17, 0x42000000, v17
	s_waitcnt lgkmcnt(1)
	v_mul_f32_e32 v8, 0x42000000, v8
	v_mul_f32_e32 v9, 0x42000000, v9
	v_med3_f32 v7, v16, s48, v47
	v_med3_f32 v16, v17, s48, v47
	v_mul_f32_e32 v20, 0x42000000, v22
	v_mul_f32_e32 v22, 0x42000000, v23
	v_cvt_pk_fp8_f32 v52, v7, v16 op_sel:[0,0,1]
	v_med3_f32 v7, v8, s48, v47
	v_med3_f32 v8, v9, s48, v47
	v_mul_f32_e32 v14, 0x42000000, v14
	v_mul_f32_e32 v15, 0x42000000, v15
	v_cvt_pk_fp8_f32 v53, v7, v8 op_sel:[0,0,1]
	v_med3_f32 v7, v20, s48, v47
	v_med3_f32 v8, v22, s48, v47
	v_mov_b32_e32 v54, 0
	v_cvt_pk_fp8_f32 v54, v7, v8
	v_med3_f32 v9, v14, s48, v47
	v_med3_f32 v12, v15, s48, v47
	v_mov_b32_e32 v55, 0
	v_cvt_pk_fp8_f32 v55, v9, v12
	v_mul_f32_e32 v18, 0x42000000, v18
	v_mul_f32_e32 v19, 0x42000000, v19
	s_waitcnt lgkmcnt(0)
	v_mul_f32_e32 v10, 0x42000000, v10
	v_mul_f32_e32 v11, 0x42000000, v11
	v_med3_f32 v7, v18, s48, v47
	v_med3_f32 v8, v19, s48, v47
	v_cvt_pk_fp8_f32 v54, v7, v8 op_sel:[0,0,1]
	v_med3_f32 v7, v10, s48, v47
	v_med3_f32 v8, v11, s48, v47
	v_cvt_pk_fp8_f32 v55, v7, v8 op_sel:[0,0,1]
	ds_read2_b32 v[22:23], v30 offset1:32
	ds_read2_b32 v[14:15], v48 offset1:32
	ds_read2_b32 v[20:21], v30 offset0:64 offset1:96
	ds_read2_b32 v[12:13], v48 offset0:64 offset1:96
	ds_read2_b32 v[18:19], v30 offset0:128 offset1:160
	ds_read2_b32 v[10:11], v48 offset0:128 offset1:160
	ds_read2_b32 v[16:17], v30 offset0:192 offset1:224
	ds_read2_b32 v[8:9], v48 offset0:192 offset1:224
	s_mul_hi_i32 s9, s6, 0xd00000
	s_mul_i32 s6, s6, 0xd00000
	s_add_u32 s6, s22, s6
	s_addc_u32 s9, s23, s9
	s_ashr_i32 s10, s7, 31
	s_add_u32 s6, s6, s7
	s_addc_u32 s7, s9, s10
	v_ashrrev_i32_e32 v7, 31, v6
	v_lshl_add_u64 v[4:5], s[6:7], 0, v[2:3]
	v_lshlrev_b64 v[6:7], 11, v[6:7]
	v_lshl_add_u64 v[6:7], v[4:5], 0, v[6:7]
	global_store_dwordx4 v[6:7], v[52:55], off sc1
	v_or_b32_e32 v7, s8, v29
	v_cmp_lt_i32_e64 s[6:7], s64, v7
	v_cmp_gt_i32_e32 vcc, s65, v7
	s_and_saveexec_b64 s[10:11], vcc
	s_bitcmp1_b32 s4, 0
	s_cselect_b64 s[18:19], -1, 0
	s_andn2_b64 s[6:7], s[6:7], exec
	s_and_b64 s[18:19], s[18:19], exec
	v_and_or_b32 v6, v7, s66, v37
	s_or_b64 s[6:7], s[6:7], s[18:19]
	s_or_b64 exec, exec, s[10:11]
	s_and_saveexec_b64 s[10:11], s[6:7]
	s_cbranch_execz .LBB0_28
	v_mov_b32_e32 v6, v7
	s_branch .LBB0_28

.LBB0_178:
	s_mul_hi_i32 s10, s34, 0x2aaaaaab
	s_lshr_b32 s14, s10, 31
	s_ashr_i32 s10, s10, 8
	s_add_i32 s14, s10, s14
	s_mul_i32 s10, s14, 0xfffffa00
	s_add_i32 s65, s34, s10
	s_cmpk_gt_i32 s65, 0x1ff
	s_mov_b64 s[16:17], -1
	s_cbranch_scc0 .LBB0_184
	s_ashr_i32 s15, s14, 31
	s_lshl_b64 s[16:17], s[14:15], 23
	s_cmpk_gt_u32 s65, 0x3ff
	s_mov_b64 s[18:19], -1
	s_cbranch_scc0 .LBB0_181
	s_waitcnt lgkmcnt(0)
	s_add_u32 s66, s8, s16
	s_addc_u32 s67, s9, s17
	s_lshl_b64 s[18:19], s[14:15], 21
	s_add_u32 s68, s22, s18
	s_addc_u32 s19, s23, s19
	s_lshl_b32 s10, s14, 10
	s_sub_i32 s10, s29, s10
	s_and_b32 s69, s10, 0x780
	s_add_i32 s10, s25, 0xffffc000
	v_or_b32_e32 v4, s69, v24
	s_and_b32 s18, s10, 0x7e0
	v_lshlrev_b32_e32 v4, 13, v4
	v_mov_b32_e32 v5, v1
	v_lshl_add_u64 v[4:5], s[66:67], 0, v[4:5]
	s_lshl_b32 s10, s18, 2
	v_lshl_add_u64 v[4:5], v[4:5], 0, s[10:11]
	v_lshl_add_u64 v[4:5], v[4:5], 0, v[0:1]
	v_add_co_u32_e32 v34, vcc, s31, v4
	s_add_u32 s66, s68, s69
	s_nop 0
	v_addc_co_u32_e32 v35, vcc, 0, v5, vcc
	v_add_co_u32_e32 v38, vcc, s35, v4
	global_load_dwordx4 v[30:33], v[4:5], off nt
	s_nop 0
	global_load_dwordx4 v[34:37], v[34:35], off nt
	v_addc_co_u32_e32 v39, vcc, 0, v5, vcc
	v_add_co_u32_e32 v42, vcc, s36, v4
	s_addc_u32 s67, s19, 0
	s_nop 0
	v_addc_co_u32_e32 v43, vcc, 0, v5, vcc
	v_add_co_u32_e32 v46, vcc, s37, v4
	global_load_dwordx4 v[38:41], v[38:39], off nt
	s_nop 0
	global_load_dwordx4 v[42:45], v[42:43], off nt
	v_addc_co_u32_e32 v47, vcc, 0, v5, vcc
	v_add_co_u32_e32 v50, vcc, s38, v4
	s_nop 1
	v_addc_co_u32_e32 v51, vcc, 0, v5, vcc
	v_add_co_u32_e32 v54, vcc, s39, v4
	global_load_dwordx4 v[46:49], v[46:47], off nt
	s_nop 0
	global_load_dwordx4 v[50:53], v[50:51], off nt
	v_addc_co_u32_e32 v55, vcc, 0, v5, vcc
	v_add_co_u32_e32 v58, vcc, s40, v4
	s_nop 1
	v_addc_co_u32_e32 v59, vcc, 0, v5, vcc
	v_add_co_u32_e32 v62, vcc, s41, v4
	global_load_dwordx4 v[54:57], v[54:55], off nt
	s_nop 0
	global_load_dwordx4 v[58:61], v[58:59], off nt
	v_addc_co_u32_e32 v63, vcc, 0, v5, vcc
	v_add_co_u32_e32 v66, vcc, s42, v4
	s_nop 1
	v_addc_co_u32_e32 v67, vcc, 0, v5, vcc
	v_add_co_u32_e32 v70, vcc, s43, v4
	global_load_dwordx4 v[62:65], v[62:63], off nt
	s_nop 0
	global_load_dwordx4 v[66:69], v[66:67], off nt
	v_addc_co_u32_e32 v71, vcc, 0, v5, vcc
	v_add_co_u32_e32 v74, vcc, s44, v4
	s_nop 1
	v_addc_co_u32_e32 v75, vcc, 0, v5, vcc
	v_add_co_u32_e32 v78, vcc, s45, v4
	global_load_dwordx4 v[70:73], v[70:71], off nt
	s_nop 0
	global_load_dwordx4 v[74:77], v[74:75], off nt
	v_addc_co_u32_e32 v79, vcc, 0, v5, vcc
	v_add_co_u32_e32 v82, vcc, s46, v4
	s_nop 1
	v_addc_co_u32_e32 v83, vcc, 0, v5, vcc
	v_add_co_u32_e32 v86, vcc, s47, v4
	global_load_dwordx4 v[78:81], v[78:79], off nt
	s_nop 0
	global_load_dwordx4 v[82:85], v[82:83], off nt
	v_addc_co_u32_e32 v87, vcc, 0, v5, vcc
	v_add_co_u32_e32 v4, vcc, s48, v4
	s_nop 1
	v_addc_co_u32_e32 v5, vcc, 0, v5, vcc
	global_load_dwordx4 v[86:89], v[86:87], off nt
	s_nop 0
	global_load_dwordx4 v[90:93], v[4:5], off nt
	v_lshl_add_u64 v[4:5], s[66:67], 0, v[2:3]
	v_readlane_b32 s66, v253, 2
	s_waitcnt vmcnt(15)
	ds_write_b128 v22, v[30:33]
	s_waitcnt vmcnt(14)
	ds_write_b128 v22, v[34:37] offset:1024
	s_waitcnt vmcnt(13)
	ds_write_b128 v15, v[38:41] offset:2048
	s_waitcnt vmcnt(12)
	ds_write_b128 v15, v[42:45] offset:3072
	s_waitcnt vmcnt(11)
	ds_write_b128 v16, v[46:49] offset:4096
	s_waitcnt vmcnt(10)
	ds_write_b128 v16, v[50:53] offset:5120
	s_waitcnt vmcnt(9)
	ds_write_b128 v17, v[54:57] offset:6144
	s_waitcnt vmcnt(8)
	ds_write_b128 v17, v[58:61] offset:7168
	s_waitcnt vmcnt(7)
	ds_write_b128 v18, v[62:65] offset:8192
	s_waitcnt vmcnt(6)
	ds_write_b128 v18, v[66:69] offset:9216
	s_waitcnt vmcnt(5)
	ds_write_b128 v19, v[70:73] offset:10240
	s_waitcnt vmcnt(4)
	ds_write_b128 v19, v[74:77] offset:11264
	s_waitcnt vmcnt(3)
	ds_write_b128 v20, v[78:81] offset:12288
	s_waitcnt vmcnt(2)
	ds_write_b128 v20, v[82:85] offset:13312
	s_waitcnt vmcnt(1)
	ds_write_b128 v21, v[86:89] offset:14336
	s_waitcnt vmcnt(0)
	ds_write_b128 v21, v[90:93] offset:15360
	s_waitcnt lgkmcnt(0)
	ds_read2_b32 v[30:31], v7 offset1:32
	ds_read2_b32 v[32:33], v23 offset1:32
	ds_read2_b32 v[34:35], v7 offset0:64 offset1:96
	ds_read2_b32 v[36:37], v23 offset0:64 offset1:96
	s_waitcnt lgkmcnt(3)
	v_mul_f32_e32 v38, 0x41800000, v30
	s_waitcnt lgkmcnt(2)
	v_mul_f32_e32 v39, 0x41800000, v32
	v_mul_f32_e32 v40, 0x41800000, v31
	v_mul_f32_e32 v41, 0x41800000, v33
	s_waitcnt lgkmcnt(1)
	v_mul_f32_e32 v42, 0x41800000, v34
	ds_read2_b32 v[30:31], v7 offset0:128 offset1:160
	s_waitcnt lgkmcnt(1)
	v_mul_f32_e32 v43, 0x41800000, v36
	v_mul_f32_e32 v44, 0x41800000, v35
	ds_read2_b32 v[32:33], v23 offset0:128 offset1:160
	v_mul_f32_e32 v45, 0x41800000, v37
	ds_read2_b32 v[34:35], v7 offset0:192 offset1:224
	ds_read2_b32 v[36:37], v23 offset0:192 offset1:224
	s_waitcnt lgkmcnt(3)
	v_mul_f32_e32 v46, 0x41800000, v30
	v_mul_f32_e32 v31, 0x41800000, v31
	s_waitcnt lgkmcnt(2)
	v_mul_f32_e32 v47, 0x41800000, v32
	s_waitcnt lgkmcnt(1)
	v_mul_f32_e32 v32, 0x41800000, v34
	s_waitcnt lgkmcnt(0)
	v_mul_f32_e32 v34, 0x41800000, v36
	v_mul_f32_e32 v36, 0x41800000, v37
	v_med3_f32 v37, v38, s49, v25
	v_med3_f32 v38, v40, s49, v25
	v_mov_b32_e32 v30, v1
	v_cvt_pk_fp8_f32 v30, v37, v38
	v_med3_f32 v37, v42, s49, v25
	v_med3_f32 v40, v46, s49, v25
	v_med3_f32 v42, v31, s49, v25
	v_mov_b32_e32 v31, v1
	v_cvt_pk_fp8_f32 v31, v40, v42
	v_mul_f32_e32 v35, 0x41800000, v35
	v_med3_f32 v38, v44, s49, v25
	v_med3_f32 v32, v32, s49, v25
	v_med3_f32 v35, v35, s49, v25
	v_mul_f32_e32 v33, 0x41800000, v33
	v_cvt_pk_fp8_f32 v30, v37, v38 op_sel:[0,0,1]
	v_cvt_pk_fp8_f32 v31, v32, v35 op_sel:[0,0,1]
	v_med3_f32 v35, v39, s49, v25
	v_med3_f32 v37, v41, s49, v25
	v_mov_b32_e32 v32, v1
	v_cvt_pk_fp8_f32 v32, v35, v37
	v_med3_f32 v38, v47, s49, v25
	v_med3_f32 v39, v33, s49, v25
	v_mov_b32_e32 v33, v1
	v_cvt_pk_fp8_f32 v33, v38, v39
	v_med3_f32 v35, v43, s49, v25
	v_med3_f32 v37, v45, s49, v25
	v_cvt_pk_fp8_f32 v32, v35, v37 op_sel:[0,0,1]
	v_med3_f32 v34, v34, s49, v25
	v_med3_f32 v35, v36, s49, v25
	v_cvt_pk_fp8_f32 v33, v34, v35 op_sel:[0,0,1]
	v_or_b32_e32 v34, s18, v24
	v_lshlrev_b32_e32 v34, 10, v34
	v_mov_b32_e32 v35, v1
	v_lshl_add_u64 v[34:35], v[4:5], 0, v[34:35]
	global_store_dwordx4 v[34:35], v[30:33], off sc1
	ds_read2_b32 v[30:31], v9 offset0:64 offset1:96
	ds_read2_b32 v[36:37], v9 offset1:32
	ds_read2_b32 v[32:33], v26 offset0:64 offset1:96
	ds_read2_b32 v[34:35], v9 offset0:128 offset1:160
	ds_read2_b32 v[38:39], v26 offset1:32
	s_waitcnt lgkmcnt(4)
	v_mul_f32_e32 v42, 0x41800000, v30
	v_mul_f32_e32 v44, 0x41800000, v31
	ds_read2_b32 v[30:31], v26 offset0:128 offset1:160
	s_waitcnt lgkmcnt(4)
	v_mul_f32_e32 v40, 0x41800000, v36
	v_mul_f32_e32 v41, 0x41800000, v37
	s_waitcnt lgkmcnt(3)
	v_mul_f32_e32 v43, 0x41800000, v32
	v_mul_f32_e32 v45, 0x41800000, v33
	s_waitcnt lgkmcnt(2)
	v_mul_f32_e32 v34, 0x41800000, v34
	ds_read2_b32 v[32:33], v9 offset0:192 offset1:224
	ds_read2_b32 v[36:37], v26 offset0:192 offset1:224
	s_waitcnt lgkmcnt(2)
	v_mul_f32_e32 v46, 0x41800000, v30
	v_mul_f32_e32 v35, 0x41800000, v35
	v_mul_f32_e32 v47, 0x41800000, v31
	v_med3_f32 v31, v40, s49, v25
	v_med3_f32 v40, v41, s49, v25
	v_mov_b32_e32 v30, v1
	v_cvt_pk_fp8_f32 v30, v31, v40
	v_med3_f32 v34, v34, s49, v25
	v_med3_f32 v35, v35, s49, v25
	v_mov_b32_e32 v31, v1
	v_cvt_pk_fp8_f32 v31, v34, v35
	s_waitcnt lgkmcnt(1)
	v_mul_f32_e32 v32, 0x41800000, v32
	v_mul_f32_e32 v33, 0x41800000, v33
	v_mul_f32_e32 v38, 0x41800000, v38
	v_mul_f32_e32 v39, 0x41800000, v39
	v_med3_f32 v32, v32, s49, v25
	v_med3_f32 v33, v33, s49, v25
	v_cvt_pk_fp8_f32 v31, v32, v33 op_sel:[0,0,1]
	v_med3_f32 v33, v38, s49, v25
	v_med3_f32 v34, v39, s49, v25
	v_mov_b32_e32 v32, v1
	v_cvt_pk_fp8_f32 v32, v33, v34
	v_med3_f32 v38, v46, s49, v25
	v_med3_f32 v39, v47, s49, v25
	v_mov_b32_e32 v33, v1
	v_cvt_pk_fp8_f32 v33, v38, v39
	s_waitcnt lgkmcnt(0)
	v_mul_f32_e32 v36, 0x41800000, v36
	v_mul_f32_e32 v37, 0x41800000, v37
	v_med3_f32 v34, v43, s49, v25
	v_med3_f32 v35, v45, s49, v25
	v_med3_f32 v40, v42, s49, v25
	v_med3_f32 v41, v44, s49, v25
	v_cvt_pk_fp8_f32 v32, v34, v35 op_sel:[0,0,1]
	v_med3_f32 v34, v36, s49, v25
	v_med3_f32 v35, v37, s49, v25
	v_cvt_pk_fp8_f32 v30, v40, v41 op_sel:[0,0,1]
	v_cvt_pk_fp8_f32 v33, v34, v35 op_sel:[0,0,1]
	v_or_b32_e32 v34, s18, v8
	v_lshlrev_b32_e32 v34, 10, v34
	v_mov_b32_e32 v35, v1
	v_lshl_add_u64 v[34:35], v[4:5], 0, v[34:35]
	global_store_dwordx4 v[34:35], v[30:33], off sc1
	ds_read2_b32 v[30:31], v11 offset0:64 offset1:96
	ds_read2_b32 v[36:37], v11 offset1:32
	ds_read2_b32 v[32:33], v27 offset0:64 offset1:96
	ds_read2_b32 v[34:35], v11 offset0:128 offset1:160
	ds_read2_b32 v[38:39], v27 offset1:32
	s_waitcnt lgkmcnt(4)
	v_mul_f32_e32 v42, 0x41800000, v30
	v_mul_f32_e32 v44, 0x41800000, v31
	ds_read2_b32 v[30:31], v27 offset0:128 offset1:160
	s_waitcnt lgkmcnt(4)
	v_mul_f32_e32 v40, 0x41800000, v36
	v_mul_f32_e32 v41, 0x41800000, v37
	s_waitcnt lgkmcnt(3)
	v_mul_f32_e32 v43, 0x41800000, v32
	v_mul_f32_e32 v45, 0x41800000, v33
	s_waitcnt lgkmcnt(2)
	v_mul_f32_e32 v34, 0x41800000, v34
	ds_read2_b32 v[32:33], v11 offset0:192 offset1:224
	ds_read2_b32 v[36:37], v27 offset0:192 offset1:224
	s_waitcnt lgkmcnt(2)
	v_mul_f32_e32 v46, 0x41800000, v30
	v_mul_f32_e32 v35, 0x41800000, v35
	v_mul_f32_e32 v47, 0x41800000, v31
	v_med3_f32 v31, v40, s49, v25
	v_med3_f32 v40, v41, s49, v25
	v_mov_b32_e32 v30, v1
	v_cvt_pk_fp8_f32 v30, v31, v40
	v_med3_f32 v34, v34, s49, v25
	v_med3_f32 v35, v35, s49, v25
	v_mov_b32_e32 v31, v1
	v_cvt_pk_fp8_f32 v31, v34, v35
	s_waitcnt lgkmcnt(1)
	v_mul_f32_e32 v32, 0x41800000, v32
	v_mul_f32_e32 v33, 0x41800000, v33
	v_mul_f32_e32 v38, 0x41800000, v38
	v_mul_f32_e32 v39, 0x41800000, v39
	v_med3_f32 v32, v32, s49, v25
	v_med3_f32 v33, v33, s49, v25
	v_cvt_pk_fp8_f32 v31, v32, v33 op_sel:[0,0,1]
	v_med3_f32 v33, v38, s49, v25
	v_med3_f32 v34, v39, s49, v25
	v_mov_b32_e32 v32, v1
	v_cvt_pk_fp8_f32 v32, v33, v34
	v_med3_f32 v38, v46, s49, v25
	v_med3_f32 v39, v47, s49, v25
	v_mov_b32_e32 v33, v1
	v_cvt_pk_fp8_f32 v33, v38, v39
	s_waitcnt lgkmcnt(0)
	v_mul_f32_e32 v36, 0x41800000, v36
	v_mul_f32_e32 v37, 0x41800000, v37
	v_med3_f32 v34, v43, s49, v25
	v_med3_f32 v35, v45, s49, v25
	v_med3_f32 v40, v42, s49, v25
	v_med3_f32 v41, v44, s49, v25
	v_cvt_pk_fp8_f32 v32, v34, v35 op_sel:[0,0,1]
	v_med3_f32 v34, v36, s49, v25
	v_med3_f32 v35, v37, s49, v25
	v_cvt_pk_fp8_f32 v30, v40, v41 op_sel:[0,0,1]
	v_cvt_pk_fp8_f32 v33, v34, v35 op_sel:[0,0,1]
	v_or_b32_e32 v34, s18, v10
	v_lshlrev_b32_e32 v34, 10, v34
	v_mov_b32_e32 v35, v1
	v_lshl_add_u64 v[34:35], v[4:5], 0, v[34:35]
	global_store_dwordx4 v[34:35], v[30:33], off sc1
	ds_read2_b32 v[30:31], v13 offset0:64 offset1:96
	ds_read2_b32 v[36:37], v13 offset1:32
	ds_read2_b32 v[32:33], v28 offset0:64 offset1:96
	ds_read2_b32 v[34:35], v13 offset0:128 offset1:160
	ds_read2_b32 v[38:39], v28 offset1:32
	s_waitcnt lgkmcnt(4)
	v_mul_f32_e32 v42, 0x41800000, v30
	v_mul_f32_e32 v44, 0x41800000, v31
	ds_read2_b32 v[30:31], v28 offset0:128 offset1:160
	s_waitcnt lgkmcnt(4)
	v_mul_f32_e32 v40, 0x41800000, v36
	v_mul_f32_e32 v41, 0x41800000, v37
	s_waitcnt lgkmcnt(3)
	v_mul_f32_e32 v43, 0x41800000, v32
	v_mul_f32_e32 v45, 0x41800000, v33
	s_waitcnt lgkmcnt(2)
	v_mul_f32_e32 v34, 0x41800000, v34
	ds_read2_b32 v[32:33], v13 offset0:192 offset1:224
	ds_read2_b32 v[36:37], v28 offset0:192 offset1:224
	s_waitcnt lgkmcnt(2)
	v_mul_f32_e32 v46, 0x41800000, v30
	v_mul_f32_e32 v35, 0x41800000, v35
	v_mul_f32_e32 v47, 0x41800000, v31
	v_med3_f32 v31, v40, s49, v25
	v_med3_f32 v40, v41, s49, v25
	v_mov_b32_e32 v30, v1
	v_cvt_pk_fp8_f32 v30, v31, v40
	v_med3_f32 v34, v34, s49, v25
	v_med3_f32 v35, v35, s49, v25
	v_mov_b32_e32 v31, v1
	v_cvt_pk_fp8_f32 v31, v34, v35
	s_waitcnt lgkmcnt(1)
	v_mul_f32_e32 v32, 0x41800000, v32
	v_mul_f32_e32 v33, 0x41800000, v33
	v_mul_f32_e32 v38, 0x41800000, v38
	v_mul_f32_e32 v39, 0x41800000, v39
	v_med3_f32 v32, v32, s49, v25
	v_med3_f32 v33, v33, s49, v25
	v_cvt_pk_fp8_f32 v31, v32, v33 op_sel:[0,0,1]
	v_med3_f32 v33, v38, s49, v25
	v_med3_f32 v34, v39, s49, v25
	v_mov_b32_e32 v32, v1
	v_cvt_pk_fp8_f32 v32, v33, v34
	v_med3_f32 v38, v46, s49, v25
	v_med3_f32 v39, v47, s49, v25
	v_mov_b32_e32 v33, v1
	v_cvt_pk_fp8_f32 v33, v38, v39
	s_waitcnt lgkmcnt(0)
	v_mul_f32_e32 v36, 0x41800000, v36
	v_mul_f32_e32 v37, 0x41800000, v37
	v_med3_f32 v34, v43, s49, v25
	v_med3_f32 v35, v45, s49, v25
	v_med3_f32 v40, v42, s49, v25
	v_med3_f32 v41, v44, s49, v25
	v_cvt_pk_fp8_f32 v32, v34, v35 op_sel:[0,0,1]
	v_med3_f32 v34, v36, s49, v25
	v_med3_f32 v35, v37, s49, v25
	v_cvt_pk_fp8_f32 v30, v40, v41 op_sel:[0,0,1]
	v_cvt_pk_fp8_f32 v33, v34, v35 op_sel:[0,0,1]
	v_or_b32_e32 v34, s18, v12
	v_lshlrev_b32_e32 v34, 10, v34
	v_mov_b32_e32 v35, v1
	v_lshl_add_u64 v[4:5], v[4:5], 0, v[34:35]
	global_store_dwordx4 v[4:5], v[30:33], off sc1
	s_waitcnt lgkmcnt(0)
	s_mov_b64 s[18:19], 0
.LBB0_181:
	s_andn2_b64 vcc, exec, s[18:19]
	s_cbranch_vccnz .LBB0_183
	s_waitcnt lgkmcnt(0)
	s_add_u32 s16, s6, s16
	s_addc_u32 s17, s7, s17
	s_lshl_b64 s[18:19], s[14:15], 22
	s_add_u32 s15, s20, s18
	s_addc_u32 s18, s21, s19
	s_and_b32 s19, s27, 0x780
	v_or_b32_e32 v4, s19, v24
	s_and_b32 s10, s25, 0x3e0
	v_lshlrev_b32_e32 v4, 12, v4
	v_mov_b32_e32 v5, v1
	v_lshl_add_u64 v[4:5], s[16:17], 0, v[4:5]
	s_lshl_b32 s10, s10, 2
	v_lshl_add_u64 v[4:5], v[4:5], 0, s[10:11]
	v_lshl_add_u64 v[4:5], v[4:5], 0, v[0:1]
	v_add_co_u32_e32 v34, vcc, s50, v4
	s_mul_i32 s10, s14, 0xfffe8000
	s_nop 0
	v_addc_co_u32_e32 v35, vcc, 0, v5, vcc
	v_add_co_u32_e32 v38, vcc, s31, v4
	global_load_dwordx4 v[30:33], v[4:5], off nt
	s_nop 0
	global_load_dwordx4 v[34:37], v[34:35], off nt
	v_addc_co_u32_e32 v39, vcc, 0, v5, vcc
	v_add_co_u32_e32 v42, vcc, s51, v4
	s_add_u32 s16, s15, s19
	s_nop 0
	v_addc_co_u32_e32 v43, vcc, 0, v5, vcc
	v_add_co_u32_e32 v46, vcc, s35, v4
	global_load_dwordx4 v[38:41], v[38:39], off nt
	s_nop 0
	global_load_dwordx4 v[42:45], v[42:43], off nt
	v_addc_co_u32_e32 v47, vcc, 0, v5, vcc
	v_add_co_u32_e32 v50, vcc, s52, v4
	s_addc_u32 s17, s18, 0
	s_nop 0
	v_addc_co_u32_e32 v51, vcc, 0, v5, vcc
	v_add_co_u32_e32 v54, vcc, s36, v4
	global_load_dwordx4 v[46:49], v[46:47], off nt
	s_nop 0
	global_load_dwordx4 v[50:53], v[50:51], off nt
	v_addc_co_u32_e32 v55, vcc, 0, v5, vcc
	v_add_co_u32_e32 v58, vcc, s53, v4
	s_nop 1
	v_addc_co_u32_e32 v59, vcc, 0, v5, vcc
	v_add_co_u32_e32 v62, vcc, s37, v4
	global_load_dwordx4 v[54:57], v[54:55], off nt
	s_nop 0
	global_load_dwordx4 v[58:61], v[58:59], off nt
	v_addc_co_u32_e32 v63, vcc, 0, v5, vcc
	v_add_co_u32_e32 v66, vcc, s54, v4
	s_nop 1
	v_addc_co_u32_e32 v67, vcc, 0, v5, vcc
	v_add_co_u32_e32 v70, vcc, s38, v4
	global_load_dwordx4 v[62:65], v[62:63], off nt
	s_nop 0
	global_load_dwordx4 v[66:69], v[66:67], off nt
	v_addc_co_u32_e32 v71, vcc, 0, v5, vcc
	v_add_co_u32_e32 v74, vcc, s55, v4
	s_nop 1
	v_addc_co_u32_e32 v75, vcc, 0, v5, vcc
	v_add_co_u32_e32 v78, vcc, s39, v4
	global_load_dwordx4 v[70:73], v[70:71], off nt
	s_nop 0
	global_load_dwordx4 v[74:77], v[74:75], off nt
	v_addc_co_u32_e32 v79, vcc, 0, v5, vcc
	v_add_co_u32_e32 v82, vcc, s56, v4
	s_nop 1
	v_addc_co_u32_e32 v83, vcc, 0, v5, vcc
	v_add_co_u32_e32 v86, vcc, s40, v4
	global_load_dwordx4 v[78:81], v[78:79], off nt
	s_nop 0
	global_load_dwordx4 v[82:85], v[82:83], off nt
	v_addc_co_u32_e32 v87, vcc, 0, v5, vcc
	v_add_co_u32_e32 v4, vcc, s57, v4
	s_nop 1
	v_addc_co_u32_e32 v5, vcc, 0, v5, vcc
	global_load_dwordx4 v[86:89], v[86:87], off nt
	s_nop 0
	global_load_dwordx4 v[90:93], v[4:5], off nt
	v_lshl_add_u64 v[4:5], s[16:17], 0, v[2:3]
	s_waitcnt vmcnt(15)
	ds_write_b128 v22, v[30:33]
	s_waitcnt vmcnt(14)
	ds_write_b128 v22, v[34:37] offset:1024
	s_waitcnt vmcnt(13)
	ds_write_b128 v15, v[38:41] offset:2048
	s_waitcnt vmcnt(12)
	ds_write_b128 v15, v[42:45] offset:3072
	s_waitcnt vmcnt(11)
	ds_write_b128 v16, v[46:49] offset:4096
	s_waitcnt vmcnt(10)
	ds_write_b128 v16, v[50:53] offset:5120
	s_waitcnt vmcnt(9)
	ds_write_b128 v17, v[54:57] offset:6144
	s_waitcnt vmcnt(8)
	ds_write_b128 v17, v[58:61] offset:7168
	s_waitcnt vmcnt(7)
	ds_write_b128 v18, v[62:65] offset:8192
	s_waitcnt vmcnt(6)
	ds_write_b128 v18, v[66:69] offset:9216
	s_waitcnt vmcnt(5)
	ds_write_b128 v19, v[70:73] offset:10240
	s_waitcnt vmcnt(4)
	ds_write_b128 v19, v[74:77] offset:11264
	s_waitcnt vmcnt(3)
	ds_write_b128 v20, v[78:81] offset:12288
	s_waitcnt vmcnt(2)
	ds_write_b128 v20, v[82:85] offset:13312
	s_waitcnt vmcnt(1)
	ds_write_b128 v21, v[86:89] offset:14336
	s_waitcnt vmcnt(0)
	ds_write_b128 v21, v[90:93] offset:15360
	s_waitcnt lgkmcnt(0)
	ds_read2_b32 v[30:31], v7 offset1:32
	ds_read2_b32 v[32:33], v23 offset1:32
	ds_read2_b32 v[34:35], v7 offset0:64 offset1:96
	ds_read2_b32 v[36:37], v23 offset0:64 offset1:96
	s_waitcnt lgkmcnt(3)
	v_mul_f32_e32 v38, 0x42000000, v30
	s_waitcnt lgkmcnt(2)
	v_mul_f32_e32 v39, 0x42000000, v32
	v_mul_f32_e32 v40, 0x42000000, v31
	v_mul_f32_e32 v41, 0x42000000, v33
	s_waitcnt lgkmcnt(1)
	v_mul_f32_e32 v42, 0x42000000, v34
	ds_read2_b32 v[30:31], v7 offset0:128 offset1:160
	s_waitcnt lgkmcnt(1)
	v_mul_f32_e32 v43, 0x42000000, v36
	v_mul_f32_e32 v44, 0x42000000, v35
	ds_read2_b32 v[32:33], v23 offset0:128 offset1:160
	v_mul_f32_e32 v45, 0x42000000, v37
	ds_read2_b32 v[34:35], v7 offset0:192 offset1:224
	ds_read2_b32 v[36:37], v23 offset0:192 offset1:224
	s_waitcnt lgkmcnt(3)
	v_mul_f32_e32 v46, 0x42000000, v30
	v_mul_f32_e32 v31, 0x42000000, v31
	s_waitcnt lgkmcnt(2)
	v_mul_f32_e32 v47, 0x42000000, v32
	s_waitcnt lgkmcnt(1)
	v_mul_f32_e32 v32, 0x42000000, v34
	s_waitcnt lgkmcnt(0)
	v_mul_f32_e32 v34, 0x42000000, v36
	v_mul_f32_e32 v36, 0x42000000, v37
	v_med3_f32 v37, v38, s49, v25
	v_med3_f32 v38, v40, s49, v25
	v_mov_b32_e32 v30, v1
	v_cvt_pk_fp8_f32 v30, v37, v38
	v_med3_f32 v37, v42, s49, v25
	v_med3_f32 v40, v46, s49, v25
	v_med3_f32 v42, v31, s49, v25
	v_mov_b32_e32 v31, v1
	v_cvt_pk_fp8_f32 v31, v40, v42
	v_mul_f32_e32 v35, 0x42000000, v35
	v_med3_f32 v38, v44, s49, v25
	v_med3_f32 v32, v32, s49, v25
	v_med3_f32 v35, v35, s49, v25
	v_mul_f32_e32 v33, 0x42000000, v33
	v_cvt_pk_fp8_f32 v30, v37, v38 op_sel:[0,0,1]
	v_cvt_pk_fp8_f32 v31, v32, v35 op_sel:[0,0,1]
	v_med3_f32 v35, v39, s49, v25
	v_med3_f32 v37, v41, s49, v25
	v_mov_b32_e32 v32, v1
	v_cvt_pk_fp8_f32 v32, v35, v37
	v_med3_f32 v38, v47, s49, v25
	v_med3_f32 v39, v33, s49, v25
	v_mov_b32_e32 v33, v1
	v_cvt_pk_fp8_f32 v33, v38, v39
	v_med3_f32 v35, v43, s49, v25
	v_med3_f32 v37, v45, s49, v25
	v_cvt_pk_fp8_f32 v32, v35, v37 op_sel:[0,0,1]
	v_med3_f32 v34, v34, s49, v25
	v_med3_f32 v35, v36, s49, v25
	v_add_u32_e32 v40, s10, v14
	v_cvt_pk_fp8_f32 v33, v34, v35 op_sel:[0,0,1]
	v_add_u32_e32 v34, 0xffff8000, v40
	v_and_or_b32 v34, v34, s58, v24
	v_lshl_or_b32 v34, v34, 11, v29
	v_mov_b32_e32 v35, v1
	v_lshl_add_u64 v[34:35], v[4:5], 0, v[34:35]
	global_store_dwordx4 v[34:35], v[30:33], off sc1
	ds_read2_b32 v[30:31], v9 offset0:64 offset1:96
	ds_read2_b32 v[36:37], v9 offset1:32
	ds_read2_b32 v[32:33], v26 offset0:64 offset1:96
	ds_read2_b32 v[34:35], v9 offset0:128 offset1:160
	ds_read2_b32 v[38:39], v26 offset1:32
	s_waitcnt lgkmcnt(4)
	v_mul_f32_e32 v43, 0x42000000, v30
	v_mul_f32_e32 v45, 0x42000000, v31
	ds_read2_b32 v[30:31], v26 offset0:128 offset1:160
	s_waitcnt lgkmcnt(4)
	v_mul_f32_e32 v41, 0x42000000, v36
	v_mul_f32_e32 v42, 0x42000000, v37
	s_waitcnt lgkmcnt(3)
	v_mul_f32_e32 v44, 0x42000000, v32
	v_mul_f32_e32 v46, 0x42000000, v33
	s_waitcnt lgkmcnt(2)
	v_mul_f32_e32 v34, 0x42000000, v34
	ds_read2_b32 v[32:33], v9 offset0:192 offset1:224
	ds_read2_b32 v[36:37], v26 offset0:192 offset1:224
	s_waitcnt lgkmcnt(2)
	v_mul_f32_e32 v47, 0x42000000, v30
	v_mul_f32_e32 v35, 0x42000000, v35
	v_mul_f32_e32 v48, 0x42000000, v31
	v_med3_f32 v31, v41, s49, v25
	v_med3_f32 v41, v42, s49, v25
	v_mov_b32_e32 v30, v1
	v_cvt_pk_fp8_f32 v30, v31, v41
	v_med3_f32 v34, v34, s49, v25
	v_med3_f32 v35, v35, s49, v25
	v_mov_b32_e32 v31, v1
	v_cvt_pk_fp8_f32 v31, v34, v35
	s_waitcnt lgkmcnt(1)
	v_mul_f32_e32 v32, 0x42000000, v32
	v_mul_f32_e32 v33, 0x42000000, v33
	v_mul_f32_e32 v38, 0x42000000, v38
	v_mul_f32_e32 v39, 0x42000000, v39
	v_med3_f32 v32, v32, s49, v25
	v_med3_f32 v33, v33, s49, v25
	v_cvt_pk_fp8_f32 v31, v32, v33 op_sel:[0,0,1]
	v_med3_f32 v33, v38, s49, v25
	v_med3_f32 v34, v39, s49, v25
	v_mov_b32_e32 v32, v1
	v_cvt_pk_fp8_f32 v32, v33, v34
	v_med3_f32 v38, v47, s49, v25
	v_med3_f32 v39, v48, s49, v25
	v_mov_b32_e32 v33, v1
	v_cvt_pk_fp8_f32 v33, v38, v39
	s_waitcnt lgkmcnt(0)
	v_mul_f32_e32 v36, 0x42000000, v36
	v_mul_f32_e32 v37, 0x42000000, v37
	v_med3_f32 v34, v44, s49, v25
	v_med3_f32 v35, v46, s49, v25
	v_med3_f32 v41, v43, s49, v25
	v_med3_f32 v42, v45, s49, v25
	v_cvt_pk_fp8_f32 v32, v34, v35 op_sel:[0,0,1]
	v_med3_f32 v34, v36, s49, v25
	v_med3_f32 v35, v37, s49, v25
	v_cvt_pk_fp8_f32 v30, v41, v42 op_sel:[0,0,1]
	v_cvt_pk_fp8_f32 v33, v34, v35 op_sel:[0,0,1]
	v_add_u32_e32 v34, 0xffff8010, v40
	v_and_or_b32 v34, v34, s59, v24
	v_lshl_or_b32 v34, v34, 11, v29
	v_mov_b32_e32 v35, v1
	v_lshl_add_u64 v[34:35], v[4:5], 0, v[34:35]
	global_store_dwordx4 v[34:35], v[30:33], off sc1
	ds_read2_b32 v[30:31], v11 offset0:64 offset1:96
	ds_read2_b32 v[36:37], v11 offset1:32
	ds_read2_b32 v[32:33], v27 offset0:64 offset1:96
	ds_read2_b32 v[34:35], v11 offset0:128 offset1:160
	ds_read2_b32 v[38:39], v27 offset1:32
	s_waitcnt lgkmcnt(4)
	v_mul_f32_e32 v43, 0x42000000, v30
	v_mul_f32_e32 v45, 0x42000000, v31
	ds_read2_b32 v[30:31], v27 offset0:128 offset1:160
	s_waitcnt lgkmcnt(4)
	v_mul_f32_e32 v41, 0x42000000, v36
	v_mul_f32_e32 v42, 0x42000000, v37
	s_waitcnt lgkmcnt(3)
	v_mul_f32_e32 v44, 0x42000000, v32
	v_mul_f32_e32 v46, 0x42000000, v33
	s_waitcnt lgkmcnt(2)
	v_mul_f32_e32 v34, 0x42000000, v34
	ds_read2_b32 v[32:33], v11 offset0:192 offset1:224
	ds_read2_b32 v[36:37], v27 offset0:192 offset1:224
	s_waitcnt lgkmcnt(2)
	v_mul_f32_e32 v47, 0x42000000, v30
	v_mul_f32_e32 v35, 0x42000000, v35
	v_mul_f32_e32 v48, 0x42000000, v31
	v_med3_f32 v31, v41, s49, v25
	v_med3_f32 v41, v42, s49, v25
	v_mov_b32_e32 v30, v1
	v_cvt_pk_fp8_f32 v30, v31, v41
	v_med3_f32 v34, v34, s49, v25
	v_med3_f32 v35, v35, s49, v25
	v_mov_b32_e32 v31, v1
	v_cvt_pk_fp8_f32 v31, v34, v35
	s_waitcnt lgkmcnt(1)
	v_mul_f32_e32 v32, 0x42000000, v32
	v_mul_f32_e32 v33, 0x42000000, v33
	v_mul_f32_e32 v38, 0x42000000, v38
	v_mul_f32_e32 v39, 0x42000000, v39
	v_med3_f32 v32, v32, s49, v25
	v_med3_f32 v33, v33, s49, v25
	v_cvt_pk_fp8_f32 v31, v32, v33 op_sel:[0,0,1]
	v_med3_f32 v33, v38, s49, v25
	v_med3_f32 v34, v39, s49, v25
	v_mov_b32_e32 v32, v1
	v_cvt_pk_fp8_f32 v32, v33, v34
	v_med3_f32 v38, v47, s49, v25
	v_med3_f32 v39, v48, s49, v25
	v_mov_b32_e32 v33, v1
	v_cvt_pk_fp8_f32 v33, v38, v39
	s_waitcnt lgkmcnt(0)
	v_mul_f32_e32 v36, 0x42000000, v36
	v_mul_f32_e32 v37, 0x42000000, v37
	v_med3_f32 v34, v44, s49, v25
	v_med3_f32 v35, v46, s49, v25
	v_med3_f32 v41, v43, s49, v25
	v_med3_f32 v42, v45, s49, v25
	v_cvt_pk_fp8_f32 v32, v34, v35 op_sel:[0,0,1]
	v_med3_f32 v34, v36, s49, v25
	v_med3_f32 v35, v37, s49, v25
	v_cvt_pk_fp8_f32 v30, v41, v42 op_sel:[0,0,1]
	v_cvt_pk_fp8_f32 v33, v34, v35 op_sel:[0,0,1]
	v_add_u32_e32 v34, 0xffff8020, v40
	v_and_or_b32 v34, v34, s60, v24
	v_lshl_or_b32 v34, v34, 11, v29
	v_mov_b32_e32 v35, v1
	v_lshl_add_u64 v[34:35], v[4:5], 0, v[34:35]
	global_store_dwordx4 v[34:35], v[30:33], off sc1
	ds_read2_b32 v[30:31], v13 offset0:64 offset1:96
	ds_read2_b32 v[36:37], v13 offset1:32
	ds_read2_b32 v[32:33], v28 offset0:64 offset1:96
	ds_read2_b32 v[34:35], v13 offset0:128 offset1:160
	ds_read2_b32 v[38:39], v28 offset1:32
	s_waitcnt lgkmcnt(4)
	v_mul_f32_e32 v43, 0x42000000, v30
	v_mul_f32_e32 v45, 0x42000000, v31
	ds_read2_b32 v[30:31], v28 offset0:128 offset1:160
	s_waitcnt lgkmcnt(4)
	v_mul_f32_e32 v41, 0x42000000, v36
	v_mul_f32_e32 v42, 0x42000000, v37
	s_waitcnt lgkmcnt(3)
	v_mul_f32_e32 v44, 0x42000000, v32
	v_mul_f32_e32 v46, 0x42000000, v33
	s_waitcnt lgkmcnt(2)
	v_mul_f32_e32 v34, 0x42000000, v34
	ds_read2_b32 v[32:33], v13 offset0:192 offset1:224
	ds_read2_b32 v[36:37], v28 offset0:192 offset1:224
	s_waitcnt lgkmcnt(2)
	v_mul_f32_e32 v47, 0x42000000, v30
	v_mul_f32_e32 v35, 0x42000000, v35
	v_mul_f32_e32 v48, 0x42000000, v31
	v_med3_f32 v31, v41, s49, v25
	v_med3_f32 v41, v42, s49, v25
	v_mov_b32_e32 v30, v1
	v_cvt_pk_fp8_f32 v30, v31, v41
	v_med3_f32 v34, v34, s49, v25
	v_med3_f32 v35, v35, s49, v25
	v_mov_b32_e32 v31, v1
	v_cvt_pk_fp8_f32 v31, v34, v35
	s_waitcnt lgkmcnt(1)
	v_mul_f32_e32 v32, 0x42000000, v32
	v_mul_f32_e32 v33, 0x42000000, v33
	v_mul_f32_e32 v38, 0x42000000, v38
	v_mul_f32_e32 v39, 0x42000000, v39
	v_med3_f32 v32, v32, s49, v25
	v_med3_f32 v33, v33, s49, v25
	v_cvt_pk_fp8_f32 v31, v32, v33 op_sel:[0,0,1]
	v_med3_f32 v33, v38, s49, v25
	v_med3_f32 v34, v39, s49, v25
	v_mov_b32_e32 v32, v1
	v_cvt_pk_fp8_f32 v32, v33, v34
	v_med3_f32 v38, v47, s49, v25
	v_med3_f32 v39, v48, s49, v25
	v_mov_b32_e32 v33, v1
	v_cvt_pk_fp8_f32 v33, v38, v39
	s_waitcnt lgkmcnt(0)
	v_mul_f32_e32 v36, 0x42000000, v36
	v_mul_f32_e32 v37, 0x42000000, v37
	v_med3_f32 v34, v44, s49, v25
	v_med3_f32 v35, v46, s49, v25
	v_med3_f32 v41, v43, s49, v25
	v_med3_f32 v42, v45, s49, v25
	v_cvt_pk_fp8_f32 v32, v34, v35 op_sel:[0,0,1]
	v_med3_f32 v34, v36, s49, v25
	v_med3_f32 v35, v37, s49, v25
	v_cvt_pk_fp8_f32 v30, v41, v42 op_sel:[0,0,1]
	v_cvt_pk_fp8_f32 v33, v34, v35 op_sel:[0,0,1]
	v_add_u32_e32 v34, 0xffff8030, v40
	v_and_or_b32 v34, v34, s61, v24
	v_lshl_or_b32 v34, v34, 11, v29
	v_mov_b32_e32 v35, v1
	v_lshl_add_u64 v[4:5], v[4:5], 0, v[34:35]
	global_store_dwordx4 v[4:5], v[30:33], off sc1
	s_waitcnt lgkmcnt(0)

.LBB0_184:
	s_andn2_b64 vcc, exec, s[16:17]
	s_cbranch_vccnz .LBB0_177
	s_ashr_i32 s15, s14, 31
	s_lshl_b64 s[16:17], s[14:15], 23
	s_waitcnt lgkmcnt(0)
	s_add_u32 s16, s4, s16
	s_addc_u32 s17, s5, s17
	s_lshl_b64 s[14:15], s[14:15], 22
	s_add_u32 s10, s20, s14
	s_addc_u32 s18, s21, s15
	s_bfe_u32 s14, s65, 0x5001a
	s_add_i32 s14, s65, s14
	s_sext_i32_i16 s15, s14
	s_lshl_b32 s15, s15, 2
	s_and_b32 s14, s14, 0xffe0
	s_and_b32 s19, s15, 0xffffff80
	s_sub_i32 s14, s65, s14
	v_or_b32_e32 v4, s19, v24
	s_sext_i32_i16 s14, s14
	v_ashrrev_i32_e32 v5, 31, v4
	s_lshl_b32 s14, s14, 5
	v_lshlrev_b64 v[4:5], 12, v[4:5]
	v_lshl_add_u64 v[4:5], s[16:17], 0, v[4:5]
	s_ashr_i32 s15, s14, 31
	v_lshl_add_u64 v[4:5], s[14:15], 2, v[4:5]
	v_lshl_add_u64 v[4:5], v[4:5], 0, v[0:1]
	v_add_co_u32_e32 v34, vcc, s50, v4
	s_ashr_i32 s15, s19, 31
	s_nop 0
	v_addc_co_u32_e32 v35, vcc, 0, v5, vcc
	v_add_co_u32_e32 v38, vcc, s31, v4
	global_load_dwordx4 v[30:33], v[4:5], off nt
	s_nop 0
	global_load_dwordx4 v[34:37], v[34:35], off nt
	v_addc_co_u32_e32 v39, vcc, 0, v5, vcc
	v_add_co_u32_e32 v42, vcc, s51, v4
	s_add_u32 s16, s10, s19
	s_nop 0
	v_addc_co_u32_e32 v43, vcc, 0, v5, vcc
	v_add_co_u32_e32 v46, vcc, s35, v4
	global_load_dwordx4 v[38:41], v[38:39], off nt
	s_nop 0
	global_load_dwordx4 v[42:45], v[42:43], off nt
	v_addc_co_u32_e32 v47, vcc, 0, v5, vcc
	v_add_co_u32_e32 v50, vcc, s52, v4
	s_addc_u32 s17, s18, s15
	s_nop 0
	v_addc_co_u32_e32 v51, vcc, 0, v5, vcc
	v_add_co_u32_e32 v54, vcc, s36, v4
	global_load_dwordx4 v[46:49], v[46:47], off nt
	s_nop 0
	global_load_dwordx4 v[50:53], v[50:51], off nt
	v_addc_co_u32_e32 v55, vcc, 0, v5, vcc
	v_add_co_u32_e32 v58, vcc, s53, v4
	s_nop 1
	v_addc_co_u32_e32 v59, vcc, 0, v5, vcc
	v_add_co_u32_e32 v62, vcc, s37, v4
	global_load_dwordx4 v[54:57], v[54:55], off nt
	s_nop 0
	global_load_dwordx4 v[58:61], v[58:59], off nt
	v_addc_co_u32_e32 v63, vcc, 0, v5, vcc
	v_add_co_u32_e32 v66, vcc, s54, v4
	s_nop 1
	v_addc_co_u32_e32 v67, vcc, 0, v5, vcc
	v_add_co_u32_e32 v70, vcc, s38, v4
	global_load_dwordx4 v[62:65], v[62:63], off nt
	s_nop 0
	global_load_dwordx4 v[66:69], v[66:67], off nt
	v_addc_co_u32_e32 v71, vcc, 0, v5, vcc
	v_add_co_u32_e32 v74, vcc, s55, v4
	s_nop 1
	v_addc_co_u32_e32 v75, vcc, 0, v5, vcc
	v_add_co_u32_e32 v78, vcc, s39, v4
	global_load_dwordx4 v[70:73], v[70:71], off nt
	s_nop 0
	global_load_dwordx4 v[74:77], v[74:75], off nt
	v_addc_co_u32_e32 v79, vcc, 0, v5, vcc
	v_add_co_u32_e32 v82, vcc, s56, v4
	s_nop 1
	v_addc_co_u32_e32 v83, vcc, 0, v5, vcc
	v_add_co_u32_e32 v86, vcc, s40, v4
	global_load_dwordx4 v[78:81], v[78:79], off nt
	s_nop 0
	global_load_dwordx4 v[82:85], v[82:83], off nt
	v_addc_co_u32_e32 v87, vcc, 0, v5, vcc
	v_add_co_u32_e32 v4, vcc, s57, v4
	s_nop 1
	v_addc_co_u32_e32 v5, vcc, 0, v5, vcc
	global_load_dwordx4 v[86:89], v[86:87], off nt
	s_nop 0
	global_load_dwordx4 v[90:93], v[4:5], off nt
	v_lshl_add_u64 v[4:5], s[16:17], 0, v[2:3]
	s_waitcnt vmcnt(15)
	ds_write_b128 v22, v[30:33]
	s_waitcnt vmcnt(14)
	ds_write_b128 v22, v[34:37] offset:1024
	s_waitcnt vmcnt(13)
	ds_write_b128 v15, v[38:41] offset:2048
	s_waitcnt vmcnt(12)
	ds_write_b128 v15, v[42:45] offset:3072
	s_waitcnt vmcnt(11)
	ds_write_b128 v16, v[46:49] offset:4096
	s_waitcnt vmcnt(10)
	ds_write_b128 v16, v[50:53] offset:5120
	s_waitcnt vmcnt(9)
	ds_write_b128 v17, v[54:57] offset:6144
	s_waitcnt vmcnt(8)
	ds_write_b128 v17, v[58:61] offset:7168
	s_waitcnt vmcnt(7)
	ds_write_b128 v18, v[62:65] offset:8192
	s_waitcnt vmcnt(6)
	ds_write_b128 v18, v[66:69] offset:9216
	s_waitcnt vmcnt(5)
	ds_write_b128 v19, v[70:73] offset:10240
	s_waitcnt vmcnt(4)
	ds_write_b128 v19, v[74:77] offset:11264
	s_waitcnt vmcnt(3)
	ds_write_b128 v20, v[78:81] offset:12288
	s_waitcnt vmcnt(2)
	ds_write_b128 v20, v[82:85] offset:13312
	s_waitcnt vmcnt(1)
	ds_write_b128 v21, v[86:89] offset:14336
	s_waitcnt vmcnt(0)
	ds_write_b128 v21, v[90:93] offset:15360
	s_waitcnt lgkmcnt(0)
	ds_read2_b32 v[30:31], v7 offset1:32
	ds_read2_b32 v[32:33], v23 offset1:32
	ds_read2_b32 v[34:35], v7 offset0:64 offset1:96
	ds_read2_b32 v[36:37], v23 offset0:64 offset1:96
	s_waitcnt lgkmcnt(3)
	v_mul_f32_e32 v38, 0x42000000, v30
	s_waitcnt lgkmcnt(2)
	v_mul_f32_e32 v39, 0x42000000, v32
	v_mul_f32_e32 v40, 0x42000000, v31
	v_mul_f32_e32 v41, 0x42000000, v33
	s_waitcnt lgkmcnt(1)
	v_mul_f32_e32 v42, 0x42000000, v34
	ds_read2_b32 v[30:31], v7 offset0:128 offset1:160
	s_waitcnt lgkmcnt(1)
	v_mul_f32_e32 v43, 0x42000000, v36
	v_mul_f32_e32 v44, 0x42000000, v35
	ds_read2_b32 v[32:33], v23 offset0:128 offset1:160
	v_mul_f32_e32 v45, 0x42000000, v37
	ds_read2_b32 v[34:35], v7 offset0:192 offset1:224
	ds_read2_b32 v[36:37], v23 offset0:192 offset1:224
	s_waitcnt lgkmcnt(3)
	v_mul_f32_e32 v46, 0x42000000, v30
	v_mul_f32_e32 v31, 0x42000000, v31
	s_waitcnt lgkmcnt(2)
	v_mul_f32_e32 v47, 0x42000000, v32
	s_waitcnt lgkmcnt(1)
	v_mul_f32_e32 v32, 0x42000000, v34
	s_waitcnt lgkmcnt(0)
	v_mul_f32_e32 v34, 0x42000000, v36
	v_mul_f32_e32 v36, 0x42000000, v37
	v_med3_f32 v37, v38, s49, v25
	v_med3_f32 v38, v40, s49, v25
	v_mov_b32_e32 v30, v1
	v_cvt_pk_fp8_f32 v30, v37, v38
	v_med3_f32 v37, v42, s49, v25
	v_med3_f32 v40, v46, s49, v25
	v_med3_f32 v42, v31, s49, v25
	v_mov_b32_e32 v31, v1
	v_cvt_pk_fp8_f32 v31, v40, v42
	v_mul_f32_e32 v35, 0x42000000, v35
	v_med3_f32 v38, v44, s49, v25
	v_med3_f32 v32, v32, s49, v25
	v_med3_f32 v35, v35, s49, v25
	v_mul_f32_e32 v33, 0x42000000, v33
	v_cvt_pk_fp8_f32 v30, v37, v38 op_sel:[0,0,1]
	v_cvt_pk_fp8_f32 v31, v32, v35 op_sel:[0,0,1]
	v_med3_f32 v35, v39, s49, v25
	v_med3_f32 v37, v41, s49, v25
	v_mov_b32_e32 v32, v1
	v_cvt_pk_fp8_f32 v32, v35, v37
	v_med3_f32 v38, v47, s49, v25
	v_med3_f32 v39, v33, s49, v25
	v_mov_b32_e32 v33, v1
	v_cvt_pk_fp8_f32 v33, v38, v39
	v_med3_f32 v35, v43, s49, v25
	v_med3_f32 v37, v45, s49, v25
	v_cvt_pk_fp8_f32 v32, v35, v37 op_sel:[0,0,1]
	v_med3_f32 v34, v34, s49, v25
	v_med3_f32 v35, v36, s49, v25
	v_cvt_pk_fp8_f32 v33, v34, v35 op_sel:[0,0,1]
	v_or_b32_e32 v34, s14, v24
	v_lshlrev_b32_e32 v34, 1, v34
	v_and_or_b32 v34, v34, s62, v6
	v_ashrrev_i32_e32 v35, 31, v34
	v_lshlrev_b64 v[34:35], 11, v[34:35]
	v_lshl_add_u64 v[34:35], v[4:5], 0, v[34:35]
	global_store_dwordx4 v[34:35], v[30:33], off sc1
	ds_read2_b32 v[30:31], v9 offset0:64 offset1:96
	ds_read2_b32 v[36:37], v9 offset1:32
	ds_read2_b32 v[32:33], v26 offset0:64 offset1:96
	ds_read2_b32 v[34:35], v9 offset0:128 offset1:160
	ds_read2_b32 v[38:39], v26 offset1:32
	s_waitcnt lgkmcnt(4)
	v_mul_f32_e32 v42, 0x42000000, v30
	v_mul_f32_e32 v44, 0x42000000, v31
	ds_read2_b32 v[30:31], v26 offset0:128 offset1:160
	s_waitcnt lgkmcnt(4)
	v_mul_f32_e32 v40, 0x42000000, v36
	v_mul_f32_e32 v41, 0x42000000, v37
	s_waitcnt lgkmcnt(3)
	v_mul_f32_e32 v43, 0x42000000, v32
	v_mul_f32_e32 v45, 0x42000000, v33
	s_waitcnt lgkmcnt(2)
	v_mul_f32_e32 v34, 0x42000000, v34
	ds_read2_b32 v[32:33], v9 offset0:192 offset1:224
	ds_read2_b32 v[36:37], v26 offset0:192 offset1:224
	s_waitcnt lgkmcnt(2)
	v_mul_f32_e32 v46, 0x42000000, v30
	v_mul_f32_e32 v35, 0x42000000, v35
	v_mul_f32_e32 v47, 0x42000000, v31
	v_med3_f32 v31, v40, s49, v25
	v_med3_f32 v40, v41, s49, v25
	v_mov_b32_e32 v30, v1
	v_cvt_pk_fp8_f32 v30, v31, v40
	v_med3_f32 v34, v34, s49, v25
	v_med3_f32 v35, v35, s49, v25
	v_mov_b32_e32 v31, v1
	v_cvt_pk_fp8_f32 v31, v34, v35
	s_waitcnt lgkmcnt(1)
	v_mul_f32_e32 v32, 0x42000000, v32
	v_mul_f32_e32 v33, 0x42000000, v33
	v_mul_f32_e32 v38, 0x42000000, v38
	v_mul_f32_e32 v39, 0x42000000, v39
	v_med3_f32 v32, v32, s49, v25
	v_med3_f32 v33, v33, s49, v25
	v_cvt_pk_fp8_f32 v31, v32, v33 op_sel:[0,0,1]
	v_med3_f32 v33, v38, s49, v25
	v_med3_f32 v34, v39, s49, v25
	v_mov_b32_e32 v32, v1
	v_cvt_pk_fp8_f32 v32, v33, v34
	v_med3_f32 v38, v46, s49, v25
	v_med3_f32 v39, v47, s49, v25
	v_mov_b32_e32 v33, v1
	v_cvt_pk_fp8_f32 v33, v38, v39
	s_waitcnt lgkmcnt(0)
	v_mul_f32_e32 v36, 0x42000000, v36
	v_mul_f32_e32 v37, 0x42000000, v37
	v_med3_f32 v34, v43, s49, v25
	v_med3_f32 v35, v45, s49, v25
	v_cvt_pk_fp8_f32 v32, v34, v35 op_sel:[0,0,1]
	v_med3_f32 v34, v36, s49, v25
	v_med3_f32 v35, v37, s49, v25
	v_cvt_pk_fp8_f32 v33, v34, v35 op_sel:[0,0,1]
	v_or_b32_e32 v34, s14, v8
	v_med3_f32 v40, v42, s49, v25
	v_med3_f32 v41, v44, s49, v25
	v_lshlrev_b32_e32 v34, 1, v34
	v_cvt_pk_fp8_f32 v30, v40, v41 op_sel:[0,0,1]
	v_and_or_b32 v34, v34, s63, v6
	v_ashrrev_i32_e32 v35, 31, v34
	v_lshlrev_b64 v[34:35], 11, v[34:35]
	v_lshl_add_u64 v[34:35], v[4:5], 0, v[34:35]
	global_store_dwordx4 v[34:35], v[30:33], off sc1
	ds_read2_b32 v[30:31], v11 offset0:64 offset1:96
	ds_read2_b32 v[36:37], v11 offset1:32
	ds_read2_b32 v[32:33], v27 offset0:64 offset1:96
	ds_read2_b32 v[34:35], v11 offset0:128 offset1:160
	ds_read2_b32 v[38:39], v27 offset1:32
	s_waitcnt lgkmcnt(4)
	v_mul_f32_e32 v42, 0x42000000, v30
	v_mul_f32_e32 v44, 0x42000000, v31
	ds_read2_b32 v[30:31], v27 offset0:128 offset1:160
	s_waitcnt lgkmcnt(4)
	v_mul_f32_e32 v40, 0x42000000, v36
	v_mul_f32_e32 v41, 0x42000000, v37
	s_waitcnt lgkmcnt(3)
	v_mul_f32_e32 v43, 0x42000000, v32
	v_mul_f32_e32 v45, 0x42000000, v33
	s_waitcnt lgkmcnt(2)
	v_mul_f32_e32 v34, 0x42000000, v34
	ds_read2_b32 v[32:33], v11 offset0:192 offset1:224
	ds_read2_b32 v[36:37], v27 offset0:192 offset1:224
	s_waitcnt lgkmcnt(2)
	v_mul_f32_e32 v46, 0x42000000, v30
	v_mul_f32_e32 v35, 0x42000000, v35
	v_mul_f32_e32 v47, 0x42000000, v31
	v_med3_f32 v31, v40, s49, v25
	v_med3_f32 v40, v41, s49, v25
	v_mov_b32_e32 v30, v1
	v_cvt_pk_fp8_f32 v30, v31, v40
	v_med3_f32 v34, v34, s49, v25
	v_med3_f32 v35, v35, s49, v25
	v_mov_b32_e32 v31, v1
	v_cvt_pk_fp8_f32 v31, v34, v35
	s_waitcnt lgkmcnt(1)
	v_mul_f32_e32 v32, 0x42000000, v32
	v_mul_f32_e32 v33, 0x42000000, v33
	v_mul_f32_e32 v38, 0x42000000, v38
	v_mul_f32_e32 v39, 0x42000000, v39
	v_med3_f32 v32, v32, s49, v25
	v_med3_f32 v33, v33, s49, v25
	v_cvt_pk_fp8_f32 v31, v32, v33 op_sel:[0,0,1]
	v_med3_f32 v33, v38, s49, v25
	v_med3_f32 v34, v39, s49, v25
	v_mov_b32_e32 v32, v1
	v_cvt_pk_fp8_f32 v32, v33, v34
	v_med3_f32 v38, v46, s49, v25
	v_med3_f32 v39, v47, s49, v25
	v_mov_b32_e32 v33, v1
	v_cvt_pk_fp8_f32 v33, v38, v39
	s_waitcnt lgkmcnt(0)
	v_mul_f32_e32 v36, 0x42000000, v36
	v_mul_f32_e32 v37, 0x42000000, v37
	v_med3_f32 v34, v43, s49, v25
	v_med3_f32 v35, v45, s49, v25
	v_cvt_pk_fp8_f32 v32, v34, v35 op_sel:[0,0,1]
	v_med3_f32 v34, v36, s49, v25
	v_med3_f32 v35, v37, s49, v25
	v_cvt_pk_fp8_f32 v33, v34, v35 op_sel:[0,0,1]
	v_or_b32_e32 v34, s14, v10
	v_med3_f32 v40, v42, s49, v25
	v_med3_f32 v41, v44, s49, v25
	v_lshlrev_b32_e32 v34, 1, v34
	v_cvt_pk_fp8_f32 v30, v40, v41 op_sel:[0,0,1]
	v_and_or_b32 v34, v34, s64, v6
	v_ashrrev_i32_e32 v35, 31, v34
	v_lshlrev_b64 v[34:35], 11, v[34:35]
	v_lshl_add_u64 v[34:35], v[4:5], 0, v[34:35]
	global_store_dwordx4 v[34:35], v[30:33], off sc1
	ds_read2_b32 v[30:31], v13 offset0:64 offset1:96
	ds_read2_b32 v[36:37], v13 offset1:32
	ds_read2_b32 v[32:33], v28 offset0:64 offset1:96
	ds_read2_b32 v[34:35], v13 offset0:128 offset1:160
	ds_read2_b32 v[38:39], v28 offset1:32
	s_waitcnt lgkmcnt(4)
	v_mul_f32_e32 v42, 0x42000000, v30
	v_mul_f32_e32 v44, 0x42000000, v31
	ds_read2_b32 v[30:31], v28 offset0:128 offset1:160
	s_waitcnt lgkmcnt(4)
	v_mul_f32_e32 v40, 0x42000000, v36
	v_mul_f32_e32 v41, 0x42000000, v37
	s_waitcnt lgkmcnt(3)
	v_mul_f32_e32 v43, 0x42000000, v32
	v_mul_f32_e32 v45, 0x42000000, v33
	s_waitcnt lgkmcnt(2)
	v_mul_f32_e32 v34, 0x42000000, v34
	ds_read2_b32 v[32:33], v13 offset0:192 offset1:224
	ds_read2_b32 v[36:37], v28 offset0:192 offset1:224
	s_waitcnt lgkmcnt(2)
	v_mul_f32_e32 v46, 0x42000000, v30
	v_mul_f32_e32 v35, 0x42000000, v35
	v_mul_f32_e32 v47, 0x42000000, v31
	v_med3_f32 v31, v40, s49, v25
	v_med3_f32 v40, v41, s49, v25
	v_mov_b32_e32 v30, v1
	v_cvt_pk_fp8_f32 v30, v31, v40
	v_med3_f32 v34, v34, s49, v25
	v_med3_f32 v35, v35, s49, v25
	v_mov_b32_e32 v31, v1
	v_cvt_pk_fp8_f32 v31, v34, v35
	s_waitcnt lgkmcnt(1)
	v_mul_f32_e32 v32, 0x42000000, v32
	v_mul_f32_e32 v33, 0x42000000, v33
	v_mul_f32_e32 v38, 0x42000000, v38
	v_mul_f32_e32 v39, 0x42000000, v39
	v_med3_f32 v32, v32, s49, v25
	v_med3_f32 v33, v33, s49, v25
	v_cvt_pk_fp8_f32 v31, v32, v33 op_sel:[0,0,1]
	v_med3_f32 v33, v38, s49, v25
	v_med3_f32 v34, v39, s49, v25
	v_mov_b32_e32 v32, v1
	v_cvt_pk_fp8_f32 v32, v33, v34
	v_med3_f32 v38, v46, s49, v25
	v_med3_f32 v39, v47, s49, v25
	v_mov_b32_e32 v33, v1
	v_cvt_pk_fp8_f32 v33, v38, v39
	s_waitcnt lgkmcnt(0)
	v_mul_f32_e32 v36, 0x42000000, v36
	v_mul_f32_e32 v37, 0x42000000, v37
	v_med3_f32 v34, v43, s49, v25
	v_med3_f32 v35, v45, s49, v25
	v_cvt_pk_fp8_f32 v32, v34, v35 op_sel:[0,0,1]
	v_med3_f32 v34, v36, s49, v25
	v_med3_f32 v35, v37, s49, v25
	v_cvt_pk_fp8_f32 v33, v34, v35 op_sel:[0,0,1]
	v_or_b32_e32 v34, s14, v12
	v_med3_f32 v40, v42, s49, v25
	v_med3_f32 v41, v44, s49, v25
	v_lshlrev_b32_e32 v34, 1, v34
	v_cvt_pk_fp8_f32 v30, v40, v41 op_sel:[0,0,1]
	v_and_or_b32 v34, v34, -8, v6
	v_ashrrev_i32_e32 v35, 31, v34
	v_lshlrev_b64 v[34:35], 11, v[34:35]
	v_lshl_add_u64 v[4:5], v[4:5], 0, v[34:35]
	global_store_dwordx4 v[4:5], v[30:33], off sc1
	s_waitcnt lgkmcnt(0)
	s_branch .LBB0_177

.LBB0_260:
	s_mul_hi_i32 s4, s13, 0x2aaaaaab
	s_lshr_b32 s5, s4, 31
	s_ashr_i32 s4, s4, 8
	s_add_i32 s4, s4, s5
	s_mul_i32 s5, s4, 0xfffffa00
	s_add_i32 s55, s13, s5
	s_cmpk_gt_i32 s55, 0x1ff
	s_mov_b64 s[6:7], -1
	s_cbranch_scc0 .LBB0_266
	s_ashr_i32 s5, s4, 31
	s_lshl_b64 s[6:7], s[4:5], 23
	s_cmpk_gt_u32 s55, 0x3ff
	s_mov_b64 s[8:9], -1
	s_cbranch_scc0 .LBB0_263
	s_add_u32 s56, s42, s6
	s_addc_u32 s57, s43, s7
	s_lshl_b64 s[8:9], s[4:5], 21
	s_add_u32 s58, s28, s8
	s_addc_u32 s9, s29, s9
	s_lshl_b32 s8, s4, 10
	s_sub_i32 s8, s53, s8
	s_and_b32 s59, s8, 0x780
	s_add_i32 s8, s49, 0xffffc000
	v_or_b32_e32 v0, s59, v3
	s_and_b32 s8, s8, 0x7e0
	v_lshlrev_b32_e32 v0, 13, v0
	v_lshl_add_u64 v[6:7], s[56:57], 0, v[0:1]
	s_lshl_b32 s20, s8, 2
	v_lshl_add_u64 v[6:7], v[6:7], 0, s[20:21]
	v_lshlrev_b32_e32 v0, 2, v2
	v_lshl_add_u64 v[6:7], v[6:7], 0, v[0:1]
	s_mov_b32 s20, 0x10000
	v_add_co_u32_e32 v30, vcc, s20, v6
	s_mov_b32 s20, 0x20000
	s_nop 0
	v_addc_co_u32_e32 v31, vcc, 0, v7, vcc
	v_add_co_u32_e32 v34, vcc, s20, v6
	s_mov_b32 s20, 0x30000
	s_nop 0
	v_addc_co_u32_e32 v35, vcc, 0, v7, vcc
	v_add_co_u32_e32 v38, vcc, s20, v6
	s_mov_b32 s20, 0x40000
	s_nop 0
	v_addc_co_u32_e32 v39, vcc, 0, v7, vcc
	v_add_co_u32_e32 v42, vcc, s20, v6
	s_mov_b32 s20, 0x50000
	s_nop 0
	v_addc_co_u32_e32 v43, vcc, 0, v7, vcc
	v_add_co_u32_e32 v46, vcc, s20, v6
	s_mov_b32 s20, 0x60000
	s_nop 0
	v_addc_co_u32_e32 v47, vcc, 0, v7, vcc
	v_add_co_u32_e32 v50, vcc, s20, v6
	s_mov_b32 s20, 0x70000
	s_nop 0
	v_addc_co_u32_e32 v51, vcc, 0, v7, vcc
	v_add_co_u32_e32 v54, vcc, s20, v6
	s_mov_b32 s20, 0x80000
	s_nop 0
	v_addc_co_u32_e32 v55, vcc, 0, v7, vcc
	v_add_co_u32_e32 v58, vcc, s20, v6
	s_mov_b32 s20, 0x90000
	s_nop 0
	v_addc_co_u32_e32 v59, vcc, 0, v7, vcc
	v_add_co_u32_e32 v62, vcc, s20, v6
	s_mov_b32 s20, 0xa0000
	s_nop 0
	v_addc_co_u32_e32 v63, vcc, 0, v7, vcc
	v_add_co_u32_e32 v68, vcc, s20, v6
	s_mov_b32 s20, 0xb0000
	s_nop 0
	v_addc_co_u32_e32 v69, vcc, 0, v7, vcc
	v_add_co_u32_e32 v72, vcc, s20, v6
	s_mov_b32 s20, 0xc0000
	s_nop 0
	v_addc_co_u32_e32 v73, vcc, 0, v7, vcc
	global_load_dwordx4 v[26:29], v[6:7], off nt
	s_nop 0
	global_load_dwordx4 v[30:33], v[30:31], off nt
	v_add_co_u32_e32 v76, vcc, s20, v6
	global_load_dwordx4 v[34:37], v[34:35], off nt
	s_nop 0
	global_load_dwordx4 v[38:41], v[38:39], off nt
	v_addc_co_u32_e32 v77, vcc, 0, v7, vcc
	s_mov_b32 s20, 0xd0000
	global_load_dwordx4 v[42:45], v[42:43], off nt
	s_nop 0
	global_load_dwordx4 v[46:49], v[46:47], off nt
	v_add_co_u32_e32 v80, vcc, s20, v6
	global_load_dwordx4 v[50:53], v[50:51], off nt
	s_nop 0
	global_load_dwordx4 v[54:57], v[54:55], off nt
	v_addc_co_u32_e32 v81, vcc, 0, v7, vcc
	s_mov_b32 s20, 0xe0000
	global_load_dwordx4 v[58:61], v[58:59], off nt
	s_nop 0
	global_load_dwordx4 v[62:65], v[62:63], off nt
	v_add_co_u32_e32 v84, vcc, s20, v6
	global_load_dwordx4 v[68:71], v[68:69], off nt
	s_nop 0
	global_load_dwordx4 v[72:75], v[72:73], off nt
	v_addc_co_u32_e32 v85, vcc, 0, v7, vcc
	s_mov_b32 s20, 0xf0000
	global_load_dwordx4 v[76:79], v[76:77], off nt
	s_nop 0
	global_load_dwordx4 v[80:83], v[80:81], off nt
	v_add_co_u32_e32 v6, vcc, s20, v6
	v_add_u32_e32 v0, v8, v4
	s_nop 0
	v_addc_co_u32_e32 v7, vcc, 0, v7, vcc
	global_load_dwordx4 v[84:87], v[84:85], off nt
	s_nop 0
	global_load_dwordx4 v[88:91], v[6:7], off nt
	s_waitcnt vmcnt(0)
	ds_write_b128 v0, v[26:29]
	s_waitcnt vmcnt(14)
	ds_write_b128 v0, v[30:33] offset:1024
	v_add_u32_e32 v0, v8, v9
	s_waitcnt vmcnt(13)
	ds_write_b128 v0, v[34:37] offset:2048
	s_waitcnt vmcnt(12)
	ds_write_b128 v0, v[38:41] offset:3072
	v_add_u32_e32 v0, v8, v10
	s_waitcnt vmcnt(11)
	ds_write_b128 v0, v[42:45] offset:4096
	s_waitcnt vmcnt(10)
	ds_write_b128 v0, v[46:49] offset:5120
	v_add_u32_e32 v0, v8, v11
	s_waitcnt vmcnt(9)
	ds_write_b128 v0, v[50:53] offset:6144
	s_waitcnt vmcnt(8)
	ds_write_b128 v0, v[54:57] offset:7168
	v_add_u32_e32 v0, v8, v12
	s_waitcnt vmcnt(7)
	ds_write_b128 v0, v[58:61] offset:8192
	s_waitcnt vmcnt(6)
	ds_write_b128 v0, v[62:65] offset:9216
	v_add_u32_e32 v0, v8, v13
	s_waitcnt vmcnt(5)
	ds_write_b128 v0, v[68:71] offset:10240
	s_waitcnt vmcnt(4)
	ds_write_b128 v0, v[72:75] offset:11264
	v_add_u32_e32 v0, v8, v14
	s_waitcnt vmcnt(3)
	ds_write_b128 v0, v[76:79] offset:12288
	s_waitcnt vmcnt(2)
	ds_write_b128 v0, v[80:83] offset:13312
	v_add_u32_e32 v0, v8, v15
	s_waitcnt vmcnt(1)
	ds_write_b128 v0, v[84:87] offset:14336
	s_waitcnt vmcnt(0)
	ds_write_b128 v0, v[88:91] offset:15360
	s_waitcnt lgkmcnt(0)
	v_add_u32_e32 v0, 0x400, v17
	ds_read2_b32 v[26:27], v17 offset1:32
	ds_read2_b32 v[28:29], v0 offset1:32
	ds_read2_b32 v[30:31], v17 offset0:64 offset1:96
	ds_read2_b32 v[32:33], v0 offset0:64 offset1:96
	s_add_u32 s56, s58, s59
	s_waitcnt lgkmcnt(3)
	v_mul_f32_e32 v25, 0x41800000, v26
	s_waitcnt lgkmcnt(2)
	v_mul_f32_e32 v34, 0x41800000, v28
	v_mul_f32_e32 v35, 0x41800000, v27
	v_mul_f32_e32 v36, 0x41800000, v29
	s_waitcnt lgkmcnt(1)
	v_mul_f32_e32 v37, 0x41800000, v30
	ds_read2_b32 v[26:27], v17 offset0:128 offset1:160
	s_waitcnt lgkmcnt(1)
	v_mul_f32_e32 v38, 0x41800000, v32
	v_mul_f32_e32 v39, 0x41800000, v31
	ds_read2_b32 v[28:29], v0 offset0:128 offset1:160
	v_mul_f32_e32 v40, 0x41800000, v33
	ds_read2_b32 v[30:31], v17 offset0:192 offset1:224
	ds_read2_b32 v[32:33], v0 offset0:192 offset1:224
	s_waitcnt lgkmcnt(3)
	v_mul_f32_e32 v41, 0x41800000, v26
	v_mul_f32_e32 v27, 0x41800000, v27
	s_waitcnt lgkmcnt(2)
	v_mul_f32_e32 v0, 0x41800000, v28
	s_waitcnt lgkmcnt(1)
	v_mul_f32_e32 v28, 0x41800000, v30
	s_waitcnt lgkmcnt(0)
	v_mul_f32_e32 v30, 0x41800000, v32
	v_mul_f32_e32 v32, 0x41800000, v33
	v_med3_f32 v25, v25, s33, v233
	v_med3_f32 v33, v35, s33, v233
	v_mov_b32_e32 v26, v1
	v_cvt_pk_fp8_f32 v26, v25, v33
	v_med3_f32 v25, v37, s33, v233
	v_med3_f32 v35, v41, s33, v233
	v_med3_f32 v37, v27, s33, v233
	v_mov_b32_e32 v27, v1
	v_cvt_pk_fp8_f32 v27, v35, v37
	v_mul_f32_e32 v31, 0x41800000, v31
	v_med3_f32 v33, v39, s33, v233
	v_cvt_pk_fp8_f32 v26, v25, v33 op_sel:[0,0,1]
	v_med3_f32 v25, v28, s33, v233
	v_med3_f32 v28, v31, s33, v233
	v_mul_f32_e32 v29, 0x41800000, v29
	v_cvt_pk_fp8_f32 v27, v25, v28 op_sel:[0,0,1]
	v_med3_f32 v25, v34, s33, v233
	v_med3_f32 v31, v36, s33, v233
	v_mov_b32_e32 v28, v1
	v_cvt_pk_fp8_f32 v28, v25, v31
	v_med3_f32 v0, v0, s33, v233
	v_med3_f32 v33, v29, s33, v233
	v_mov_b32_e32 v29, v1
	v_cvt_pk_fp8_f32 v29, v0, v33
	v_med3_f32 v25, v38, s33, v233
	v_med3_f32 v31, v40, s33, v233
	v_cvt_pk_fp8_f32 v28, v25, v31 op_sel:[0,0,1]
	v_med3_f32 v0, v30, s33, v233
	v_med3_f32 v25, v32, s33, v233
	v_cvt_pk_fp8_f32 v29, v0, v25 op_sel:[0,0,1]
	s_addc_u32 s57, s9, 0
	v_or_b32_e32 v0, s8, v3
	v_lshl_add_u64 v[6:7], s[56:57], 0, v[4:5]
	v_lshlrev_b32_e32 v0, 10, v0
	v_lshl_add_u64 v[34:35], v[6:7], 0, v[0:1]
	ds_read2_b32 v[30:31], v19 offset1:32
	global_store_dwordx4 v[34:35], v[26:29], off sc1
	ds_read2_b32 v[26:27], v19 offset0:64 offset1:96
	v_add_u32_e32 v25, 0x400, v19
	ds_read2_b32 v[32:33], v25 offset1:32
	s_waitcnt lgkmcnt(2)
	v_mul_f32_e32 v0, 0x41800000, v30
	ds_read2_b32 v[28:29], v25 offset0:64 offset1:96
	v_mul_f32_e32 v35, 0x41800000, v31
	s_waitcnt lgkmcnt(2)
	v_mul_f32_e32 v37, 0x41800000, v26
	ds_read2_b32 v[30:31], v19 offset0:128 offset1:160
	v_mul_f32_e32 v39, 0x41800000, v27
	ds_read2_b32 v[26:27], v25 offset0:128 offset1:160
	s_waitcnt lgkmcnt(3)
	v_mul_f32_e32 v34, 0x41800000, v32
	v_mul_f32_e32 v36, 0x41800000, v33
	s_waitcnt lgkmcnt(2)
	v_mul_f32_e32 v38, 0x41800000, v28
	v_mul_f32_e32 v40, 0x41800000, v29
	s_waitcnt lgkmcnt(1)
	v_mul_f32_e32 v30, 0x41800000, v30
	ds_read2_b32 v[28:29], v19 offset0:192 offset1:224
	ds_read2_b32 v[32:33], v25 offset0:192 offset1:224
	s_waitcnt lgkmcnt(2)
	v_mul_f32_e32 v25, 0x41800000, v26
	v_mul_f32_e32 v31, 0x41800000, v31
	v_mul_f32_e32 v41, 0x41800000, v27
	v_med3_f32 v0, v0, s33, v233
	v_med3_f32 v27, v35, s33, v233
	v_mov_b32_e32 v26, v1
	v_cvt_pk_fp8_f32 v26, v0, v27
	v_med3_f32 v30, v30, s33, v233
	v_med3_f32 v31, v31, s33, v233
	v_mov_b32_e32 v27, v1
	v_cvt_pk_fp8_f32 v27, v30, v31
	s_waitcnt lgkmcnt(1)
	v_mul_f32_e32 v28, 0x41800000, v28
	v_mul_f32_e32 v29, 0x41800000, v29
	v_med3_f32 v0, v37, s33, v233
	v_med3_f32 v35, v39, s33, v233
	v_cvt_pk_fp8_f32 v26, v0, v35 op_sel:[0,0,1]
	v_med3_f32 v0, v28, s33, v233
	v_med3_f32 v28, v29, s33, v233
	v_cvt_pk_fp8_f32 v27, v0, v28 op_sel:[0,0,1]
	v_med3_f32 v0, v34, s33, v233
	v_med3_f32 v29, v36, s33, v233
	v_mov_b32_e32 v28, v1
	v_cvt_pk_fp8_f32 v28, v0, v29
	v_med3_f32 v25, v25, s33, v233
	v_med3_f32 v31, v41, s33, v233
	v_mov_b32_e32 v29, v1
	v_cvt_pk_fp8_f32 v29, v25, v31
	s_waitcnt lgkmcnt(0)
	v_mul_f32_e32 v32, 0x41800000, v32
	v_mul_f32_e32 v33, 0x41800000, v33
	v_med3_f32 v0, v38, s33, v233
	v_med3_f32 v30, v40, s33, v233
	v_cvt_pk_fp8_f32 v28, v0, v30 op_sel:[0,0,1]
	v_med3_f32 v0, v32, s33, v233
	v_med3_f32 v25, v33, s33, v233
	v_cvt_pk_fp8_f32 v29, v0, v25 op_sel:[0,0,1]
	v_or_b32_e32 v0, s8, v18
	v_lshlrev_b32_e32 v0, 10, v0
	v_lshl_add_u64 v[34:35], v[6:7], 0, v[0:1]
	ds_read2_b32 v[30:31], v21 offset1:32
	global_store_dwordx4 v[34:35], v[26:29], off sc1
	ds_read2_b32 v[26:27], v21 offset0:64 offset1:96
	v_add_u32_e32 v25, 0x400, v21
	ds_read2_b32 v[32:33], v25 offset1:32
	s_waitcnt lgkmcnt(2)
	v_mul_f32_e32 v0, 0x41800000, v30
	ds_read2_b32 v[28:29], v25 offset0:64 offset1:96
	v_mul_f32_e32 v35, 0x41800000, v31
	s_waitcnt lgkmcnt(2)
	v_mul_f32_e32 v37, 0x41800000, v26
	ds_read2_b32 v[30:31], v21 offset0:128 offset1:160
	v_mul_f32_e32 v39, 0x41800000, v27
	ds_read2_b32 v[26:27], v25 offset0:128 offset1:160
	s_waitcnt lgkmcnt(3)
	v_mul_f32_e32 v34, 0x41800000, v32
	v_mul_f32_e32 v36, 0x41800000, v33
	s_waitcnt lgkmcnt(2)
	v_mul_f32_e32 v38, 0x41800000, v28
	v_mul_f32_e32 v40, 0x41800000, v29
	s_waitcnt lgkmcnt(1)
	v_mul_f32_e32 v30, 0x41800000, v30
	ds_read2_b32 v[28:29], v21 offset0:192 offset1:224
	ds_read2_b32 v[32:33], v25 offset0:192 offset1:224
	s_waitcnt lgkmcnt(2)
	v_mul_f32_e32 v25, 0x41800000, v26
	v_mul_f32_e32 v31, 0x41800000, v31
	v_mul_f32_e32 v41, 0x41800000, v27
	v_med3_f32 v0, v0, s33, v233
	v_med3_f32 v27, v35, s33, v233
	v_mov_b32_e32 v26, v1
	v_cvt_pk_fp8_f32 v26, v0, v27
	v_med3_f32 v30, v30, s33, v233
	v_med3_f32 v31, v31, s33, v233
	v_mov_b32_e32 v27, v1
	v_cvt_pk_fp8_f32 v27, v30, v31
	s_waitcnt lgkmcnt(1)
	v_mul_f32_e32 v28, 0x41800000, v28
	v_mul_f32_e32 v29, 0x41800000, v29
	v_med3_f32 v0, v37, s33, v233
	v_med3_f32 v35, v39, s33, v233
	v_cvt_pk_fp8_f32 v26, v0, v35 op_sel:[0,0,1]
	v_med3_f32 v0, v28, s33, v233
	v_med3_f32 v28, v29, s33, v233
	v_cvt_pk_fp8_f32 v27, v0, v28 op_sel:[0,0,1]
	v_med3_f32 v0, v34, s33, v233
	v_med3_f32 v29, v36, s33, v233
	v_mov_b32_e32 v28, v1
	v_cvt_pk_fp8_f32 v28, v0, v29
	v_med3_f32 v25, v25, s33, v233
	v_med3_f32 v31, v41, s33, v233
	v_mov_b32_e32 v29, v1
	v_cvt_pk_fp8_f32 v29, v25, v31
	s_waitcnt lgkmcnt(0)
	v_mul_f32_e32 v32, 0x41800000, v32
	v_mul_f32_e32 v33, 0x41800000, v33
	v_med3_f32 v0, v38, s33, v233
	v_med3_f32 v30, v40, s33, v233
	v_cvt_pk_fp8_f32 v28, v0, v30 op_sel:[0,0,1]
	v_med3_f32 v0, v32, s33, v233
	v_med3_f32 v25, v33, s33, v233
	v_cvt_pk_fp8_f32 v29, v0, v25 op_sel:[0,0,1]
	v_or_b32_e32 v0, s8, v20
	v_lshlrev_b32_e32 v0, 10, v0
	v_lshl_add_u64 v[34:35], v[6:7], 0, v[0:1]
	ds_read2_b32 v[30:31], v23 offset1:32
	global_store_dwordx4 v[34:35], v[26:29], off sc1
	ds_read2_b32 v[26:27], v23 offset0:64 offset1:96
	v_add_u32_e32 v25, 0x400, v23
	ds_read2_b32 v[32:33], v25 offset1:32
	s_waitcnt lgkmcnt(2)
	v_mul_f32_e32 v0, 0x41800000, v30
	ds_read2_b32 v[28:29], v25 offset0:64 offset1:96
	v_mul_f32_e32 v35, 0x41800000, v31
	s_waitcnt lgkmcnt(2)
	v_mul_f32_e32 v37, 0x41800000, v26
	ds_read2_b32 v[30:31], v23 offset0:128 offset1:160
	v_mul_f32_e32 v39, 0x41800000, v27
	ds_read2_b32 v[26:27], v25 offset0:128 offset1:160
	s_waitcnt lgkmcnt(3)
	v_mul_f32_e32 v34, 0x41800000, v32
	v_mul_f32_e32 v36, 0x41800000, v33
	s_waitcnt lgkmcnt(2)
	v_mul_f32_e32 v38, 0x41800000, v28
	v_mul_f32_e32 v40, 0x41800000, v29
	s_waitcnt lgkmcnt(1)
	v_mul_f32_e32 v30, 0x41800000, v30
	ds_read2_b32 v[28:29], v23 offset0:192 offset1:224
	ds_read2_b32 v[32:33], v25 offset0:192 offset1:224
	s_waitcnt lgkmcnt(2)
	v_mul_f32_e32 v25, 0x41800000, v26
	v_mul_f32_e32 v31, 0x41800000, v31
	v_mul_f32_e32 v41, 0x41800000, v27
	v_med3_f32 v0, v0, s33, v233
	v_med3_f32 v27, v35, s33, v233
	v_mov_b32_e32 v26, v1
	v_cvt_pk_fp8_f32 v26, v0, v27
	v_med3_f32 v30, v30, s33, v233
	v_med3_f32 v31, v31, s33, v233
	v_mov_b32_e32 v27, v1
	v_cvt_pk_fp8_f32 v27, v30, v31
	s_waitcnt lgkmcnt(1)
	v_mul_f32_e32 v28, 0x41800000, v28
	v_mul_f32_e32 v29, 0x41800000, v29
	v_med3_f32 v0, v37, s33, v233
	v_med3_f32 v35, v39, s33, v233
	v_cvt_pk_fp8_f32 v26, v0, v35 op_sel:[0,0,1]
	v_med3_f32 v0, v28, s33, v233
	v_med3_f32 v28, v29, s33, v233
	v_cvt_pk_fp8_f32 v27, v0, v28 op_sel:[0,0,1]
	v_med3_f32 v0, v34, s33, v233
	v_med3_f32 v29, v36, s33, v233
	v_mov_b32_e32 v28, v1
	v_cvt_pk_fp8_f32 v28, v0, v29
	v_med3_f32 v25, v25, s33, v233
	v_med3_f32 v31, v41, s33, v233
	v_mov_b32_e32 v29, v1
	v_cvt_pk_fp8_f32 v29, v25, v31
	s_waitcnt lgkmcnt(0)
	v_mul_f32_e32 v32, 0x41800000, v32
	v_mul_f32_e32 v33, 0x41800000, v33
	v_med3_f32 v0, v38, s33, v233
	v_med3_f32 v30, v40, s33, v233
	v_cvt_pk_fp8_f32 v28, v0, v30 op_sel:[0,0,1]
	v_med3_f32 v0, v32, s33, v233
	v_med3_f32 v25, v33, s33, v233
	v_cvt_pk_fp8_f32 v29, v0, v25 op_sel:[0,0,1]
	v_or_b32_e32 v0, s8, v22
	v_lshlrev_b32_e32 v0, 10, v0
	v_lshl_add_u64 v[6:7], v[6:7], 0, v[0:1]
	global_store_dwordx4 v[6:7], v[26:29], off sc1
	s_waitcnt lgkmcnt(0)
	s_mov_b64 s[8:9], 0
.LBB0_263:
	s_andn2_b64 vcc, exec, s[8:9]
	s_cbranch_vccnz .LBB0_265
	s_add_u32 s6, s40, s6
	s_addc_u32 s7, s41, s7
	s_lshl_b64 s[8:9], s[4:5], 22
	s_add_u32 s5, s24, s8
	s_addc_u32 s8, s25, s9
	s_and_b32 s9, s51, 0x780
	v_or_b32_e32 v0, s9, v3
	s_and_b32 s20, s49, 0x3e0
	v_lshlrev_b32_e32 v0, 12, v0
	v_lshl_add_u64 v[6:7], s[6:7], 0, v[0:1]
	s_lshl_b32 s20, s20, 2
	v_lshl_add_u64 v[6:7], v[6:7], 0, s[20:21]
	v_lshlrev_b32_e32 v0, 2, v2
	v_lshl_add_u64 v[6:7], v[6:7], 0, v[0:1]
	s_mov_b32 s6, 0x8000
	v_add_co_u32_e32 v30, vcc, s6, v6
	s_mov_b32 s6, 0x10000
	s_nop 0
	v_addc_co_u32_e32 v31, vcc, 0, v7, vcc
	v_add_co_u32_e32 v34, vcc, s6, v6
	s_mov_b32 s6, 0x18000
	s_nop 0
	v_addc_co_u32_e32 v35, vcc, 0, v7, vcc
	v_add_co_u32_e32 v38, vcc, s6, v6
	s_mov_b32 s6, 0x20000
	s_nop 0
	v_addc_co_u32_e32 v39, vcc, 0, v7, vcc
	v_add_co_u32_e32 v42, vcc, s6, v6
	s_mov_b32 s6, 0x28000
	s_nop 0
	v_addc_co_u32_e32 v43, vcc, 0, v7, vcc
	v_add_co_u32_e32 v46, vcc, s6, v6
	s_mov_b32 s6, 0x30000
	s_nop 0
	v_addc_co_u32_e32 v47, vcc, 0, v7, vcc
	v_add_co_u32_e32 v50, vcc, s6, v6
	s_mov_b32 s6, 0x38000
	s_nop 0
	v_addc_co_u32_e32 v51, vcc, 0, v7, vcc
	v_add_co_u32_e32 v54, vcc, s6, v6
	s_mov_b32 s6, 0x40000
	s_nop 0
	v_addc_co_u32_e32 v55, vcc, 0, v7, vcc
	v_add_co_u32_e32 v58, vcc, s6, v6
	s_mov_b32 s6, 0x48000
	s_nop 0
	v_addc_co_u32_e32 v59, vcc, 0, v7, vcc
	v_add_co_u32_e32 v62, vcc, s6, v6
	s_mov_b32 s6, 0x50000
	s_nop 0
	v_addc_co_u32_e32 v63, vcc, 0, v7, vcc
	v_add_co_u32_e32 v68, vcc, s6, v6
	s_mov_b32 s6, 0x58000
	s_nop 0
	v_addc_co_u32_e32 v69, vcc, 0, v7, vcc
	v_add_co_u32_e32 v72, vcc, s6, v6
	s_mov_b32 s6, 0x60000
	s_nop 0
	v_addc_co_u32_e32 v73, vcc, 0, v7, vcc
	global_load_dwordx4 v[26:29], v[6:7], off nt
	s_nop 0
	global_load_dwordx4 v[30:33], v[30:31], off nt
	v_add_co_u32_e32 v76, vcc, s6, v6
	global_load_dwordx4 v[34:37], v[34:35], off nt
	s_nop 0
	global_load_dwordx4 v[38:41], v[38:39], off nt
	v_addc_co_u32_e32 v77, vcc, 0, v7, vcc
	s_mov_b32 s6, 0x68000
	global_load_dwordx4 v[42:45], v[42:43], off nt
	s_nop 0
	global_load_dwordx4 v[46:49], v[46:47], off nt
	v_add_co_u32_e32 v80, vcc, s6, v6
	global_load_dwordx4 v[50:53], v[50:51], off nt
	s_nop 0
	global_load_dwordx4 v[54:57], v[54:55], off nt
	v_addc_co_u32_e32 v81, vcc, 0, v7, vcc
	s_mov_b32 s6, 0x70000
	global_load_dwordx4 v[58:61], v[58:59], off nt
	s_nop 0
	global_load_dwordx4 v[62:65], v[62:63], off nt
	v_add_co_u32_e32 v84, vcc, s6, v6
	global_load_dwordx4 v[68:71], v[68:69], off nt
	s_nop 0
	global_load_dwordx4 v[72:75], v[72:73], off nt
	v_addc_co_u32_e32 v85, vcc, 0, v7, vcc
	s_mov_b32 s6, 0x78000
	global_load_dwordx4 v[76:79], v[76:77], off nt
	s_nop 0
	global_load_dwordx4 v[80:83], v[80:81], off nt
	v_add_co_u32_e32 v6, vcc, s6, v6
	v_add_u32_e32 v0, v8, v4
	s_nop 0
	v_addc_co_u32_e32 v7, vcc, 0, v7, vcc
	global_load_dwordx4 v[84:87], v[84:85], off nt
	s_nop 0
	global_load_dwordx4 v[88:91], v[6:7], off nt
	s_waitcnt vmcnt(0)
	ds_write_b128 v0, v[26:29]
	s_waitcnt vmcnt(14)
	ds_write_b128 v0, v[30:33] offset:1024
	v_add_u32_e32 v0, v8, v9
	s_waitcnt vmcnt(13)
	ds_write_b128 v0, v[34:37] offset:2048
	s_waitcnt vmcnt(12)
	ds_write_b128 v0, v[38:41] offset:3072
	v_add_u32_e32 v0, v8, v10
	s_waitcnt vmcnt(11)
	ds_write_b128 v0, v[42:45] offset:4096
	s_waitcnt vmcnt(10)
	ds_write_b128 v0, v[46:49] offset:5120
	v_add_u32_e32 v0, v8, v11
	s_waitcnt vmcnt(9)
	ds_write_b128 v0, v[50:53] offset:6144
	s_waitcnt vmcnt(8)
	ds_write_b128 v0, v[54:57] offset:7168
	v_add_u32_e32 v0, v8, v12
	s_waitcnt vmcnt(7)
	ds_write_b128 v0, v[58:61] offset:8192
	s_waitcnt vmcnt(6)
	ds_write_b128 v0, v[62:65] offset:9216
	v_add_u32_e32 v0, v8, v13
	s_waitcnt vmcnt(5)
	ds_write_b128 v0, v[68:71] offset:10240
	s_waitcnt vmcnt(4)
	ds_write_b128 v0, v[72:75] offset:11264
	v_add_u32_e32 v0, v8, v14
	s_waitcnt vmcnt(3)
	ds_write_b128 v0, v[76:79] offset:12288
	s_waitcnt vmcnt(2)
	ds_write_b128 v0, v[80:83] offset:13312
	v_add_u32_e32 v0, v8, v15
	s_waitcnt vmcnt(1)
	ds_write_b128 v0, v[84:87] offset:14336
	s_waitcnt vmcnt(0)
	ds_write_b128 v0, v[88:91] offset:15360
	s_waitcnt lgkmcnt(0)
	v_add_u32_e32 v0, 0x400, v17
	ds_read2_b32 v[26:27], v17 offset1:32
	ds_read2_b32 v[28:29], v0 offset1:32
	ds_read2_b32 v[30:31], v17 offset0:64 offset1:96
	ds_read2_b32 v[32:33], v0 offset0:64 offset1:96
	s_add_u32 s6, s5, s9
	s_waitcnt lgkmcnt(3)
	v_mul_f32_e32 v25, 0x42000000, v26
	s_waitcnt lgkmcnt(2)
	v_mul_f32_e32 v34, 0x42000000, v28
	v_mul_f32_e32 v35, 0x42000000, v27
	v_mul_f32_e32 v36, 0x42000000, v29
	s_waitcnt lgkmcnt(1)
	v_mul_f32_e32 v37, 0x42000000, v30
	ds_read2_b32 v[26:27], v17 offset0:128 offset1:160
	s_waitcnt lgkmcnt(1)
	v_mul_f32_e32 v38, 0x42000000, v32
	v_mul_f32_e32 v39, 0x42000000, v31
	ds_read2_b32 v[28:29], v0 offset0:128 offset1:160
	v_mul_f32_e32 v40, 0x42000000, v33
	ds_read2_b32 v[30:31], v17 offset0:192 offset1:224
	ds_read2_b32 v[32:33], v0 offset0:192 offset1:224
	s_waitcnt lgkmcnt(3)
	v_mul_f32_e32 v41, 0x42000000, v26
	v_mul_f32_e32 v27, 0x42000000, v27
	s_waitcnt lgkmcnt(2)
	v_mul_f32_e32 v0, 0x42000000, v28
	s_waitcnt lgkmcnt(1)
	v_mul_f32_e32 v28, 0x42000000, v30
	s_waitcnt lgkmcnt(0)
	v_mul_f32_e32 v30, 0x42000000, v32
	v_mul_f32_e32 v32, 0x42000000, v33
	v_med3_f32 v25, v25, s33, v233
	v_med3_f32 v33, v35, s33, v233
	v_mov_b32_e32 v26, v1
	v_cvt_pk_fp8_f32 v26, v25, v33
	v_med3_f32 v25, v37, s33, v233
	v_med3_f32 v35, v41, s33, v233
	v_med3_f32 v37, v27, s33, v233
	v_mov_b32_e32 v27, v1
	v_cvt_pk_fp8_f32 v27, v35, v37
	v_mul_f32_e32 v31, 0x42000000, v31
	v_med3_f32 v33, v39, s33, v233
	v_cvt_pk_fp8_f32 v26, v25, v33 op_sel:[0,0,1]
	v_med3_f32 v25, v28, s33, v233
	v_med3_f32 v28, v31, s33, v233
	v_mul_f32_e32 v29, 0x42000000, v29
	v_cvt_pk_fp8_f32 v27, v25, v28 op_sel:[0,0,1]
	v_med3_f32 v25, v34, s33, v233
	v_med3_f32 v31, v36, s33, v233
	v_mov_b32_e32 v28, v1
	v_cvt_pk_fp8_f32 v28, v25, v31
	v_med3_f32 v0, v0, s33, v233
	v_med3_f32 v33, v29, s33, v233
	v_mov_b32_e32 v29, v1
	v_cvt_pk_fp8_f32 v29, v0, v33
	v_med3_f32 v25, v38, s33, v233
	v_med3_f32 v31, v40, s33, v233
	v_cvt_pk_fp8_f32 v28, v25, v31 op_sel:[0,0,1]
	v_med3_f32 v0, v30, s33, v233
	v_med3_f32 v25, v32, s33, v233
	s_mul_i32 s5, s4, 0xfffe8000
	v_cvt_pk_fp8_f32 v29, v0, v25 op_sel:[0,0,1]
	v_add_u32_e32 v25, s5, v24
	v_add_u32_e32 v0, 0xffff8000, v25
	s_movk_i32 s5, 0x7c8
	s_addc_u32 s7, s8, 0
	v_and_or_b32 v0, v0, s5, v3
	v_mov_b32_e32 v43, 0x2000
	v_lshl_add_u64 v[6:7], s[6:7], 0, v[4:5]
	v_lshl_or_b32 v0, v0, 11, v43
	v_lshl_add_u64 v[34:35], v[6:7], 0, v[0:1]
	ds_read2_b32 v[30:31], v19 offset1:32
	global_store_dwordx4 v[34:35], v[26:29], off sc1
	ds_read2_b32 v[26:27], v19 offset0:64 offset1:96
	v_add_u32_e32 v36, 0x400, v19
	ds_read2_b32 v[32:33], v36 offset1:32
	s_waitcnt lgkmcnt(2)
	v_mul_f32_e32 v0, 0x42000000, v30
	ds_read2_b32 v[28:29], v36 offset0:64 offset1:96
	v_mul_f32_e32 v35, 0x42000000, v31
	s_waitcnt lgkmcnt(2)
	v_mul_f32_e32 v38, 0x42000000, v26
	ds_read2_b32 v[30:31], v19 offset0:128 offset1:160
	v_mul_f32_e32 v40, 0x42000000, v27
	ds_read2_b32 v[26:27], v36 offset0:128 offset1:160
	s_waitcnt lgkmcnt(3)
	v_mul_f32_e32 v34, 0x42000000, v32
	v_mul_f32_e32 v37, 0x42000000, v33
	s_waitcnt lgkmcnt(2)
	v_mul_f32_e32 v39, 0x42000000, v28
	v_mul_f32_e32 v41, 0x42000000, v29
	s_waitcnt lgkmcnt(1)
	v_mul_f32_e32 v30, 0x42000000, v30
	ds_read2_b32 v[28:29], v19 offset0:192 offset1:224
	ds_read2_b32 v[32:33], v36 offset0:192 offset1:224
	s_waitcnt lgkmcnt(2)
	v_mul_f32_e32 v36, 0x42000000, v26
	v_mul_f32_e32 v31, 0x42000000, v31
	v_mul_f32_e32 v42, 0x42000000, v27
	v_med3_f32 v0, v0, s33, v233
	v_med3_f32 v27, v35, s33, v233
	v_mov_b32_e32 v26, v1
	v_cvt_pk_fp8_f32 v26, v0, v27
	v_med3_f32 v30, v30, s33, v233
	v_med3_f32 v31, v31, s33, v233
	v_mov_b32_e32 v27, v1
	v_cvt_pk_fp8_f32 v27, v30, v31
	s_waitcnt lgkmcnt(1)
	v_mul_f32_e32 v28, 0x42000000, v28
	v_mul_f32_e32 v29, 0x42000000, v29
	v_med3_f32 v0, v38, s33, v233
	v_med3_f32 v35, v40, s33, v233
	v_cvt_pk_fp8_f32 v26, v0, v35 op_sel:[0,0,1]
	v_med3_f32 v0, v28, s33, v233
	v_med3_f32 v28, v29, s33, v233
	v_cvt_pk_fp8_f32 v27, v0, v28 op_sel:[0,0,1]
	v_med3_f32 v0, v34, s33, v233
	v_med3_f32 v29, v37, s33, v233
	v_mov_b32_e32 v28, v1
	v_cvt_pk_fp8_f32 v28, v0, v29
	v_med3_f32 v31, v36, s33, v233
	v_med3_f32 v34, v42, s33, v233
	v_mov_b32_e32 v29, v1
	v_cvt_pk_fp8_f32 v29, v31, v34
	s_waitcnt lgkmcnt(0)
	v_mul_f32_e32 v32, 0x42000000, v32
	v_mul_f32_e32 v33, 0x42000000, v33
	v_med3_f32 v0, v39, s33, v233
	v_med3_f32 v30, v41, s33, v233
	v_cvt_pk_fp8_f32 v28, v0, v30 op_sel:[0,0,1]
	v_med3_f32 v0, v32, s33, v233
	v_med3_f32 v30, v33, s33, v233
	v_cvt_pk_fp8_f32 v29, v0, v30 op_sel:[0,0,1]
	v_add_u32_e32 v0, 0xffff8010, v25
	s_movk_i32 s5, 0x7d8
	v_and_or_b32 v0, v0, s5, v3
	v_lshl_or_b32 v0, v0, 11, v43
	v_lshl_add_u64 v[34:35], v[6:7], 0, v[0:1]
	ds_read2_b32 v[30:31], v21 offset1:32
	global_store_dwordx4 v[34:35], v[26:29], off sc1
	ds_read2_b32 v[26:27], v21 offset0:64 offset1:96
	v_add_u32_e32 v36, 0x400, v21
	ds_read2_b32 v[32:33], v36 offset1:32
	s_waitcnt lgkmcnt(2)
	v_mul_f32_e32 v0, 0x42000000, v30
	ds_read2_b32 v[28:29], v36 offset0:64 offset1:96
	v_mul_f32_e32 v35, 0x42000000, v31
	s_waitcnt lgkmcnt(2)
	v_mul_f32_e32 v38, 0x42000000, v26
	ds_read2_b32 v[30:31], v21 offset0:128 offset1:160
	v_mul_f32_e32 v40, 0x42000000, v27
	ds_read2_b32 v[26:27], v36 offset0:128 offset1:160
	s_waitcnt lgkmcnt(3)
	v_mul_f32_e32 v34, 0x42000000, v32
	v_mul_f32_e32 v37, 0x42000000, v33
	s_waitcnt lgkmcnt(2)
	v_mul_f32_e32 v39, 0x42000000, v28
	v_mul_f32_e32 v41, 0x42000000, v29
	s_waitcnt lgkmcnt(1)
	v_mul_f32_e32 v30, 0x42000000, v30
	ds_read2_b32 v[28:29], v21 offset0:192 offset1:224
	ds_read2_b32 v[32:33], v36 offset0:192 offset1:224
	s_waitcnt lgkmcnt(2)
	v_mul_f32_e32 v36, 0x42000000, v26
	v_mul_f32_e32 v31, 0x42000000, v31
	v_mul_f32_e32 v42, 0x42000000, v27
	v_med3_f32 v0, v0, s33, v233
	v_med3_f32 v27, v35, s33, v233
	v_mov_b32_e32 v26, v1
	v_cvt_pk_fp8_f32 v26, v0, v27
	v_med3_f32 v30, v30, s33, v233
	v_med3_f32 v31, v31, s33, v233
	v_mov_b32_e32 v27, v1
	v_cvt_pk_fp8_f32 v27, v30, v31
	s_waitcnt lgkmcnt(1)
	v_mul_f32_e32 v28, 0x42000000, v28
	v_mul_f32_e32 v29, 0x42000000, v29
	v_med3_f32 v0, v38, s33, v233
	v_med3_f32 v35, v40, s33, v233
	v_cvt_pk_fp8_f32 v26, v0, v35 op_sel:[0,0,1]
	v_med3_f32 v0, v28, s33, v233
	v_med3_f32 v28, v29, s33, v233
	v_cvt_pk_fp8_f32 v27, v0, v28 op_sel:[0,0,1]
	v_med3_f32 v0, v34, s33, v233
	v_med3_f32 v29, v37, s33, v233
	v_mov_b32_e32 v28, v1
	v_cvt_pk_fp8_f32 v28, v0, v29
	v_med3_f32 v31, v36, s33, v233
	v_med3_f32 v34, v42, s33, v233
	v_mov_b32_e32 v29, v1
	v_cvt_pk_fp8_f32 v29, v31, v34
	s_waitcnt lgkmcnt(0)
	v_mul_f32_e32 v32, 0x42000000, v32
	v_mul_f32_e32 v33, 0x42000000, v33
	v_med3_f32 v0, v39, s33, v233
	v_med3_f32 v30, v41, s33, v233
	v_cvt_pk_fp8_f32 v28, v0, v30 op_sel:[0,0,1]
	v_med3_f32 v0, v32, s33, v233
	v_med3_f32 v30, v33, s33, v233
	v_cvt_pk_fp8_f32 v29, v0, v30 op_sel:[0,0,1]
	v_add_u32_e32 v0, 0xffff8020, v25
	s_movk_i32 s5, 0x7e8
	v_and_or_b32 v0, v0, s5, v3
	v_lshl_or_b32 v0, v0, 11, v43
	v_lshl_add_u64 v[34:35], v[6:7], 0, v[0:1]
	ds_read2_b32 v[30:31], v23 offset1:32
	global_store_dwordx4 v[34:35], v[26:29], off sc1
	ds_read2_b32 v[26:27], v23 offset0:64 offset1:96
	v_add_u32_e32 v36, 0x400, v23
	ds_read2_b32 v[32:33], v36 offset1:32
	s_waitcnt lgkmcnt(2)
	v_mul_f32_e32 v0, 0x42000000, v30
	ds_read2_b32 v[28:29], v36 offset0:64 offset1:96
	v_mul_f32_e32 v35, 0x42000000, v31
	s_waitcnt lgkmcnt(2)
	v_mul_f32_e32 v38, 0x42000000, v26
	ds_read2_b32 v[30:31], v23 offset0:128 offset1:160
	v_mul_f32_e32 v40, 0x42000000, v27
	ds_read2_b32 v[26:27], v36 offset0:128 offset1:160
	s_waitcnt lgkmcnt(3)
	v_mul_f32_e32 v34, 0x42000000, v32
	v_mul_f32_e32 v37, 0x42000000, v33
	s_waitcnt lgkmcnt(2)
	v_mul_f32_e32 v39, 0x42000000, v28
	v_mul_f32_e32 v41, 0x42000000, v29
	s_waitcnt lgkmcnt(1)
	v_mul_f32_e32 v30, 0x42000000, v30
	ds_read2_b32 v[28:29], v23 offset0:192 offset1:224
	ds_read2_b32 v[32:33], v36 offset0:192 offset1:224
	s_waitcnt lgkmcnt(2)
	v_mul_f32_e32 v36, 0x42000000, v26
	v_mul_f32_e32 v31, 0x42000000, v31
	v_mul_f32_e32 v42, 0x42000000, v27
	v_med3_f32 v0, v0, s33, v233
	v_med3_f32 v27, v35, s33, v233
	v_mov_b32_e32 v26, v1
	v_cvt_pk_fp8_f32 v26, v0, v27
	v_med3_f32 v30, v30, s33, v233
	v_med3_f32 v31, v31, s33, v233
	v_mov_b32_e32 v27, v1
	v_cvt_pk_fp8_f32 v27, v30, v31
	s_waitcnt lgkmcnt(1)
	v_mul_f32_e32 v28, 0x42000000, v28
	v_mul_f32_e32 v29, 0x42000000, v29
	v_med3_f32 v0, v38, s33, v233
	v_med3_f32 v35, v40, s33, v233
	v_cvt_pk_fp8_f32 v26, v0, v35 op_sel:[0,0,1]
	v_med3_f32 v0, v28, s33, v233
	v_med3_f32 v28, v29, s33, v233
	v_cvt_pk_fp8_f32 v27, v0, v28 op_sel:[0,0,1]
	v_med3_f32 v0, v34, s33, v233
	v_med3_f32 v29, v37, s33, v233
	v_mov_b32_e32 v28, v1
	v_cvt_pk_fp8_f32 v28, v0, v29
	v_med3_f32 v31, v36, s33, v233
	v_med3_f32 v34, v42, s33, v233
	v_mov_b32_e32 v29, v1
	v_cvt_pk_fp8_f32 v29, v31, v34
	s_waitcnt lgkmcnt(0)
	v_mul_f32_e32 v32, 0x42000000, v32
	v_mul_f32_e32 v33, 0x42000000, v33
	v_med3_f32 v0, v39, s33, v233
	v_med3_f32 v30, v41, s33, v233
	v_cvt_pk_fp8_f32 v28, v0, v30 op_sel:[0,0,1]
	v_med3_f32 v0, v32, s33, v233
	v_med3_f32 v30, v33, s33, v233
	v_cvt_pk_fp8_f32 v29, v0, v30 op_sel:[0,0,1]
	v_add_u32_e32 v0, 0xffff8030, v25
	s_movk_i32 s5, 0x7f8
	v_and_or_b32 v0, v0, s5, v3
	v_lshl_or_b32 v0, v0, 11, v43
	v_lshl_add_u64 v[6:7], v[6:7], 0, v[0:1]
	global_store_dwordx4 v[6:7], v[26:29], off sc1
	s_waitcnt lgkmcnt(0)

.LBB0_266:
	s_andn2_b64 vcc, exec, s[6:7]
	s_cbranch_vccnz .LBB0_259
	s_ashr_i32 s5, s4, 31
	s_lshl_b64 s[6:7], s[4:5], 23
	s_add_u32 s6, s38, s6
	s_addc_u32 s7, s39, s7
	s_lshl_b64 s[4:5], s[4:5], 22
	s_add_u32 s8, s24, s4
	s_addc_u32 s9, s25, s5
	s_bfe_u32 s4, s55, 0x5001a
	s_add_i32 s4, s55, s4
	s_sext_i32_i16 s5, s4
	s_lshl_b32 s5, s5, 2
	s_and_b32 s4, s4, 0xffe0
	s_and_b32 s20, s5, 0xffffff80
	s_sub_i32 s4, s55, s4
	v_or_b32_e32 v6, s20, v3
	s_sext_i32_i16 s4, s4
	v_ashrrev_i32_e32 v7, 31, v6
	s_lshl_b32 s4, s4, 5
	v_lshlrev_b64 v[6:7], 12, v[6:7]
	v_lshl_add_u64 v[6:7], s[6:7], 0, v[6:7]
	s_ashr_i32 s5, s4, 31
	v_lshl_add_u64 v[6:7], s[4:5], 2, v[6:7]
	v_lshlrev_b32_e32 v0, 2, v2
	v_lshl_add_u64 v[6:7], v[6:7], 0, v[0:1]
	s_mov_b32 s5, 0x8000
	v_add_co_u32_e32 v30, vcc, s5, v6
	s_mov_b32 s5, 0x10000
	s_nop 0
	v_addc_co_u32_e32 v31, vcc, 0, v7, vcc
	v_add_co_u32_e32 v34, vcc, s5, v6
	s_mov_b32 s5, 0x18000
	s_nop 0
	v_addc_co_u32_e32 v35, vcc, 0, v7, vcc
	v_add_co_u32_e32 v38, vcc, s5, v6
	s_mov_b32 s5, 0x20000
	s_nop 0
	v_addc_co_u32_e32 v39, vcc, 0, v7, vcc
	v_add_co_u32_e32 v42, vcc, s5, v6
	s_mov_b32 s5, 0x28000
	s_nop 0
	v_addc_co_u32_e32 v43, vcc, 0, v7, vcc
	v_add_co_u32_e32 v46, vcc, s5, v6
	s_mov_b32 s5, 0x30000
	s_nop 0
	v_addc_co_u32_e32 v47, vcc, 0, v7, vcc
	v_add_co_u32_e32 v50, vcc, s5, v6
	s_mov_b32 s5, 0x38000
	s_nop 0
	v_addc_co_u32_e32 v51, vcc, 0, v7, vcc
	v_add_co_u32_e32 v54, vcc, s5, v6
	s_mov_b32 s5, 0x40000
	s_nop 0
	v_addc_co_u32_e32 v55, vcc, 0, v7, vcc
	v_add_co_u32_e32 v58, vcc, s5, v6
	s_mov_b32 s5, 0x48000
	s_nop 0
	v_addc_co_u32_e32 v59, vcc, 0, v7, vcc
	v_add_co_u32_e32 v62, vcc, s5, v6
	s_mov_b32 s5, 0x50000
	s_nop 0
	v_addc_co_u32_e32 v63, vcc, 0, v7, vcc
	v_add_co_u32_e32 v68, vcc, s5, v6
	s_mov_b32 s5, 0x58000
	s_nop 0
	v_addc_co_u32_e32 v69, vcc, 0, v7, vcc
	v_add_co_u32_e32 v72, vcc, s5, v6
	s_mov_b32 s5, 0x60000
	s_nop 0
	v_addc_co_u32_e32 v73, vcc, 0, v7, vcc
	global_load_dwordx4 v[26:29], v[6:7], off nt
	s_nop 0
	global_load_dwordx4 v[30:33], v[30:31], off nt
	v_add_co_u32_e32 v76, vcc, s5, v6
	global_load_dwordx4 v[34:37], v[34:35], off nt
	s_nop 0
	global_load_dwordx4 v[38:41], v[38:39], off nt
	v_addc_co_u32_e32 v77, vcc, 0, v7, vcc
	s_mov_b32 s5, 0x68000
	global_load_dwordx4 v[42:45], v[42:43], off nt
	s_nop 0
	global_load_dwordx4 v[46:49], v[46:47], off nt
	v_add_co_u32_e32 v80, vcc, s5, v6
	global_load_dwordx4 v[50:53], v[50:51], off nt
	s_nop 0
	global_load_dwordx4 v[54:57], v[54:55], off nt
	v_addc_co_u32_e32 v81, vcc, 0, v7, vcc
	s_mov_b32 s5, 0x70000
	global_load_dwordx4 v[58:61], v[58:59], off nt
	s_nop 0
	global_load_dwordx4 v[62:65], v[62:63], off nt
	v_add_co_u32_e32 v84, vcc, s5, v6
	global_load_dwordx4 v[68:71], v[68:69], off nt
	s_nop 0
	global_load_dwordx4 v[72:75], v[72:73], off nt
	v_addc_co_u32_e32 v85, vcc, 0, v7, vcc
	s_mov_b32 s5, 0x78000
	global_load_dwordx4 v[76:79], v[76:77], off nt
	s_nop 0
	global_load_dwordx4 v[80:83], v[80:81], off nt
	v_add_co_u32_e32 v6, vcc, s5, v6
	v_add_u32_e32 v0, v8, v4
	s_nop 0
	v_addc_co_u32_e32 v7, vcc, 0, v7, vcc
	global_load_dwordx4 v[84:87], v[84:85], off nt
	s_nop 0
	global_load_dwordx4 v[88:91], v[6:7], off nt
	s_waitcnt vmcnt(0)
	ds_write_b128 v0, v[26:29]
	s_waitcnt vmcnt(14)
	ds_write_b128 v0, v[30:33] offset:1024
	v_add_u32_e32 v0, v8, v9
	s_waitcnt vmcnt(13)
	ds_write_b128 v0, v[34:37] offset:2048
	s_waitcnt vmcnt(12)
	ds_write_b128 v0, v[38:41] offset:3072
	v_add_u32_e32 v0, v8, v10
	s_waitcnt vmcnt(11)
	ds_write_b128 v0, v[42:45] offset:4096
	s_waitcnt vmcnt(10)
	ds_write_b128 v0, v[46:49] offset:5120
	v_add_u32_e32 v0, v8, v11
	s_waitcnt vmcnt(9)
	ds_write_b128 v0, v[50:53] offset:6144
	s_waitcnt vmcnt(8)
	ds_write_b128 v0, v[54:57] offset:7168
	v_add_u32_e32 v0, v8, v12
	s_waitcnt vmcnt(7)
	ds_write_b128 v0, v[58:61] offset:8192
	s_waitcnt vmcnt(6)
	ds_write_b128 v0, v[62:65] offset:9216
	v_add_u32_e32 v0, v8, v13
	s_waitcnt vmcnt(5)
	ds_write_b128 v0, v[68:71] offset:10240
	s_waitcnt vmcnt(4)
	ds_write_b128 v0, v[72:75] offset:11264
	v_add_u32_e32 v0, v8, v14
	s_waitcnt vmcnt(3)
	ds_write_b128 v0, v[76:79] offset:12288
	s_waitcnt vmcnt(2)
	ds_write_b128 v0, v[80:83] offset:13312
	v_add_u32_e32 v0, v8, v15
	s_waitcnt vmcnt(1)
	ds_write_b128 v0, v[84:87] offset:14336
	s_waitcnt vmcnt(0)
	ds_write_b128 v0, v[88:91] offset:15360
	s_waitcnt lgkmcnt(0)
	v_add_u32_e32 v0, 0x400, v17
	ds_read2_b32 v[26:27], v17 offset1:32
	ds_read2_b32 v[28:29], v0 offset1:32
	ds_read2_b32 v[30:31], v17 offset0:64 offset1:96
	ds_read2_b32 v[32:33], v0 offset0:64 offset1:96
	s_ashr_i32 s5, s20, 31
	s_waitcnt lgkmcnt(3)
	v_mul_f32_e32 v25, 0x42000000, v26
	s_waitcnt lgkmcnt(2)
	v_mul_f32_e32 v34, 0x42000000, v28
	v_mul_f32_e32 v35, 0x42000000, v27
	v_mul_f32_e32 v36, 0x42000000, v29
	s_waitcnt lgkmcnt(1)
	v_mul_f32_e32 v37, 0x42000000, v30
	ds_read2_b32 v[26:27], v17 offset0:128 offset1:160
	s_waitcnt lgkmcnt(1)
	v_mul_f32_e32 v38, 0x42000000, v32
	v_mul_f32_e32 v39, 0x42000000, v31
	ds_read2_b32 v[28:29], v0 offset0:128 offset1:160
	v_mul_f32_e32 v40, 0x42000000, v33
	ds_read2_b32 v[30:31], v17 offset0:192 offset1:224
	ds_read2_b32 v[32:33], v0 offset0:192 offset1:224
	s_waitcnt lgkmcnt(3)
	v_mul_f32_e32 v41, 0x42000000, v26
	v_mul_f32_e32 v27, 0x42000000, v27
	s_waitcnt lgkmcnt(2)
	v_mul_f32_e32 v0, 0x42000000, v28
	s_waitcnt lgkmcnt(1)
	v_mul_f32_e32 v28, 0x42000000, v30
	s_waitcnt lgkmcnt(0)
	v_mul_f32_e32 v30, 0x42000000, v32
	v_mul_f32_e32 v32, 0x42000000, v33
	v_med3_f32 v25, v25, s33, v233
	v_med3_f32 v33, v35, s33, v233
	v_mov_b32_e32 v26, v1
	v_cvt_pk_fp8_f32 v26, v25, v33
	v_med3_f32 v25, v37, s33, v233
	v_med3_f32 v35, v41, s33, v233
	v_med3_f32 v37, v27, s33, v233
	v_mov_b32_e32 v27, v1
	v_cvt_pk_fp8_f32 v27, v35, v37
	v_mul_f32_e32 v31, 0x42000000, v31
	v_med3_f32 v33, v39, s33, v233
	v_cvt_pk_fp8_f32 v26, v25, v33 op_sel:[0,0,1]
	v_med3_f32 v25, v28, s33, v233
	v_med3_f32 v28, v31, s33, v233
	v_mul_f32_e32 v29, 0x42000000, v29
	v_cvt_pk_fp8_f32 v27, v25, v28 op_sel:[0,0,1]
	v_med3_f32 v25, v34, s33, v233
	v_med3_f32 v31, v36, s33, v233
	v_mov_b32_e32 v28, v1
	v_cvt_pk_fp8_f32 v28, v25, v31
	v_med3_f32 v0, v0, s33, v233
	v_med3_f32 v33, v29, s33, v233
	v_mov_b32_e32 v29, v1
	v_cvt_pk_fp8_f32 v29, v0, v33
	v_med3_f32 v25, v38, s33, v233
	v_med3_f32 v31, v40, s33, v233
	v_cvt_pk_fp8_f32 v28, v25, v31 op_sel:[0,0,1]
	v_med3_f32 v0, v30, s33, v233
	v_med3_f32 v25, v32, s33, v233
	s_add_u32 s6, s8, s20
	v_cvt_pk_fp8_f32 v29, v0, v25 op_sel:[0,0,1]
	v_or_b32_e32 v0, s4, v3
	s_addc_u32 s7, s9, s5
	v_lshlrev_b32_e32 v0, 1, v0
	s_movk_i32 s5, 0xffc8
	v_and_or_b32 v30, v0, s5, v16
	v_ashrrev_i32_e32 v31, 31, v30
	v_lshl_add_u64 v[6:7], s[6:7], 0, v[4:5]
	v_lshlrev_b64 v[30:31], 11, v[30:31]
	v_lshl_add_u64 v[30:31], v[6:7], 0, v[30:31]
	global_store_dwordx4 v[30:31], v[26:29], off sc1
	ds_read2_b32 v[26:27], v19 offset0:64 offset1:96
	ds_read2_b32 v[32:33], v19 offset1:32
	v_add_u32_e32 v0, 0x400, v19
	ds_read2_b32 v[28:29], v0 offset0:64 offset1:96
	ds_read2_b32 v[30:31], v19 offset0:128 offset1:160
	s_waitcnt lgkmcnt(3)
	v_mul_f32_e32 v37, 0x42000000, v26
	v_mul_f32_e32 v39, 0x42000000, v27
	ds_read2_b32 v[26:27], v0 offset0:128 offset1:160
	s_waitcnt lgkmcnt(3)
	v_mul_f32_e32 v25, 0x42000000, v32
	v_mul_f32_e32 v36, 0x42000000, v33
	ds_read2_b32 v[34:35], v0 offset1:32
	s_waitcnt lgkmcnt(3)
	v_mul_f32_e32 v38, 0x42000000, v28
	v_mul_f32_e32 v40, 0x42000000, v29
	s_waitcnt lgkmcnt(2)
	v_mul_f32_e32 v30, 0x42000000, v30
	ds_read2_b32 v[28:29], v19 offset0:192 offset1:224
	ds_read2_b32 v[32:33], v0 offset0:192 offset1:224
	s_waitcnt lgkmcnt(3)
	v_mul_f32_e32 v0, 0x42000000, v26
	v_mul_f32_e32 v31, 0x42000000, v31
	v_mul_f32_e32 v41, 0x42000000, v27
	v_med3_f32 v25, v25, s33, v233
	v_med3_f32 v27, v36, s33, v233
	v_mov_b32_e32 v26, v1
	v_cvt_pk_fp8_f32 v26, v25, v27
	v_med3_f32 v30, v30, s33, v233
	v_med3_f32 v31, v31, s33, v233
	v_mov_b32_e32 v27, v1
	v_cvt_pk_fp8_f32 v27, v30, v31
	s_waitcnt lgkmcnt(1)
	v_mul_f32_e32 v28, 0x42000000, v28
	v_mul_f32_e32 v29, 0x42000000, v29
	v_med3_f32 v25, v37, s33, v233
	v_med3_f32 v36, v39, s33, v233
	v_mul_f32_e32 v34, 0x42000000, v34
	v_mul_f32_e32 v35, 0x42000000, v35
	v_cvt_pk_fp8_f32 v26, v25, v36 op_sel:[0,0,1]
	v_med3_f32 v25, v28, s33, v233
	v_med3_f32 v28, v29, s33, v233
	v_cvt_pk_fp8_f32 v27, v25, v28 op_sel:[0,0,1]
	v_med3_f32 v25, v34, s33, v233
	v_med3_f32 v29, v35, s33, v233
	v_mov_b32_e32 v28, v1
	v_cvt_pk_fp8_f32 v28, v25, v29
	v_med3_f32 v0, v0, s33, v233
	v_med3_f32 v31, v41, s33, v233
	v_mov_b32_e32 v29, v1
	v_cvt_pk_fp8_f32 v29, v0, v31
	s_waitcnt lgkmcnt(0)
	v_mul_f32_e32 v32, 0x42000000, v32
	v_mul_f32_e32 v33, 0x42000000, v33
	v_med3_f32 v25, v38, s33, v233
	v_med3_f32 v30, v40, s33, v233
	v_cvt_pk_fp8_f32 v28, v25, v30 op_sel:[0,0,1]
	v_med3_f32 v0, v32, s33, v233
	v_med3_f32 v25, v33, s33, v233
	v_cvt_pk_fp8_f32 v29, v0, v25 op_sel:[0,0,1]
	v_or_b32_e32 v0, s4, v18
	v_lshlrev_b32_e32 v0, 1, v0
	s_movk_i32 s5, 0xffd8
	v_and_or_b32 v30, v0, s5, v16
	v_ashrrev_i32_e32 v31, 31, v30
	v_lshlrev_b64 v[30:31], 11, v[30:31]
	v_lshl_add_u64 v[30:31], v[6:7], 0, v[30:31]
	global_store_dwordx4 v[30:31], v[26:29], off sc1
	ds_read2_b32 v[26:27], v21 offset0:64 offset1:96
	ds_read2_b32 v[32:33], v21 offset1:32
	v_add_u32_e32 v0, 0x400, v21
	ds_read2_b32 v[28:29], v0 offset0:64 offset1:96
	ds_read2_b32 v[30:31], v21 offset0:128 offset1:160
	s_waitcnt lgkmcnt(3)
	v_mul_f32_e32 v37, 0x42000000, v26
	v_mul_f32_e32 v39, 0x42000000, v27
	ds_read2_b32 v[26:27], v0 offset0:128 offset1:160
	s_waitcnt lgkmcnt(3)
	v_mul_f32_e32 v25, 0x42000000, v32
	v_mul_f32_e32 v36, 0x42000000, v33
	ds_read2_b32 v[34:35], v0 offset1:32
	s_waitcnt lgkmcnt(3)
	v_mul_f32_e32 v38, 0x42000000, v28
	v_mul_f32_e32 v40, 0x42000000, v29
	s_waitcnt lgkmcnt(2)
	v_mul_f32_e32 v30, 0x42000000, v30
	ds_read2_b32 v[28:29], v21 offset0:192 offset1:224
	ds_read2_b32 v[32:33], v0 offset0:192 offset1:224
	s_waitcnt lgkmcnt(3)
	v_mul_f32_e32 v0, 0x42000000, v26
	v_mul_f32_e32 v31, 0x42000000, v31
	v_mul_f32_e32 v41, 0x42000000, v27
	v_med3_f32 v25, v25, s33, v233
	v_med3_f32 v27, v36, s33, v233
	v_mov_b32_e32 v26, v1
	v_cvt_pk_fp8_f32 v26, v25, v27
	v_med3_f32 v30, v30, s33, v233
	v_med3_f32 v31, v31, s33, v233
	v_mov_b32_e32 v27, v1
	v_cvt_pk_fp8_f32 v27, v30, v31
	s_waitcnt lgkmcnt(1)
	v_mul_f32_e32 v28, 0x42000000, v28
	v_mul_f32_e32 v29, 0x42000000, v29
	v_med3_f32 v25, v37, s33, v233
	v_med3_f32 v36, v39, s33, v233
	v_mul_f32_e32 v34, 0x42000000, v34
	v_mul_f32_e32 v35, 0x42000000, v35
	v_cvt_pk_fp8_f32 v26, v25, v36 op_sel:[0,0,1]
	v_med3_f32 v25, v28, s33, v233
	v_med3_f32 v28, v29, s33, v233
	v_cvt_pk_fp8_f32 v27, v25, v28 op_sel:[0,0,1]
	v_med3_f32 v25, v34, s33, v233
	v_med3_f32 v29, v35, s33, v233
	v_mov_b32_e32 v28, v1
	v_cvt_pk_fp8_f32 v28, v25, v29
	v_med3_f32 v0, v0, s33, v233
	v_med3_f32 v31, v41, s33, v233
	v_mov_b32_e32 v29, v1
	v_cvt_pk_fp8_f32 v29, v0, v31
	s_waitcnt lgkmcnt(0)
	v_mul_f32_e32 v32, 0x42000000, v32
	v_mul_f32_e32 v33, 0x42000000, v33
	v_med3_f32 v25, v38, s33, v233
	v_med3_f32 v30, v40, s33, v233
	v_cvt_pk_fp8_f32 v28, v25, v30 op_sel:[0,0,1]
	v_med3_f32 v0, v32, s33, v233
	v_med3_f32 v25, v33, s33, v233
	v_cvt_pk_fp8_f32 v29, v0, v25 op_sel:[0,0,1]
	v_or_b32_e32 v0, s4, v20
	v_lshlrev_b32_e32 v0, 1, v0
	s_movk_i32 s5, 0xffe8
	v_and_or_b32 v30, v0, s5, v16
	v_ashrrev_i32_e32 v31, 31, v30
	v_lshlrev_b64 v[30:31], 11, v[30:31]
	v_lshl_add_u64 v[30:31], v[6:7], 0, v[30:31]
	global_store_dwordx4 v[30:31], v[26:29], off sc1
	ds_read2_b32 v[26:27], v23 offset0:64 offset1:96
	ds_read2_b32 v[32:33], v23 offset1:32
	v_add_u32_e32 v0, 0x400, v23
	ds_read2_b32 v[28:29], v0 offset0:64 offset1:96
	ds_read2_b32 v[30:31], v23 offset0:128 offset1:160
	s_waitcnt lgkmcnt(3)
	v_mul_f32_e32 v37, 0x42000000, v26
	v_mul_f32_e32 v39, 0x42000000, v27
	ds_read2_b32 v[26:27], v0 offset0:128 offset1:160
	s_waitcnt lgkmcnt(3)
	v_mul_f32_e32 v25, 0x42000000, v32
	v_mul_f32_e32 v36, 0x42000000, v33
	ds_read2_b32 v[34:35], v0 offset1:32
	s_waitcnt lgkmcnt(3)
	v_mul_f32_e32 v38, 0x42000000, v28
	v_mul_f32_e32 v40, 0x42000000, v29
	s_waitcnt lgkmcnt(2)
	v_mul_f32_e32 v30, 0x42000000, v30
	ds_read2_b32 v[28:29], v23 offset0:192 offset1:224
	ds_read2_b32 v[32:33], v0 offset0:192 offset1:224
	s_waitcnt lgkmcnt(3)
	v_mul_f32_e32 v0, 0x42000000, v26
	v_mul_f32_e32 v31, 0x42000000, v31
	v_mul_f32_e32 v41, 0x42000000, v27
	v_med3_f32 v25, v25, s33, v233
	v_med3_f32 v27, v36, s33, v233
	v_mov_b32_e32 v26, v1
	v_cvt_pk_fp8_f32 v26, v25, v27
	v_med3_f32 v30, v30, s33, v233
	v_med3_f32 v31, v31, s33, v233
	v_mov_b32_e32 v27, v1
	v_cvt_pk_fp8_f32 v27, v30, v31
	s_waitcnt lgkmcnt(1)
	v_mul_f32_e32 v28, 0x42000000, v28
	v_mul_f32_e32 v29, 0x42000000, v29
	v_med3_f32 v25, v37, s33, v233
	v_med3_f32 v36, v39, s33, v233
	v_mul_f32_e32 v34, 0x42000000, v34
	v_mul_f32_e32 v35, 0x42000000, v35
	v_cvt_pk_fp8_f32 v26, v25, v36 op_sel:[0,0,1]
	v_med3_f32 v25, v28, s33, v233
	v_med3_f32 v28, v29, s33, v233
	v_cvt_pk_fp8_f32 v27, v25, v28 op_sel:[0,0,1]
	v_med3_f32 v25, v34, s33, v233
	v_med3_f32 v29, v35, s33, v233
	v_mov_b32_e32 v28, v1
	v_cvt_pk_fp8_f32 v28, v25, v29
	v_med3_f32 v0, v0, s33, v233
	v_med3_f32 v31, v41, s33, v233
	v_mov_b32_e32 v29, v1
	v_cvt_pk_fp8_f32 v29, v0, v31
	s_waitcnt lgkmcnt(0)
	v_mul_f32_e32 v32, 0x42000000, v32
	v_mul_f32_e32 v33, 0x42000000, v33
	v_med3_f32 v25, v38, s33, v233
	v_med3_f32 v30, v40, s33, v233
	v_cvt_pk_fp8_f32 v28, v25, v30 op_sel:[0,0,1]
	v_med3_f32 v0, v32, s33, v233
	v_med3_f32 v25, v33, s33, v233
	v_cvt_pk_fp8_f32 v29, v0, v25 op_sel:[0,0,1]
	v_or_b32_e32 v0, s4, v22
	v_lshlrev_b32_e32 v0, 1, v0
	v_and_or_b32 v30, v0, -8, v16
	v_ashrrev_i32_e32 v31, 31, v30
	v_lshlrev_b64 v[30:31], 11, v[30:31]
	v_lshl_add_u64 v[6:7], v[6:7], 0, v[30:31]
	global_store_dwordx4 v[6:7], v[26:29], off sc1
	s_waitcnt lgkmcnt(0)
	s_branch .LBB0_259

.LBB0_274:
	v_add_co_u32_e32 v34, vcc, 0xfffff000, v108
	s_add_i32 s24, s24, s66
	s_nop 0
	v_addc_co_u32_e32 v35, vcc, -1, v109, vcc
	global_load_dwordx4 v[126:129], v[34:35], off offset:-3072 nt
	global_load_dwordx4 v[58:61], v[34:35], off offset:-2048 nt
	global_load_dwordx4 v[54:57], v[34:35], off offset:-1024 nt
	global_load_dwordx4 v[50:53], v[108:109], off offset:-4096 nt
	global_load_dwordx4 v[46:49], v[108:109], off offset:-3072 nt
	global_load_dwordx4 v[42:45], v[108:109], off offset:-2048 nt
	global_load_dwordx4 v[38:41], v[108:109], off offset:-1024 nt
	s_nop 0
	global_load_dwordx4 v[34:37], v[108:109], off nt
	v_lshl_add_u64 v[108:109], v[108:109], 0, s[28:29]
	s_cmp_ge_i32 s24, s25
	s_waitcnt vmcnt(7)
	v_mul_f32_e32 v110, v127, v127
	v_mul_f32_e32 v112, v129, v129
	v_fmac_f32_e32 v110, v126, v126
	v_fmac_f32_e32 v112, v128, v128
	v_add_f32_e32 v110, v110, v112
	s_waitcnt vmcnt(6)
	v_mul_f32_e32 v112, v59, v59
	v_mul_f32_e32 v113, v61, v61
	v_fmac_f32_e32 v112, v58, v58
	v_fmac_f32_e32 v113, v60, v60
	v_add_f32_e32 v112, v112, v113
	v_add_f32_e32 v110, v110, v112
	s_waitcnt vmcnt(5)
	v_mul_f32_e32 v112, v55, v55
	v_mul_f32_e32 v113, v57, v57
	v_fmac_f32_e32 v112, v54, v54
	v_fmac_f32_e32 v113, v56, v56
	v_add_f32_e32 v112, v112, v113
	v_add_f32_e32 v110, v110, v112
	s_waitcnt vmcnt(4)
	v_mul_f32_e32 v112, v51, v51
	v_mul_f32_e32 v113, v53, v53
	v_fmac_f32_e32 v112, v50, v50
	v_fmac_f32_e32 v113, v52, v52
	v_add_f32_e32 v112, v112, v113
	v_add_f32_e32 v110, v110, v112
	s_waitcnt vmcnt(3)
	v_mul_f32_e32 v112, v47, v47
	v_mul_f32_e32 v113, v49, v49
	v_fmac_f32_e32 v112, v46, v46
	v_fmac_f32_e32 v113, v48, v48
	v_add_f32_e32 v112, v112, v113
	v_add_f32_e32 v110, v110, v112
	s_waitcnt vmcnt(2)
	v_mul_f32_e32 v112, v43, v43
	v_mul_f32_e32 v113, v45, v45
	v_fmac_f32_e32 v112, v42, v42
	v_fmac_f32_e32 v113, v44, v44
	v_add_f32_e32 v112, v112, v113
	v_add_f32_e32 v110, v110, v112
	s_waitcnt vmcnt(1)
	v_mul_f32_e32 v112, v39, v39
	v_mul_f32_e32 v113, v41, v41
	v_fmac_f32_e32 v112, v38, v38
	v_fmac_f32_e32 v113, v40, v40
	v_add_f32_e32 v112, v112, v113
	v_add_f32_e32 v110, v110, v112
	s_waitcnt vmcnt(0)
	v_mul_f32_e32 v112, v35, v35
	v_mul_f32_e32 v113, v37, v37
	v_fmac_f32_e32 v112, v34, v34
	v_fmac_f32_e32 v113, v36, v36
	v_add_f32_e32 v112, v112, v113
	v_add_f32_e32 v110, v110, v112
	ds_bpermute_b32 v112, v121, v110
	s_waitcnt lgkmcnt(0)
	v_add_f32_e32 v110, v110, v112
	ds_bpermute_b32 v112, v122, v110
	s_waitcnt lgkmcnt(0)
	v_add_f32_e32 v110, v110, v112
	ds_bpermute_b32 v112, v123, v110
	s_waitcnt lgkmcnt(0)
	v_add_f32_e32 v110, v110, v112
	ds_bpermute_b32 v112, v124, v110
	s_waitcnt lgkmcnt(0)
	v_add_f32_e32 v110, v110, v112
	v_mov_b32_e32 v112, v110
	s_nop 1
	v_permlane16_swap_b32_e32 v110, v112
	v_add_f32_e32 v110, v110, v112
	v_mov_b32_e32 v112, v110
	s_nop 1
	v_permlane32_swap_b32_e32 v110, v112
	v_add_f32_e32 v110, v110, v112
	v_fmamk_f32 v110, v110, 0x3a000000, v228
	v_cmp_gt_f32_e32 vcc, s82, v110
	v_mul_f32_e32 v112, 0x4f800000, v110
	s_nop 0
	v_cndmask_b32_e32 v110, v110, v112, vcc
	v_sqrt_f32_e32 v112, v110
	s_nop 0
	v_add_u32_e32 v113, -1, v112
	v_fma_f32 v125, -v113, v112, v110
	v_cmp_ge_f32_e64 s[38:39], 0, v125
	v_add_u32_e32 v125, 1, v112
	s_nop 0
	v_cndmask_b32_e64 v113, v112, v113, s[38:39]
	v_fma_f32 v112, -v125, v112, v110
	v_cmp_lt_f32_e64 s[38:39], 0, v112
	s_nop 1
	v_cndmask_b32_e64 v112, v113, v125, s[38:39]
	v_mul_f32_e32 v113, 0x37800000, v112
	v_cndmask_b32_e32 v112, v112, v113, vcc
	v_cmp_class_f32_e32 vcc, v110, v229
	s_nop 1
	v_cndmask_b32_e32 v110, v112, v110, vcc
	v_div_scale_f32 v112, s[4:5], v110, v110, 1.0
	v_rcp_f32_e32 v113, v112
	s_nop 0
	v_fma_f32 v125, -v112, v113, 1.0
	v_fmac_f32_e32 v113, v125, v113
	v_div_scale_f32 v125, vcc, 1.0, v110, 1.0
	v_mul_f32_e32 v130, v125, v113
	v_fma_f32 v131, -v112, v130, v125
	v_fmac_f32_e32 v130, v131, v113
	v_fma_f32 v112, -v112, v130, v125
	v_div_fmas_f32 v112, v112, v113, v130
	v_div_fixup_f32 v110, v112, v110, 1.0
	v_pk_mul_f32 v[126:127], v[126:127], v[110:111] op_sel_hi:[1,0]
	v_pk_mul_f32 v[112:113], v[128:129], v[110:111] op_sel_hi:[1,0]
	v_pk_fma_f32 v[126:127], v[78:79], v[126:127], v[2:3]
	v_pk_fma_f32 v[112:113], v[76:77], v[112:113], v[4:5]
	v_med3_f32 v125, v126, s33, v233
	v_med3_f32 v126, v127, s33, v233
	v_mov_b32_e32 v127, 0
	v_cvt_pk_fp8_f32 v127, v125, v126
	v_pk_mul_f32 v[58:59], v[58:59], v[110:111] op_sel_hi:[1,0]
	v_med3_f32 v112, v112, s33, v233
	v_med3_f32 v113, v113, s33, v233
	v_pk_fma_f32 v[58:59], v[82:83], v[58:59], v[6:7]
	v_cvt_pk_fp8_f32 v127, v112, v113 op_sel:[0,0,1]
	v_med3_f32 v58, v58, s33, v233
	v_med3_f32 v59, v59, s33, v233
	v_mov_b32_e32 v112, 0
	v_cvt_pk_fp8_f32 v112, v58, v59
	v_pk_mul_f32 v[60:61], v[60:61], v[110:111] op_sel_hi:[1,0]
	v_pk_mul_f32 v[54:55], v[54:55], v[110:111] op_sel_hi:[1,0]
	v_pk_fma_f32 v[60:61], v[80:81], v[60:61], v[8:9]
	v_pk_fma_f32 v[54:55], v[86:87], v[54:55], v[10:11]
	v_med3_f32 v58, v60, s33, v233
	v_med3_f32 v59, v61, s33, v233
	v_cvt_pk_fp8_f32 v112, v58, v59 op_sel:[0,0,1]
	v_med3_f32 v54, v54, s33, v233
	v_med3_f32 v55, v55, s33, v233
	v_mov_b32_e32 v58, 0
	v_cvt_pk_fp8_f32 v58, v54, v55
	v_pk_mul_f32 v[56:57], v[56:57], v[110:111] op_sel_hi:[1,0]
	v_pk_mul_f32 v[50:51], v[50:51], v[110:111] op_sel_hi:[1,0]
	v_pk_fma_f32 v[56:57], v[84:85], v[56:57], v[12:13]
	v_pk_fma_f32 v[50:51], v[90:91], v[50:51], v[14:15]
	v_med3_f32 v54, v56, s33, v233
	v_med3_f32 v55, v57, s33, v233
	v_cvt_pk_fp8_f32 v58, v54, v55 op_sel:[0,0,1]
	v_med3_f32 v50, v50, s33, v233
	v_med3_f32 v51, v51, s33, v233
	v_mov_b32_e32 v54, 0
	v_cvt_pk_fp8_f32 v54, v50, v51
	v_pk_mul_f32 v[52:53], v[52:53], v[110:111] op_sel_hi:[1,0]
	v_pk_mul_f32 v[46:47], v[46:47], v[110:111] op_sel_hi:[1,0]
	v_pk_fma_f32 v[52:53], v[88:89], v[52:53], v[16:17]
	v_pk_fma_f32 v[46:47], v[94:95], v[46:47], v[18:19]
	v_med3_f32 v50, v52, s33, v233
	v_med3_f32 v51, v53, s33, v233
	v_cvt_pk_fp8_f32 v54, v50, v51 op_sel:[0,0,1]
	v_med3_f32 v46, v46, s33, v233
	v_med3_f32 v47, v47, s33, v233
	v_mov_b32_e32 v50, 0
	v_cvt_pk_fp8_f32 v50, v46, v47
	v_pk_mul_f32 v[48:49], v[48:49], v[110:111] op_sel_hi:[1,0]
	v_pk_mul_f32 v[42:43], v[42:43], v[110:111] op_sel_hi:[1,0]
	v_pk_fma_f32 v[48:49], v[92:93], v[48:49], v[20:21]
	v_pk_fma_f32 v[42:43], v[98:99], v[42:43], v[22:23]
	v_med3_f32 v46, v48, s33, v233
	v_med3_f32 v47, v49, s33, v233
	v_cvt_pk_fp8_f32 v50, v46, v47 op_sel:[0,0,1]
	v_med3_f32 v42, v42, s33, v233
	v_med3_f32 v43, v43, s33, v233
	v_mov_b32_e32 v46, 0
	v_cvt_pk_fp8_f32 v46, v42, v43
	v_pk_mul_f32 v[44:45], v[44:45], v[110:111] op_sel_hi:[1,0]
	v_pk_mul_f32 v[38:39], v[38:39], v[110:111] op_sel_hi:[1,0]
	v_pk_fma_f32 v[44:45], v[96:97], v[44:45], v[24:25]
	v_pk_fma_f32 v[38:39], v[102:103], v[38:39], v[26:27]
	v_med3_f32 v42, v44, s33, v233
	v_med3_f32 v43, v45, s33, v233
	v_cvt_pk_fp8_f32 v46, v42, v43 op_sel:[0,0,1]
	v_med3_f32 v38, v38, s33, v233
	v_med3_f32 v39, v39, s33, v233
	v_mov_b32_e32 v42, 0
	v_cvt_pk_fp8_f32 v42, v38, v39
	v_pk_mul_f32 v[40:41], v[40:41], v[110:111] op_sel_hi:[1,0]
	v_pk_mul_f32 v[34:35], v[34:35], v[110:111] op_sel_hi:[1,0]
	v_pk_fma_f32 v[40:41], v[100:101], v[40:41], v[28:29]
	v_pk_fma_f32 v[34:35], v[106:107], v[34:35], v[30:31]
	v_med3_f32 v38, v40, s33, v233
	v_med3_f32 v39, v41, s33, v233
	v_cvt_pk_fp8_f32 v42, v38, v39 op_sel:[0,0,1]
	v_med3_f32 v34, v34, s33, v233
	v_med3_f32 v35, v35, s33, v233
	v_mov_b32_e32 v38, 0
	v_cvt_pk_fp8_f32 v38, v34, v35
	v_pk_mul_f32 v[36:37], v[36:37], v[110:111] op_sel_hi:[1,0]
	global_store_dword v[74:75], v127, off offset:-1792
	v_pk_fma_f32 v[36:37], v[104:105], v[36:37], v[32:33]
	global_store_dword v[74:75], v112, off offset:-1536
	v_med3_f32 v34, v36, s33, v233
	v_med3_f32 v35, v37, s33, v233
	v_cvt_pk_fp8_f32 v38, v34, v35 op_sel:[0,0,1]
	global_store_dword v[74:75], v58, off offset:-1280
	global_store_dword v[74:75], v54, off offset:-1024
	global_store_dword v[74:75], v50, off offset:-768
	global_store_dword v[74:75], v46, off offset:-512
	global_store_dword v[74:75], v42, off offset:-256
	global_store_dword v[74:75], v38, off
	v_lshl_add_u64 v[74:75], v[74:75], 0, s[22:23]
	s_cbranch_scc0 .LBB0_274
	s_branch .LBB0_271

.LBB0_450:
	s_bfe_i32 s5, s13, 0x10019
	s_lshl_b32 s4, s13, 6
	s_lshr_b32 s5, s5, 20
	s_add_i32 s5, s4, s5
	s_and_b32 s5, s5, 0xfffff000
	s_sub_i32 s10, s4, s5
	s_ashr_i32 s5, s4, 31
	s_mul_i32 s6, s13, 0xd0000
	s_mul_hi_i32 s7, s4, 0x3400
	s_add_u32 s24, s50, s6
	s_addc_u32 s25, s51, s7
	v_lshl_add_u64 v[4:5], v[2:3], 1, s[24:25]
	s_mov_b64 s[24:25], 0x21201800
	s_cmp_eq_u32 s10, 0
	v_lshl_add_u64 v[4:5], v[4:5], 0, s[24:25]
	s_cbranch_scc1 .LBB0_452
	v_add_co_u32_e32 v6, vcc, 0xffffd000, v4
	s_nop 1
	v_addc_co_u32_e32 v7, vcc, -1, v5, vcc
	global_load_dwordx4 v[6:9], v[6:7], off offset:-1024 nt
	s_waitcnt vmcnt(0)
	v_lshlrev_b32_e32 v99, 16, v6
	v_and_b32_e32 v98, 0xffff0000, v6
	v_lshlrev_b32_e32 v97, 16, v7
	v_and_b32_e32 v96, 0xffff0000, v7
	v_and_b32_e32 v89, 0xffff0000, v8
	v_lshlrev_b32_e32 v88, 16, v8
	v_and_b32_e32 v91, 0xffff0000, v9
	v_lshlrev_b32_e32 v90, 16, v9
	s_branch .LBB0_453

.LBB0_453:
	s_movk_i32 s13, 0x3000
	v_add_co_u32_e32 v10, vcc, s13, v4
	s_movk_i32 s13, 0x6000
	s_nop 0
	v_addc_co_u32_e32 v11, vcc, 0, v5, vcc
	v_add_co_u32_e32 v12, vcc, s13, v4
	s_mov_b32 s13, 0x9000
	s_nop 0
	v_addc_co_u32_e32 v13, vcc, 0, v5, vcc
	v_add_co_u32_e32 v14, vcc, s13, v4
	s_mov_b32 s13, 0xd000
	s_nop 0
	v_addc_co_u32_e32 v15, vcc, 0, v5, vcc
	global_load_dwordx4 v[6:9], v[4:5], off nt
	global_load_dwordx4 v[58:61], v[12:13], off offset:2048 nt
	global_load_dwordx4 v[54:57], v[14:15], off offset:3072 nt
	v_add_co_u32_e32 v12, vcc, s13, v4
	s_mov_b32 s13, 0x10000
	s_nop 0
	v_addc_co_u32_e32 v13, vcc, 0, v5, vcc
	v_add_co_u32_e32 v14, vcc, s13, v4
	s_mov_b32 s13, 0x16000
	s_nop 0
	v_addc_co_u32_e32 v15, vcc, 0, v5, vcc
	global_load_dwordx4 v[50:53], v[12:13], off nt
	global_load_dwordx4 v[46:49], v[14:15], off offset:1024 nt
	v_add_co_u32_e32 v12, vcc, s13, v4
	s_mov_b32 s13, 0x1a000
	s_nop 0
	v_addc_co_u32_e32 v13, vcc, 0, v5, vcc
	global_load_dwordx4 v[38:41], v[12:13], off offset:3072 nt
	v_add_co_u32_e32 v12, vcc, s13, v4
	s_mov_b32 s13, 0x13000
	s_nop 0
	v_addc_co_u32_e32 v13, vcc, 0, v5, vcc
	v_add_co_u32_e32 v4, vcc, s13, v4
	global_load_dwordx4 v[34:37], v[12:13], off nt
	s_nop 0
	v_addc_co_u32_e32 v5, vcc, 0, v5, vcc
	global_load_dwordx4 v[42:45], v[4:5], off offset:2048 nt
	global_load_dwordx4 v[62:65], v[10:11], off offset:1024 nt
	v_mov_b32_e32 v0, 0x300
	s_cmp_gt_i32 s11, 5
	v_lshl_add_u64 v[80:81], v[2:3], 1, s[6:7]
	v_mad_i64_i32 v[82:83], s[6:7], s4, v0, v[66:67]
	s_cselect_b64 s[56:57], -1, 0
	s_ashr_i32 s7, s11, 1
	s_and_b32 s11, s12, 0x200
	s_lshl_b32 s12, s7, 10
	s_ashr_i32 s13, s12, 31
	v_or_b32_e32 v0, s11, v100
	s_cmp_eq_u32 s7, 1
	v_lshlrev_b32_e32 v0, 1, v0
	s_cselect_b64 s[58:59], -1, 0
	s_lshl_b64 s[4:5], s[4:5], 13
	s_lshl_b64 s[12:13], s[12:13], 1
	v_or_b32_e32 v84, s4, v0
	s_add_u32 s4, s4, s12
	v_mov_b32_e32 v85, s5
	s_addc_u32 s5, s5, s13
	v_or_b32_e32 v86, s4, v0
	s_mov_b32 s6, 7
	v_mov_b32_e32 v87, s5
	s_waitcnt vmcnt(0)
	v_lshlrev_b32_e32 v115, 16, v6
	v_and_b32_e32 v114, 0xffff0000, v6
	v_lshlrev_b32_e32 v113, 16, v7
	v_and_b32_e32 v0, 0xffff0000, v7
	v_and_b32_e32 v95, 0xffff0000, v8
	v_lshlrev_b32_e32 v94, 16, v8
	v_and_b32_e32 v93, 0xffff0000, v9
	v_lshlrev_b32_e32 v92, 16, v9
	s_waitcnt vmcnt(7)
	v_mov_b64_e32 v[2:3], v[58:59]
	s_waitcnt vmcnt(6)
	v_mov_b64_e32 v[10:11], v[54:55]
	v_mov_b64_e32 v[4:5], v[60:61]
	s_waitcnt vmcnt(5)
	v_mov_b64_e32 v[14:15], v[50:51]
	s_waitcnt vmcnt(4)
	v_mov_b64_e32 v[18:19], v[46:47]
	v_mov_b64_e32 v[12:13], v[56:57]
	v_mov_b64_e32 v[20:21], v[48:49]
	v_mov_b64_e32 v[16:17], v[52:53]
	s_waitcnt vmcnt(3)
	v_mov_b64_e32 v[22:23], v[38:39]
	v_mov_b64_e32 v[24:25], v[40:41]
	s_waitcnt vmcnt(2)
	v_mov_b64_e32 v[26:27], v[34:35]
	v_mov_b64_e32 v[28:29], v[36:37]
	s_waitcnt vmcnt(1)
	v_mov_b64_e32 v[30:31], v[42:43]
	s_waitcnt vmcnt(0)
	v_mov_b64_e32 v[6:7], v[62:63]
	v_mov_b64_e32 v[32:33], v[44:45]
	v_mov_b64_e32 v[8:9], v[64:65]
	s_branch .LBB0_455

.LBB0_455:
	s_add_i32 s7, s6, -7
	s_cmp_gt_u32 s7, 55
	s_cbranch_scc1 .LBB0_457
	v_lshl_add_u64 v[22:23], s[50:51], 0, v[80:81]
	v_add_co_u32_e32 v2, vcc, 0x2121e000, v22
	s_nop 1
	v_addc_co_u32_e32 v3, vcc, 0, v23, vcc
	v_add_co_u32_e32 v4, vcc, 0x21222000, v22
	s_nop 1
	v_addc_co_u32_e32 v5, vcc, 0, v23, vcc
	v_add_co_u32_e32 v10, vcc, 0x21225000, v22
	global_load_dwordx4 v[6:9], v[2:3], off offset:3072 nt
	s_nop 0
	global_load_dwordx4 v[2:5], v[4:5], off nt
	v_addc_co_u32_e32 v11, vcc, 0, v23, vcc
	v_add_co_u32_e32 v14, vcc, 0x21228000, v22
	s_nop 1
	v_addc_co_u32_e32 v15, vcc, 0, v23, vcc
	v_add_co_u32_e32 v18, vcc, 0x2122b000, v22
	global_load_dwordx4 v[10:13], v[10:11], off offset:1024 nt
	s_nop 0
	global_load_dwordx4 v[14:17], v[14:15], off offset:2048 nt
	v_addc_co_u32_e32 v19, vcc, 0, v23, vcc
	v_add_co_u32_e32 v24, vcc, 0x2122f000, v22
	s_nop 1
	v_addc_co_u32_e32 v25, vcc, 0, v23, vcc
	global_load_dwordx4 v[18:21], v[18:19], off offset:3072 nt
	s_nop 0
	global_load_dwordx4 v[30:33], v[24:25], off nt
	v_add_co_u32_e32 v24, vcc, 0x21232000, v22
	s_nop 1
	v_addc_co_u32_e32 v25, vcc, 0, v23, vcc
	v_add_co_u32_e32 v26, vcc, 0x21235000, v22
	s_nop 1
	v_addc_co_u32_e32 v27, vcc, 0, v23, vcc
	global_load_dwordx4 v[22:25], v[24:25], off offset:1024 nt
	s_nop 0
	global_load_dwordx4 v[26:29], v[26:27], off offset:2048 nt

.LBB0_1141:
	s_waitcnt lgkmcnt(0)
	v_lshl_add_u64 v[50:51], s[40:41], 0, v[80:81]
	s_mov_b64 s[4:5], 0x40e00000
	v_lshl_add_u64 v[46:47], v[50:51], 0, s[4:5]
	v_add_co_u32_e32 v48, vcc, 0x40e00000, v50
	s_mov_b64 s[4:5], 0x42e00000
	s_nop 0
	v_addc_co_u32_e32 v49, vcc, 0, v51, vcc
	v_lshl_add_u64 v[52:53], v[50:51], 0, s[4:5]
	s_mov_b32 s4, 0x42e00000
	v_add_co_u32_e32 v50, vcc, s4, v50
	global_load_dwordx4 v[54:57], v[48:49], off nt
	s_nop 0
	global_load_dwordx4 v[46:49], v[46:47], off offset:16 nt
	v_addc_co_u32_e32 v51, vcc, 0, v51, vcc
	global_load_dwordx4 v[58:61], v[50:51], off nt
	s_nop 0
	global_load_dwordx4 v[50:53], v[52:53], off offset:16 nt
	v_lshl_add_u64 v[108:109], s[40:41], 0, v[76:77]
	s_mov_b64 s[4:5], 0x2e200000
	v_lshl_add_u64 v[156:157], s[40:41], 0, v[74:75]
	s_add_i32 s48, s48, s66
	v_lshl_add_u64 v[74:75], v[74:75], 0, s[6:7]
	v_lshl_add_u64 v[76:77], v[76:77], 0, s[10:11]
	v_lshl_add_u64 v[80:81], v[80:81], 0, s[22:23]
	s_cmpk_lt_i32 s48, 0x4000
	s_waitcnt vmcnt(3)
	v_lshlrev_b32_e32 v2, 16, v54
	v_and_b32_e32 v82, 0xffff0000, v54
	v_lshlrev_b32_e32 v86, 16, v55
	v_and_b32_e32 v127, 0xffff0000, v55
	v_lshl_add_u64 v[54:55], v[108:109], 0, s[4:5]
	s_mov_b32 s4, 0x2e200000
	s_waitcnt vmcnt(1)
	v_lshlrev_b32_e32 v4, 16, v58
	v_and_b32_e32 v72, 0xffff0000, v58
	v_add_co_u32_e32 v58, vcc, s4, v108
	v_lshlrev_b32_e32 v123, 16, v59
	v_and_b32_e32 v125, 0xffff0000, v59
	v_addc_co_u32_e32 v59, vcc, 0, v109, vcc
	s_mov_b32 s4, 0x2e201000
	v_add_co_u32_e32 v110, vcc, s4, v108
	s_mov_b64 s[4:5], 0x2e200800
	v_lshlrev_b32_e32 v131, 16, v60
	v_and_b32_e32 v133, 0xffff0000, v60
	v_lshlrev_b32_e32 v137, 16, v61
	v_and_b32_e32 v136, 0xffff0000, v61
	v_addc_co_u32_e32 v111, vcc, 0, v109, vcc
	v_lshl_add_u64 v[60:61], v[108:109], 0, s[4:5]
	s_mov_b64 s[4:5], 0x2e201000
	v_lshlrev_b32_e32 v135, 16, v57
	v_lshlrev_b32_e32 v129, 16, v56
	v_and_b32_e32 v134, 0xffff0000, v56
	v_and_b32_e32 v164, 0xffff0000, v57
	global_load_dwordx4 v[62:65], v[110:111], off offset:-4096 nt
	s_nop 0
	global_load_dwordx4 v[54:57], v[54:55], off offset:16 nt
	s_nop 0
	global_load_dwordx4 v[66:69], v[58:59], off offset:2048 nt
	s_nop 0
	global_load_dwordx4 v[58:61], v[60:61], off offset:16 nt
	v_lshl_add_u64 v[112:113], v[108:109], 0, s[4:5]
	global_load_dwordx4 v[108:111], v[110:111], off nt
	s_nop 0
	global_load_dwordx4 v[140:143], v[112:113], off offset:16 nt
	s_mov_b64 s[4:5], 0x36e01000
	v_lshl_add_u64 v[144:145], v[156:157], 0, s[4:5]
	s_mov_b32 s4, 0x36e01000
	v_add_co_u32_e32 v148, vcc, s4, v156
	s_mov_b32 s4, 0x36e02000
	s_nop 0
	v_addc_co_u32_e32 v149, vcc, 0, v157, vcc
	v_add_co_u32_e32 v158, vcc, s4, v156
	s_mov_b64 s[4:5], 0x36e01800
	s_nop 0
	v_addc_co_u32_e32 v159, vcc, 0, v157, vcc
	v_lshl_add_u64 v[152:153], v[156:157], 0, s[4:5]
	s_mov_b64 s[4:5], 0x36e02000
	v_lshl_add_u64 v[160:161], v[156:157], 0, s[4:5]
	v_add_f32_e32 v82, v72, v82
	v_add_f32_e32 v4, v4, v2
	v_add_f32_e32 v2, 0, v4
	v_add_f32_e32 v2, v82, v2
	v_add_f32_e32 v86, v123, v86
	v_add_f32_e32 v2, v86, v2
	v_add_f32_e32 v123, v125, v127
	v_add_f32_e32 v2, v123, v2
	v_add_f32_e32 v125, v131, v129
	v_add_f32_e32 v2, v125, v2
	s_waitcnt vmcnt(5)
	v_lshlrev_b32_e32 v165, 16, v62
	v_and_b32_e32 v166, 0xffff0000, v62
	s_waitcnt vmcnt(3)
	v_lshlrev_b32_e32 v169, 16, v66
	v_and_b32_e32 v170, 0xffff0000, v66
	s_waitcnt vmcnt(1)
	v_lshlrev_b32_e32 v132, 16, v108
	v_and_b32_e32 v130, 0xffff0000, v108
	v_lshlrev_b32_e32 v124, 16, v110
	v_and_b32_e32 v122, 0xffff0000, v110
	s_waitcnt vmcnt(0)
	v_lshlrev_b32_e32 v118, 16, v140
	v_and_b32_e32 v116, 0xffff0000, v140
	v_lshlrev_b32_e32 v114, 16, v141
	v_and_b32_e32 v112, 0xffff0000, v141
	v_lshlrev_b32_e32 v110, 16, v142
	v_and_b32_e32 v108, 0xffff0000, v142
	v_lshlrev_b32_e32 v66, 16, v143
	v_and_b32_e32 v62, 0xffff0000, v143
	global_load_dwordx4 v[140:143], v[158:159], off offset:-4096 nt
	s_nop 0
	global_load_dwordx4 v[144:147], v[144:145], off offset:16 nt
	s_nop 0
	global_load_dwordx4 v[148:151], v[148:149], off offset:2048 nt
	s_nop 0
	global_load_dwordx4 v[152:155], v[152:153], off offset:16 nt
	s_nop 0
	global_load_dwordx4 v[156:159], v[158:159], off nt
	s_nop 0
	global_load_dwordx4 v[160:163], v[160:161], off offset:16 nt
	v_lshlrev_b32_e32 v128, 16, v109
	v_and_b32_e32 v126, 0xffff0000, v109
	v_lshlrev_b32_e32 v84, 16, v111
	v_and_b32_e32 v120, 0xffff0000, v111
	v_lshlrev_b32_e32 v171, 16, v67
	v_lshlrev_b32_e32 v167, 16, v63
	v_and_b32_e32 v168, 0xffff0000, v57
	v_and_b32_e32 v172, 0xffff0000, v61
	s_waitcnt vmcnt(5)
	v_lshlrev_b32_e32 v173, 16, v140
	s_waitcnt vmcnt(3)
	v_lshlrev_b32_e32 v175, 16, v148
	v_and_b32_e32 v140, 0xffff0000, v140
	v_and_b32_e32 v148, 0xffff0000, v148
	s_waitcnt vmcnt(1)
	v_lshlrev_b32_e32 v179, 16, v156
	v_and_b32_e32 v180, 0xffff0000, v156
	v_add_f32_e32 v156, v173, v175
	v_add_f32_e32 v156, -2.0, v156
	v_add_f32_e32 v72, v140, v148
	v_fma_f32 v156, v14, v156, 2.0
	v_add_f32_e32 v72, -2.0, v72
	v_mul_f32_e32 v156, v156, v169
	v_fma_f32 v72, v15, v72, 2.0
	v_lshlrev_b32_e32 v174, 16, v141
	s_waitcnt vmcnt(0)
	v_lshlrev_b32_e32 v115, 16, v160
	v_and_b32_e32 v113, 0xffff0000, v160
	v_lshlrev_b32_e32 v111, 16, v161
	v_and_b32_e32 v109, 0xffff0000, v161
	v_mul_f32_e32 v156, v156, v165
	v_mul_f32_e32 v72, v72, v170
	v_lshlrev_b32_e32 v161, 16, v142
	v_and_b32_e32 v160, 0xffff0000, v141
	v_lshlrev_b32_e32 v141, 16, v150
	v_and_b32_e32 v140, 0xffff0000, v149
	v_lshlrev_b32_e32 v176, 16, v149
	v_lshlrev_b32_e32 v20, 16, v162
	v_and_b32_e32 v17, 0xffff0000, v162
	v_fma_f32 v162, v6, v156, 0
	v_mul_f32_e32 v72, v72, v166
	v_pk_add_f32 v[140:141], v[160:161], v[140:141]
	v_fmac_f32_e32 v162, v7, v72
	v_add_f32_e32 v72, v174, v176
	v_pk_add_f32 v[140:141], v[140:141], -2.0 op_sel_hi:[1,0]
	v_lshlrev_b32_e32 v70, 16, v158
	v_and_b32_e32 v121, 0xffff0000, v158
	v_lshlrev_b32_e32 v119, 16, v159
	v_and_b32_e32 v117, 0xffff0000, v159
	v_add_f32_e32 v72, -2.0, v72
	v_lshlrev_b32_e32 v159, 16, v68
	v_and_b32_e32 v158, 0xffff0000, v67
	v_pk_fma_f32 v[140:141], v[98:99], v[140:141], 2.0 op_sel_hi:[1,1,0]
	v_lshlrev_b32_e32 v181, 16, v157
	v_and_b32_e32 v182, 0xffff0000, v157
	v_fma_f32 v72, v16, v72, 2.0
	v_lshlrev_b32_e32 v157, 16, v64
	v_and_b32_e32 v156, 0xffff0000, v63
	v_pk_mul_f32 v[140:141], v[140:141], v[158:159]
	v_mul_f32_e32 v72, v72, v171
	v_pk_mul_f32 v[140:141], v[140:141], v[156:157]
	v_lshlrev_b32_e32 v157, 16, v143
	v_and_b32_e32 v156, 0xffff0000, v142
	v_lshlrev_b32_e32 v159, 16, v151
	v_and_b32_e32 v158, 0xffff0000, v150
	v_mul_f32_e32 v72, v72, v167
	v_pk_add_f32 v[156:157], v[156:157], v[158:159]
	v_fmac_f32_e32 v162, v8, v72
	v_pk_mul_f32 v[140:141], v[88:89], v[140:141]
	v_pk_add_f32 v[156:157], v[156:157], -2.0 op_sel_hi:[1,0]
	v_add_f32_e32 v63, v140, v162
	v_lshlrev_b32_e32 v149, 16, v69
	v_and_b32_e32 v148, 0xffff0000, v68
	v_pk_fma_f32 v[156:157], v[100:101], v[156:157], 2.0 op_sel_hi:[1,1,0]
	v_add_f32_e32 v63, v141, v63
	v_lshlrev_b32_e32 v141, 16, v65
	v_and_b32_e32 v140, 0xffff0000, v64
	v_pk_mul_f32 v[148:149], v[156:157], v[148:149]
	v_and_b32_e32 v64, 0xffff0000, v69
	v_lshlrev_b32_e32 v69, 16, v144
	v_and_b32_e32 v68, 0xffff0000, v143
	v_lshlrev_b32_e32 v143, 16, v152
	v_and_b32_e32 v142, 0xffff0000, v151
	v_pk_mul_f32 v[140:141], v[148:149], v[140:141]
	v_pk_add_f32 v[68:69], v[68:69], v[142:143]
	v_pk_mul_f32 v[140:141], v[90:91], v[140:141]
	v_pk_add_f32 v[68:69], v[68:69], -2.0 op_sel_hi:[1,0]
	v_add_f32_e32 v63, v140, v63
	v_and_b32_e32 v140, 0xffff0000, v65
	v_lshlrev_b32_e32 v65, 16, v58
	v_pk_fma_f32 v[68:69], v[102:103], v[68:69], 2.0 op_sel_hi:[1,1,0]
	v_add_f32_e32 v63, v141, v63
	v_lshlrev_b32_e32 v141, 16, v54
	v_pk_mul_f32 v[64:65], v[68:69], v[64:65]
	v_lshlrev_b32_e32 v143, 16, v145
	v_pk_mul_f32 v[64:65], v[64:65], v[140:141]
	v_and_b32_e32 v142, 0xffff0000, v144
	v_lshlrev_b32_e32 v149, 16, v153
	v_and_b32_e32 v148, 0xffff0000, v152
	v_pk_mul_f32 v[64:65], v[92:93], v[64:65]
	v_pk_add_f32 v[142:143], v[142:143], v[148:149]
	v_add_f32_e32 v63, v64, v63
	v_pk_add_f32 v[142:143], v[142:143], -2.0 op_sel_hi:[1,0]
	v_add_f32_e32 v63, v65, v63
	v_and_b32_e32 v64, 0xffff0000, v46
	v_lshlrev_b32_e32 v65, 16, v46
	v_and_b32_e32 v68, 0xffff0000, v50
	v_lshlrev_b32_e32 v69, 16, v50
	v_lshlrev_b32_e32 v141, 16, v59
	v_and_b32_e32 v140, 0xffff0000, v58
	v_pk_fma_f32 v[142:143], v[104:105], v[142:143], 2.0 op_sel_hi:[1,1,0]
	v_pk_add_f32 v[64:65], v[64:65], v[68:69]
	v_lshlrev_b32_e32 v69, 16, v55
	v_and_b32_e32 v68, 0xffff0000, v54
	v_pk_mul_f32 v[140:141], v[142:143], v[140:141]
	v_and_b32_e32 v54, 0xffff0000, v59
	v_pk_mul_f32 v[68:69], v[140:141], v[68:69]
	v_lshlrev_b32_e32 v59, 16, v146
	v_pk_mul_f32 v[68:69], v[94:95], v[68:69]
	v_and_b32_e32 v58, 0xffff0000, v145
	v_add_f32_e32 v46, v68, v63
	v_add_f32_e32 v63, v69, v46
	v_lshlrev_b32_e32 v69, 16, v154
	v_and_b32_e32 v68, 0xffff0000, v153
	v_pk_add_f32 v[58:59], v[58:59], v[68:69]
	v_and_b32_e32 v46, 0xffff0000, v47
	v_lshlrev_b32_e32 v47, 16, v47
	v_and_b32_e32 v50, 0xffff0000, v51
	v_lshlrev_b32_e32 v51, 16, v51
	v_pk_add_f32 v[58:59], v[58:59], -2.0 op_sel_hi:[1,0]
	v_pk_add_f32 v[50:51], v[46:47], v[50:51]
	v_and_b32_e32 v46, 0xffff0000, v55
	v_lshlrev_b32_e32 v55, 16, v60
	v_pk_fma_f32 v[58:59], v[106:107], v[58:59], 2.0 op_sel_hi:[1,1,0]
	v_lshlrev_b32_e32 v47, 16, v56
	v_pk_mul_f32 v[54:55], v[58:59], v[54:55]
	v_and_b32_e32 v177, 0xffff0000, v155
	v_pk_mul_f32 v[46:47], v[54:55], v[46:47]
	v_and_b32_e32 v54, 0xffff0000, v52
	v_pk_mul_f32 v[46:47], v[96:97], v[46:47]
	v_lshlrev_b32_e32 v55, 16, v52
	v_add_f32_e32 v46, v46, v63
	v_add_f32_e32 v63, v47, v46
	v_and_b32_e32 v46, 0xffff0000, v48
	v_lshlrev_b32_e32 v47, 16, v48
	v_pk_add_f32 v[58:59], v[46:47], v[54:55]
	v_lshlrev_b32_e32 v47, 16, v57
	v_and_b32_e32 v46, 0xffff0000, v56
	v_lshlrev_b32_e32 v55, 16, v61
	v_and_b32_e32 v54, 0xffff0000, v60
	v_lshlrev_b32_e32 v57, 16, v147
	v_and_b32_e32 v56, 0xffff0000, v146
	v_lshlrev_b32_e32 v61, 16, v155
	v_and_b32_e32 v60, 0xffff0000, v154
	v_pk_add_f32 v[56:57], v[56:57], v[60:61]
	v_and_b32_e32 v178, 0xffff0000, v147
	v_pk_add_f32 v[56:57], v[56:57], -2.0 op_sel_hi:[1,0]
	v_add_f32_e32 v150, v136, v164
	v_pk_fma_f32 v[56:57], v[18:19], v[56:57], 2.0 op_sel_hi:[1,1,0]
	v_and_b32_e32 v48, 0xffff0000, v53
	v_pk_mul_f32 v[54:55], v[56:57], v[54:55]
	v_add_f32_e32 v67, v133, v134
	v_pk_mul_f32 v[46:47], v[54:55], v[46:47]
	v_add_f32_e32 v2, v67, v2
	v_pk_mul_f32 v[46:47], v[10:11], v[46:47]
	v_lshlrev_b32_e32 v12, 16, v163
	v_add_f32_e32 v46, v46, v63
	v_add_f32_e32 v136, v47, v46
	v_and_b32_e32 v46, 0xffff0000, v49
	v_lshlrev_b32_e32 v47, 16, v49
	v_lshlrev_b32_e32 v49, 16, v53
	v_pk_add_f32 v[48:49], v[46:47], v[48:49]
	v_add_f32_e32 v46, v177, v178
	v_add_f32_e32 v46, -2.0, v46
	v_fma_f32 v46, v21, v46, 2.0
	v_mul_f32_e32 v46, v46, v172
	v_mul_f32_e32 v46, v46, v168
	v_mul_f32_e32 v134, v13, v46
	v_pk_add_f32 v[46:47], v[134:135], v[136:137]
	v_and_b32_e32 v9, 0xffff0000, v163
	v_add_f32_e32 v2, v47, v2
	v_add_f32_e32 v2, v150, v2
	v_add_f32_e32 v2, v65, v2
	v_add_f32_e32 v2, v64, v2
	v_add_f32_e32 v2, v51, v2
	v_add_f32_e32 v2, v50, v2
	v_add_f32_e32 v2, v59, v2
	v_add_f32_e32 v2, v58, v2
	v_add_f32_e32 v2, v49, v2
	v_add_f32_e32 v2, v48, v2
	ds_bpermute_b32 v52, v138, v2
	s_waitcnt lgkmcnt(0)
	v_add_f32_e32 v2, v2, v52
	ds_bpermute_b32 v52, v139, v2
	s_waitcnt lgkmcnt(0)
	v_add_f32_e32 v2, v2, v52
	ds_bpermute_b32 v52, v138, v46
	v_mul_f32_e32 v53, 0x3c800000, v2
	v_fmac_f32_e32 v82, 0xbc800000, v2
	v_fmac_f32_e32 v4, 0xbc800000, v2
	v_fmac_f32_e32 v86, 0xbc800000, v2
	s_waitcnt lgkmcnt(0)
	v_pk_add_f32 v[54:55], v[46:47], v[52:53]
	v_pk_add_f32 v[56:57], v[46:47], v[52:53] neg_lo:[0,1] neg_hi:[0,1]
	v_mul_f32_e32 v47, v82, v82
	v_fmac_f32_e32 v47, v4, v4
	v_fmac_f32_e32 v47, v86, v86
	v_fmac_f32_e32 v123, 0xbc800000, v2
	v_fmac_f32_e32 v47, v123, v123
	v_fmac_f32_e32 v125, 0xbc800000, v2
	v_fmac_f32_e32 v47, v125, v125
	v_fmac_f32_e32 v67, 0xbc800000, v2
	v_fmac_f32_e32 v47, v67, v67
	v_fmac_f32_e32 v47, v57, v57
	v_fmac_f32_e32 v150, 0xbc800000, v2
	v_fmac_f32_e32 v47, v150, v150
	v_fmamk_f32 v60, v2, 0xbc800000, v65
	v_fmac_f32_e32 v64, 0xbc800000, v2
	v_mov_b32_e32 v2, v53
	v_fmac_f32_e32 v47, v60, v60
	v_pk_add_f32 v[52:53], v[50:51], v[2:3] op_sel_hi:[1,0] neg_lo:[0,1] neg_hi:[0,1]
	v_fmac_f32_e32 v47, v64, v64
	v_pk_mul_f32 v[50:51], v[52:53], v[52:53]
	v_pk_add_f32 v[48:49], v[48:49], v[2:3] op_sel_hi:[1,0] neg_lo:[0,1] neg_hi:[0,1]
	v_add_f32_e32 v47, v51, v47
	v_add_f32_e32 v47, v50, v47
	v_pk_add_f32 v[50:51], v[58:59], v[2:3] op_sel_hi:[1,0] neg_lo:[0,1] neg_hi:[0,1]
	ds_bpermute_b32 v46, v139, v54
	v_pk_mul_f32 v[58:59], v[50:51], v[50:51]
	s_nop 0
	v_add_f32_e32 v47, v59, v47
	v_add_f32_e32 v47, v58, v47
	v_pk_mul_f32 v[58:59], v[48:49], v[48:49]
	s_nop 0
	v_add_f32_e32 v2, v59, v47
	v_add_f32_e32 v2, v58, v2
	ds_bpermute_b32 v47, v138, v2
	s_waitcnt lgkmcnt(0)
	v_add_f32_e32 v2, v2, v47
	ds_bpermute_b32 v47, v139, v2
	s_waitcnt lgkmcnt(0)
	v_add_f32_e32 v2, v2, v47
	v_mov_b32_e32 v47, 0x3a27c5ac
	v_fmamk_f32 v2, v2, 0x3c800000, v47
	v_cmp_gt_f32_e32 vcc, s82, v2
	v_mul_f32_e32 v47, 0x4f800000, v2
	s_nop 0
	v_cndmask_b32_e32 v2, v2, v47, vcc
	v_sqrt_f32_e32 v47, v2
	s_nop 0
	v_add_u32_e32 v58, -1, v47
	v_fma_f32 v59, -v58, v47, v2
	v_cmp_ge_f32_e64 s[38:39], 0, v59
	v_add_u32_e32 v59, 1, v47
	s_nop 0
	v_cndmask_b32_e64 v58, v47, v58, s[38:39]
	v_fma_f32 v47, -v59, v47, v2
	v_cmp_lt_f32_e64 s[38:39], 0, v47
	s_nop 1
	v_cndmask_b32_e64 v47, v58, v59, s[38:39]
	v_mul_f32_e32 v58, 0x37800000, v47
	v_cndmask_b32_e32 v47, v47, v58, vcc
	v_cmp_class_f32_e32 vcc, v2, v229
	s_nop 1
	v_cndmask_b32_e32 v2, v47, v2, vcc
	v_div_scale_f32 v47, s[4:5], v2, v2, 1.0
	v_rcp_f32_e32 v58, v47
	s_nop 0
	v_fma_f32 v59, -v47, v58, 1.0
	v_fmac_f32_e32 v58, v59, v58
	v_div_scale_f32 v59, vcc, 1.0, v2, 1.0
	v_mul_f32_e32 v61, v59, v58
	v_fma_f32 v63, -v47, v61, v59
	v_fmac_f32_e32 v61, v63, v58
	v_fma_f32 v47, -v47, v61, v59
	v_div_fmas_f32 v47, v47, v58, v61
	v_div_fixup_f32 v47, v47, v2, 1.0
	v_pk_add_f32 v[54:55], v[54:55], v[46:47]
	v_mul_f32_e32 v133, v4, v47
	v_pk_mul_f32 v[56:57], v[56:57], v[46:47]
	v_mov_b32_e32 v72, v54
	v_mov_b32_e32 v55, v57
	v_pk_mul_f32 v[56:57], v[72:73], v[132:133]
	v_mul_f32_e32 v131, v82, v47
	v_add_f32_e32 v2, v22, v57
	v_add_f32_e32 v2, v56, v2
	v_mul_f32_e32 v58, v2, v179
	v_mov_b32_e32 v2, v54
	v_pk_mul_f32 v[56:57], v[2:3], v[130:131]
	v_mul_f32_e32 v129, v86, v47
	v_add_f32_e32 v2, v23, v57
	v_mov_b32_e32 v82, v54
	v_add_f32_e32 v2, v56, v2
	v_pk_mul_f32 v[56:57], v[82:83], v[128:129]
	v_mul_f32_e32 v127, v123, v47
	v_add_f32_e32 v4, v24, v57
	v_add_f32_e32 v4, v56, v4
	v_mul_f32_e32 v59, v4, v181
	v_mov_b32_e32 v4, v54
	v_pk_mul_f32 v[56:57], v[4:5], v[126:127]
	v_mul_f32_e32 v125, v125, v47
	v_add_f32_e32 v4, v25, v57
	v_mov_b32_e32 v86, v54
	v_add_f32_e32 v4, v56, v4
	v_pk_mul_f32 v[56:57], v[86:87], v[124:125]
	v_mul_f32_e32 v123, v67, v47
	v_add_f32_e32 v46, v26, v57
	v_add_f32_e32 v46, v56, v46
	v_mul_f32_e32 v61, v46, v70
	v_mov_b32_e32 v70, v54
	v_pk_mul_f32 v[56:57], v[70:71], v[122:123]
	v_mul_f32_e32 v2, v2, v180
	v_add_f32_e32 v46, v27, v57
	v_add_f32_e32 v46, v56, v46
	v_pk_mul_f32 v[56:57], v[54:55], v[84:85]
	v_mul_f32_e32 v65, v46, v121
	v_add_f32_e32 v46, v28, v57
	v_mul_f32_e32 v121, v150, v47
	v_mov_b32_e32 v55, v38
	v_add_f32_e32 v46, v56, v46
	v_pk_mul_f32 v[56:57], v[54:55], v[120:121]
	v_mul_f32_e32 v68, v46, v119
	v_add_f32_e32 v46, v29, v57
	v_mul_f32_e32 v119, v60, v47
	v_mov_b32_e32 v55, v39
	v_add_f32_e32 v46, v56, v46
	v_pk_mul_f32 v[56:57], v[54:55], v[118:119]
	v_mul_f32_e32 v69, v46, v117
	v_add_f32_e32 v46, v30, v57
	v_mul_f32_e32 v117, v64, v47
	v_mov_b32_e32 v55, v40
	v_add_f32_e32 v46, v56, v46
	v_pk_mul_f32 v[56:57], v[54:55], v[116:117]
	v_mul_f32_e32 v60, v46, v115
	v_add_f32_e32 v46, v31, v57
	v_mul_f32_e32 v115, v53, v47
	v_mov_b32_e32 v55, v41
	v_add_f32_e32 v46, v56, v46
	v_pk_mul_f32 v[56:57], v[54:55], v[114:115]
	v_mul_f32_e32 v64, v46, v113
	v_add_f32_e32 v46, v32, v57
	v_mul_f32_e32 v113, v52, v47
	v_mov_b32_e32 v55, v42
	v_add_f32_e32 v46, v56, v46
	v_pk_mul_f32 v[52:53], v[54:55], v[112:113]
	v_mul_f32_e32 v70, v46, v111
	v_add_f32_e32 v46, v33, v53
	v_mul_f32_e32 v111, v51, v47
	v_mov_b32_e32 v55, v43
	v_add_f32_e32 v46, v52, v46
	v_pk_mul_f32 v[52:53], v[54:55], v[110:111]
	v_mul_f32_e32 v72, v46, v109
	v_add_f32_e32 v46, v34, v53
	v_mul_f32_e32 v109, v50, v47
	v_mov_b32_e32 v55, v44
	v_add_f32_e32 v46, v52, v46
	v_pk_mul_f32 v[50:51], v[54:55], v[108:109]
	v_mul_f32_e32 v20, v46, v20
	v_add_f32_e32 v46, v35, v51
	v_mul_f32_e32 v67, v49, v47
	v_mov_b32_e32 v55, v45
	v_add_f32_e32 v46, v50, v46
	v_pk_mul_f32 v[50:51], v[54:55], v[66:67]
	v_mul_f32_e32 v56, 0x41000000, v58
	v_mul_f32_e32 v57, 0x41000000, v2
	v_mul_f32_e32 v82, v46, v17
	v_add_f32_e32 v17, v36, v51
	v_mul_f32_e32 v63, v48, v47
	v_mov_b32_e32 v55, v0
	v_mul_f32_e32 v48, 0x41000000, v60
	v_mul_f32_e32 v49, 0x41000000, v64
	v_med3_f32 v58, v56, s33, v233
	v_med3_f32 v57, v57, s33, v233
	v_mov_b32_e32 v56, v1
	v_add_f32_e32 v17, v50, v17
	v_pk_mul_f32 v[46:47], v[54:55], v[62:63]
	v_cvt_pk_fp8_f32 v56, v58, v57
	v_med3_f32 v48, v48, s33, v233
	v_med3_f32 v49, v49, s33, v233
	v_mov_b32_e32 v58, v1
	v_mul_f32_e32 v51, v17, v12
	v_add_f32_e32 v12, v37, v47
	v_cvt_pk_fp8_f32 v58, v48, v49
	v_mul_f32_e32 v4, v4, v182
	v_add_f32_e32 v12, v46, v12
	v_mul_f32_e32 v46, v12, v9
	v_mul_f32_e32 v52, 0x41000000, v59
	v_mul_f32_e32 v9, 0x41000000, v70
	v_mul_f32_e32 v53, 0x41000000, v4
	v_mul_f32_e32 v12, 0x41000000, v72
	v_mul_f32_e32 v54, 0x41000000, v61
	v_mul_f32_e32 v17, 0x41000000, v20
	v_mul_f32_e32 v55, 0x41000000, v65
	v_mul_f32_e32 v20, 0x41000000, v82
	v_med3_f32 v52, v52, s33, v233
	v_med3_f32 v53, v53, s33, v233
	v_med3_f32 v9, v9, s33, v233
	v_med3_f32 v12, v12, s33, v233
	v_cvt_pk_fp8_f32 v56, v52, v53 op_sel:[0,0,1]
	v_med3_f32 v52, v54, s33, v233
	v_med3_f32 v53, v55, s33, v233
	v_mov_b32_e32 v57, v1
	v_cvt_pk_fp8_f32 v58, v9, v12 op_sel:[0,0,1]
	v_med3_f32 v9, v17, s33, v233
	v_med3_f32 v12, v20, s33, v233
	v_mov_b32_e32 v59, v1
	v_cvt_pk_fp8_f32 v57, v52, v53
	v_cvt_pk_fp8_f32 v59, v9, v12
	v_mul_f32_e32 v50, 0x41000000, v68
	v_mul_f32_e32 v2, 0x41000000, v51
	v_mul_f32_e32 v51, 0x41000000, v69
	v_mul_f32_e32 v4, 0x41000000, v46
	v_med3_f32 v50, v50, s33, v233
	v_med3_f32 v51, v51, s33, v233
	v_med3_f32 v2, v2, s33, v233
	v_med3_f32 v4, v4, s33, v233
	v_cvt_pk_fp8_f32 v57, v50, v51 op_sel:[0,0,1]
	v_cvt_pk_fp8_f32 v59, v2, v4 op_sel:[0,0,1]
	v_lshl_add_u64 v[46:47], s[40:41], 0, v[78:79]
	v_add_co_u32_e32 v46, vcc, 0x1d200000, v46
	v_lshl_add_u64 v[78:79], v[78:79], 0, s[22:23]
	s_nop 0
	v_addc_co_u32_e32 v47, vcc, 0, v47, vcc
	global_store_dwordx4 v[46:47], v[56:59], off offset:1024 sc1
	s_cbranch_scc1 .LBB0_1141
